# speedup vs baseline: 1.0440x; 1.0017x over previous
.LBB6_4:
	s_or_b64 exec, exec, s[26:27]
	s_lshl_b32 s3, s30, 1
	s_and_b32 s26, s3, 0xffffffe
	s_mov_b32 s27, 0
	v_mov_b32_e32 v67, 0
	s_waitcnt lgkmcnt(0)
	v_lshl_add_u64 v[2:3], s[4:5], 0, v[66:67]
	s_lshl_b64 s[4:5], s[26:27], 13
	s_or_b32 s26, s26, 1
	v_lshl_add_u64 v[4:5], v[2:3], 0, s[4:5]
	s_lshl_b64 s[4:5], s[26:27], 13
	v_lshl_add_u64 v[2:3], v[2:3], 0, s[4:5]
	global_load_dwordx4 v[70:73], v[4:5], off
	global_load_dwordx4 v[74:77], v[2:3], off
	v_lshl_add_u64 v[2:3], s[20:21], 0, v[66:67]
	s_movk_i32 s3, 0x2000
	v_add_co_u32_e64 v4, s[4:5], s3, v2
	global_load_dwordx4 v[14:17], v66, s[20:21]
	s_nop 0
	v_addc_co_u32_e64 v5, s[4:5], 0, v3, s[4:5]
	s_movk_i32 s20, 0x4000
	v_add_co_u32_e64 v18, s[4:5], s20, v2
	s_movk_i32 s3, 0x6000
	s_nop 0
	v_addc_co_u32_e64 v19, s[4:5], 0, v3, s[4:5]
	global_load_dwordx4 v[10:13], v[4:5], off
	global_load_dwordx4 v[6:9], v[18:19], off
	v_add_co_u32_e64 v18, s[4:5], s3, v2
	s_lshl_b32 s26, s30, 2
	s_nop 0
	v_addc_co_u32_e64 v19, s[4:5], 0, v3, s[4:5]
	s_add_u32 s4, s8, 0x800000
	s_addc_u32 s5, s9, 0
	s_lshl_b64 s[8:9], s[26:27], 13
	v_lshlrev_b32_e32 v1, 2, v0
	global_load_dwordx4 v[2:5], v[18:19], off
	global_load_dword v69, v1, s[22:23]
	v_or_b32_e32 v18, s8, v66
	v_mov_b32_e32 v19, s9
	s_or_b32 s8, s26, 1
	s_mov_b32 s9, s27
	s_lshl_b64 s[8:9], s[8:9], 13
	v_lshl_add_u64 v[78:79], s[18:19], 0, v[18:19]
	v_lshl_add_u64 v[80:81], s[16:17], 0, v[18:19]
	v_lshl_add_u64 v[82:83], s[4:5], 0, v[18:19]
	v_or_b32_e32 v18, s8, v66
	v_mov_b32_e32 v19, s9
	s_or_b32 s8, s26, 2
	s_mov_b32 s9, s27
	s_lshl_b64 s[8:9], s[8:9], 13
	s_or_b32 s26, s26, 3
	v_lshl_add_u64 v[84:85], s[18:19], 0, v[18:19]
	v_lshl_add_u64 v[86:87], s[16:17], 0, v[18:19]
	v_lshl_add_u64 v[88:89], s[4:5], 0, v[18:19]
	v_or_b32_e32 v18, s8, v66
	v_mov_b32_e32 v19, s9
	s_lshl_b64 s[8:9], s[26:27], 13
	v_lshl_add_u64 v[90:91], s[18:19], 0, v[18:19]
	v_lshl_add_u64 v[92:93], s[16:17], 0, v[18:19]
	v_lshl_add_u64 v[94:95], s[4:5], 0, v[18:19]
	v_or_b32_e32 v18, s8, v66
	v_mov_b32_e32 v19, s9
	v_lshl_add_u64 v[96:97], s[18:19], 0, v[18:19]
	v_lshl_add_u64 v[98:99], s[16:17], 0, v[18:19]
	v_lshl_add_u64 v[100:101], s[4:5], 0, v[18:19]
	global_load_dwordx4 v[62:65], v[78:79], off
	global_load_dwordx4 v[54:57], v[80:81], off
	global_load_dwordx4 v[58:61], v[82:83], off
	v_mov_b64_e32 v[178:179], v[84:85]
	v_mov_b64_e32 v[180:181], v[86:87]
	v_mov_b64_e32 v[182:183], v[88:89]
	v_mov_b64_e32 v[184:185], v[90:91]
	v_mov_b64_e32 v[186:187], v[92:93]
	v_mov_b64_e32 v[188:189], v[94:95]
	v_mov_b64_e32 v[190:191], v[96:97]
	v_mov_b64_e32 v[192:193], v[98:99]
	v_mov_b64_e32 v[194:195], v[100:101]
	s_barrier
	s_waitcnt vmcnt(9)
	v_cvt_f32_f16_e32 v136, v70
	v_cvt_f32_f16_sdwa v137, v70 dst_sel:DWORD dst_unused:UNUSED_PAD src0_sel:WORD_1
	v_cvt_f32_f16_e32 v138, v71
	v_cvt_f32_f16_sdwa v139, v71 dst_sel:DWORD dst_unused:UNUSED_PAD src0_sel:WORD_1
	v_cvt_f32_f16_e32 v140, v72
	v_cvt_f32_f16_sdwa v141, v72 dst_sel:DWORD dst_unused:UNUSED_PAD src0_sel:WORD_1
	v_cvt_f32_f16_e32 v142, v73
	v_cvt_f32_f16_sdwa v143, v73 dst_sel:DWORD dst_unused:UNUSED_PAD src0_sel:WORD_1
	s_waitcnt vmcnt(8)
	v_cvt_f32_f16_e32 v144, v74
	v_cvt_f32_f16_sdwa v145, v74 dst_sel:DWORD dst_unused:UNUSED_PAD src0_sel:WORD_1
	v_cvt_f32_f16_e32 v146, v75
	v_cvt_f32_f16_sdwa v147, v75 dst_sel:DWORD dst_unused:UNUSED_PAD src0_sel:WORD_1
	v_cvt_f32_f16_e32 v148, v76
	v_cvt_f32_f16_sdwa v149, v76 dst_sel:DWORD dst_unused:UNUSED_PAD src0_sel:WORD_1
	v_cvt_f32_f16_e32 v150, v77
	v_cvt_f32_f16_sdwa v151, v77 dst_sel:DWORD dst_unused:UNUSED_PAD src0_sel:WORD_1
	ds_read_b128 v[72:75], v67
	ds_read_b128 v[76:79], v67 offset:16
	ds_read_b128 v[80:83], v67 offset:32
	ds_read_b128 v[84:87], v67 offset:48
	ds_read_b128 v[88:91], v67 offset:64
	ds_read_b128 v[92:95], v67 offset:80
	ds_read_b128 v[96:99], v67 offset:96
	ds_read_b128 v[100:103], v67 offset:112
	ds_read_b128 v[104:107], v67 offset:128
	ds_read_b128 v[108:111], v67 offset:144
	ds_read_b128 v[112:115], v67 offset:160
	ds_read_b128 v[116:119], v67 offset:176
	ds_read_b128 v[120:123], v67 offset:192
	ds_read_b128 v[124:127], v67 offset:208
	ds_read_b128 v[128:131], v67 offset:224
	ds_read_b128 v[132:135], v67 offset:240
	v_lshlrev_b32_e32 v70, 1, v0
	s_waitcnt vmcnt(2)
	v_cvt_f32_f16_e32 v152, v62
	s_waitcnt vmcnt(1)
	v_cvt_f32_f16_e32 v71, v54
	v_pk_mul_f32 v[156:157], v[152:153], v[14:15] op_sel_hi:[0,1]
	v_exp_f32_e32 v156, v156
	v_exp_f32_e32 v157, v157
	v_pk_mul_f32 v[158:159], v[152:153], v[16:17] op_sel_hi:[0,1]
	v_exp_f32_e32 v158, v158
	v_exp_f32_e32 v159, v159
	v_mul_f32_e32 v154, v152, v71
	v_pk_mul_f32 v[136:137], v[156:157], v[136:137]
	s_waitcnt lgkmcnt(14)
	v_pk_fma_f32 v[136:137], v[154:155], v[72:73], v[136:137] op_sel_hi:[0,1,1]
	s_waitcnt lgkmcnt(11)
	v_pk_fma_f32 v[72:73], v[88:89], v[136:137], 0 op_sel_hi:[1,1,0]
	v_pk_mul_f32 v[88:89], v[158:159], v[138:139]
	s_nop 0
	v_pk_fma_f32 v[138:139], v[154:155], v[74:75], v[88:89] op_sel_hi:[0,1,1]
	v_pk_mul_f32 v[74:75], v[152:153], v[10:11] op_sel_hi:[0,1]
	v_exp_f32_e32 v74, v74
	v_exp_f32_e32 v75, v75
	v_pk_mul_f32 v[88:89], v[152:153], v[12:13] op_sel_hi:[0,1]
	v_exp_f32_e32 v88, v88
	v_exp_f32_e32 v89, v89
	v_pk_mul_f32 v[74:75], v[74:75], v[140:141]
	v_pk_fma_f32 v[72:73], v[90:91], v[138:139], v[72:73]
	v_pk_fma_f32 v[140:141], v[154:155], v[76:77], v[74:75] op_sel_hi:[0,1,1]
	v_pk_mul_f32 v[74:75], v[88:89], v[142:143]
	v_pk_mul_f32 v[76:77], v[152:153], v[8:9] op_sel_hi:[0,1]
	v_pk_fma_f32 v[142:143], v[154:155], v[78:79], v[74:75] op_sel_hi:[0,1,1]
	v_pk_mul_f32 v[74:75], v[152:153], v[6:7] op_sel_hi:[0,1]
	v_exp_f32_e32 v74, v74
	v_exp_f32_e32 v75, v75
	v_exp_f32_e32 v76, v76
	v_exp_f32_e32 v77, v77
	s_waitcnt lgkmcnt(10)
	v_pk_fma_f32 v[72:73], v[92:93], v[140:141], v[72:73]
	v_pk_mul_f32 v[74:75], v[74:75], v[144:145]
	v_pk_fma_f32 v[72:73], v[94:95], v[142:143], v[72:73]
	v_pk_fma_f32 v[144:145], v[154:155], v[80:81], v[74:75] op_sel_hi:[0,1,1]
	v_pk_mul_f32 v[74:75], v[76:77], v[146:147]
	v_pk_mul_f32 v[76:77], v[152:153], v[4:5] op_sel_hi:[0,1]
	v_pk_fma_f32 v[146:147], v[154:155], v[82:83], v[74:75] op_sel_hi:[0,1,1]
	v_pk_mul_f32 v[74:75], v[152:153], v[2:3] op_sel_hi:[0,1]
	v_exp_f32_e32 v74, v74
	v_exp_f32_e32 v75, v75
	v_exp_f32_e32 v76, v76
	v_exp_f32_e32 v77, v77
	s_waitcnt lgkmcnt(9)
	v_pk_fma_f32 v[72:73], v[96:97], v[144:145], v[72:73]
	v_pk_mul_f32 v[74:75], v[74:75], v[148:149]
	v_pk_fma_f32 v[72:73], v[98:99], v[146:147], v[72:73]
	v_pk_fma_f32 v[148:149], v[154:155], v[84:85], v[74:75] op_sel_hi:[0,1,1]
	v_pk_mul_f32 v[74:75], v[76:77], v[150:151]
	s_waitcnt lgkmcnt(8)
	v_pk_fma_f32 v[72:73], v[100:101], v[148:149], v[72:73]
	v_pk_fma_f32 v[150:151], v[154:155], v[86:87], v[74:75] op_sel_hi:[0,1,1]
	v_pk_fma_f32 v[72:73], v[102:103], v[150:151], v[72:73]
	s_nop 0
	v_add_f32_e32 v71, v72, v73
	v_fma_mix_f32 v71, v69, v54, v71 op_sel_hi:[0,1,0]
	s_waitcnt vmcnt(0)
	v_fma_mixlo_f16 v71, v71, v58, 0 op_sel_hi:[0,1,0]
	ds_write_b16 v70, v71 offset:4096
	global_load_dwordx4 v[50:53], v[178:179], off
	global_load_dwordx4 v[42:45], v[180:181], off
	global_load_dwordx4 v[46:49], v[182:183], off
	global_load_dwordx4 v[38:41], v[184:185], off
	global_load_dwordx4 v[30:33], v[186:187], off
	global_load_dwordx4 v[34:37], v[188:189], off
	global_load_dwordx4 v[26:29], v[190:191], off
	global_load_dwordx4 v[18:21], v[192:193], off
	global_load_dwordx4 v[22:25], v[194:195], off
	ds_read_b128 v[72:75], v67 offset:256
	ds_read_b128 v[76:79], v67 offset:272
	ds_read_b128 v[80:83], v67 offset:288
	ds_read_b128 v[84:87], v67 offset:304
	ds_read_b128 v[88:91], v67 offset:320
	ds_read_b128 v[92:95], v67 offset:336
	ds_read_b128 v[96:99], v67 offset:352
	ds_read_b128 v[100:103], v67 offset:368
	v_cvt_f32_f16_sdwa v62, v62 dst_sel:DWORD dst_unused:UNUSED_PAD src0_sel:WORD_1
	v_cvt_f32_f16_sdwa v71, v54 dst_sel:DWORD dst_unused:UNUSED_PAD src0_sel:WORD_1
	v_pk_mul_f32 v[154:155], v[62:63], v[14:15] op_sel_hi:[0,1]
	v_exp_f32_e32 v154, v154
	v_exp_f32_e32 v155, v155
	v_pk_mul_f32 v[156:157], v[62:63], v[16:17] op_sel_hi:[0,1]
	v_exp_f32_e32 v156, v156
	v_exp_f32_e32 v157, v157
	v_mul_f32_e32 v152, v62, v71
	v_pk_mul_f32 v[136:137], v[154:155], v[136:137]
	s_waitcnt lgkmcnt(14)
	v_pk_fma_f32 v[136:137], v[152:153], v[104:105], v[136:137] op_sel_hi:[0,1,1]
	s_waitcnt lgkmcnt(12)
	v_pk_fma_f32 v[104:105], v[120:121], v[136:137], 0 op_sel_hi:[1,1,0]
	v_pk_mul_f32 v[120:121], v[156:157], v[138:139]
	s_nop 0
	v_pk_fma_f32 v[138:139], v[152:153], v[106:107], v[120:121] op_sel_hi:[0,1,1]
	v_pk_mul_f32 v[106:107], v[62:63], v[10:11] op_sel_hi:[0,1]
	v_exp_f32_e32 v106, v106
	v_exp_f32_e32 v107, v107
	v_pk_mul_f32 v[120:121], v[62:63], v[12:13] op_sel_hi:[0,1]
	v_exp_f32_e32 v120, v120
	v_exp_f32_e32 v121, v121
	v_pk_mul_f32 v[106:107], v[106:107], v[140:141]
	v_pk_fma_f32 v[104:105], v[122:123], v[138:139], v[104:105]
	v_pk_fma_f32 v[140:141], v[152:153], v[108:109], v[106:107] op_sel_hi:[0,1,1]
	v_pk_mul_f32 v[106:107], v[120:121], v[142:143]
	v_pk_mul_f32 v[108:109], v[62:63], v[8:9] op_sel_hi:[0,1]
	v_pk_fma_f32 v[142:143], v[152:153], v[110:111], v[106:107] op_sel_hi:[0,1,1]
	v_pk_mul_f32 v[106:107], v[62:63], v[6:7] op_sel_hi:[0,1]
	v_exp_f32_e32 v106, v106
	v_exp_f32_e32 v107, v107
	v_exp_f32_e32 v108, v108
	v_exp_f32_e32 v109, v109
	s_waitcnt lgkmcnt(11)
	v_pk_fma_f32 v[104:105], v[124:125], v[140:141], v[104:105]
	v_pk_mul_f32 v[106:107], v[106:107], v[144:145]
	v_pk_fma_f32 v[104:105], v[126:127], v[142:143], v[104:105]
	v_pk_fma_f32 v[144:145], v[152:153], v[112:113], v[106:107] op_sel_hi:[0,1,1]
	v_pk_mul_f32 v[106:107], v[108:109], v[146:147]
	v_pk_mul_f32 v[108:109], v[62:63], v[4:5] op_sel_hi:[0,1]
	v_pk_fma_f32 v[146:147], v[152:153], v[114:115], v[106:107] op_sel_hi:[0,1,1]
	v_pk_mul_f32 v[106:107], v[62:63], v[2:3] op_sel_hi:[0,1]
	v_exp_f32_e32 v106, v106
	v_exp_f32_e32 v107, v107
	v_exp_f32_e32 v108, v108
	v_exp_f32_e32 v109, v109
	s_waitcnt lgkmcnt(10)
	v_pk_fma_f32 v[104:105], v[128:129], v[144:145], v[104:105]
	v_pk_mul_f32 v[106:107], v[106:107], v[148:149]
	v_pk_fma_f32 v[104:105], v[130:131], v[146:147], v[104:105]
	v_pk_fma_f32 v[148:149], v[152:153], v[116:117], v[106:107] op_sel_hi:[0,1,1]
	v_pk_mul_f32 v[106:107], v[108:109], v[150:151]
	s_waitcnt lgkmcnt(9)
	v_pk_fma_f32 v[104:105], v[132:133], v[148:149], v[104:105]
	v_pk_fma_f32 v[150:151], v[152:153], v[118:119], v[106:107] op_sel_hi:[0,1,1]
	v_pk_fma_f32 v[104:105], v[134:135], v[150:151], v[104:105]
	s_nop 0
	v_add_f32_e32 v62, v104, v105
	v_fma_mix_f32 v54, v69, v54, v62 op_sel:[0,1,0] op_sel_hi:[0,1,0]
	v_fma_mixlo_f16 v54, v54, v58, 0 op_sel:[0,1,0] op_sel_hi:[0,1,0]
	ds_write_b16 v70, v54 offset:5136
	ds_read_b128 v[104:107], v67 offset:384
	ds_read_b128 v[108:111], v67 offset:400
	ds_read_b128 v[112:115], v67 offset:416
	ds_read_b128 v[116:119], v67 offset:432
	ds_read_b128 v[120:123], v67 offset:448
	ds_read_b128 v[124:127], v67 offset:464
	ds_read_b128 v[128:131], v67 offset:480
	ds_read_b128 v[132:135], v67 offset:496
	v_cvt_f32_f16_e32 v54, v63
	v_cvt_f32_f16_e32 v58, v55
	v_pk_mul_f32 v[152:153], v[54:55], v[14:15] op_sel_hi:[0,1]
	v_exp_f32_e32 v152, v152
	v_exp_f32_e32 v153, v153
	v_pk_mul_f32 v[154:155], v[54:55], v[16:17] op_sel_hi:[0,1]
	v_exp_f32_e32 v154, v154
	v_exp_f32_e32 v155, v155
	v_mul_f32_e32 v58, v54, v58
	v_pk_mul_f32 v[136:137], v[152:153], v[136:137]
	s_waitcnt lgkmcnt(14)
	v_pk_fma_f32 v[136:137], v[58:59], v[72:73], v[136:137] op_sel_hi:[0,1,1]
	s_waitcnt lgkmcnt(12)
	v_pk_fma_f32 v[72:73], v[88:89], v[136:137], 0 op_sel_hi:[1,1,0]
	v_pk_mul_f32 v[88:89], v[154:155], v[138:139]
	s_nop 0
	v_pk_fma_f32 v[138:139], v[58:59], v[74:75], v[88:89] op_sel_hi:[0,1,1]
	v_pk_mul_f32 v[74:75], v[54:55], v[10:11] op_sel_hi:[0,1]
	v_exp_f32_e32 v74, v74
	v_exp_f32_e32 v75, v75
	v_pk_mul_f32 v[88:89], v[54:55], v[12:13] op_sel_hi:[0,1]
	v_exp_f32_e32 v88, v88
	v_exp_f32_e32 v89, v89
	v_pk_mul_f32 v[74:75], v[74:75], v[140:141]
	v_pk_fma_f32 v[72:73], v[90:91], v[138:139], v[72:73]
	v_pk_fma_f32 v[140:141], v[58:59], v[76:77], v[74:75] op_sel_hi:[0,1,1]
	v_pk_mul_f32 v[74:75], v[88:89], v[142:143]
	v_pk_mul_f32 v[76:77], v[54:55], v[8:9] op_sel_hi:[0,1]
	v_pk_fma_f32 v[142:143], v[58:59], v[78:79], v[74:75] op_sel_hi:[0,1,1]
	v_pk_mul_f32 v[74:75], v[54:55], v[6:7] op_sel_hi:[0,1]
	v_exp_f32_e32 v74, v74
	v_exp_f32_e32 v75, v75
	v_exp_f32_e32 v76, v76
	v_exp_f32_e32 v77, v77
	s_waitcnt lgkmcnt(11)
	v_pk_fma_f32 v[72:73], v[92:93], v[140:141], v[72:73]
	v_pk_mul_f32 v[74:75], v[74:75], v[144:145]
	v_pk_fma_f32 v[72:73], v[94:95], v[142:143], v[72:73]
	v_pk_fma_f32 v[144:145], v[58:59], v[80:81], v[74:75] op_sel_hi:[0,1,1]
	v_pk_mul_f32 v[74:75], v[76:77], v[146:147]
	v_pk_mul_f32 v[76:77], v[54:55], v[4:5] op_sel_hi:[0,1]
	v_pk_fma_f32 v[146:147], v[58:59], v[82:83], v[74:75] op_sel_hi:[0,1,1]
	v_pk_mul_f32 v[74:75], v[54:55], v[2:3] op_sel_hi:[0,1]
	v_exp_f32_e32 v74, v74
	v_exp_f32_e32 v75, v75
	v_exp_f32_e32 v76, v76
	v_exp_f32_e32 v77, v77
	s_waitcnt lgkmcnt(10)
	v_pk_fma_f32 v[72:73], v[96:97], v[144:145], v[72:73]
	v_pk_mul_f32 v[74:75], v[74:75], v[148:149]
	v_pk_fma_f32 v[72:73], v[98:99], v[146:147], v[72:73]
	v_pk_fma_f32 v[148:149], v[58:59], v[84:85], v[74:75] op_sel_hi:[0,1,1]
	v_pk_mul_f32 v[74:75], v[76:77], v[150:151]
	s_waitcnt lgkmcnt(9)
	v_pk_fma_f32 v[72:73], v[100:101], v[148:149], v[72:73]
	v_pk_fma_f32 v[150:151], v[58:59], v[86:87], v[74:75] op_sel_hi:[0,1,1]
	v_pk_fma_f32 v[72:73], v[102:103], v[150:151], v[72:73]
	s_nop 0
	v_add_f32_e32 v54, v72, v73
	v_fma_mix_f32 v54, v69, v55, v54 op_sel_hi:[0,1,0]
	v_fma_mixlo_f16 v54, v54, v59, 0 op_sel_hi:[0,1,0]
	ds_write_b16 v70, v54 offset:6176
	ds_read_b128 v[72:75], v67 offset:512
	ds_read_b128 v[76:79], v67 offset:528
	ds_read_b128 v[80:83], v67 offset:544
	ds_read_b128 v[84:87], v67 offset:560
	ds_read_b128 v[88:91], v67 offset:576
	ds_read_b128 v[92:95], v67 offset:592
	ds_read_b128 v[96:99], v67 offset:608
	ds_read_b128 v[100:103], v67 offset:624
	v_cvt_f32_f16_sdwa v54, v63 dst_sel:DWORD dst_unused:UNUSED_PAD src0_sel:WORD_1
	v_cvt_f32_f16_sdwa v58, v55 dst_sel:DWORD dst_unused:UNUSED_PAD src0_sel:WORD_1
	v_pk_mul_f32 v[62:63], v[54:55], v[14:15] op_sel_hi:[0,1]
	v_exp_f32_e32 v62, v62
	v_exp_f32_e32 v63, v63
	v_pk_mul_f32 v[152:153], v[54:55], v[16:17] op_sel_hi:[0,1]
	v_exp_f32_e32 v152, v152
	v_exp_f32_e32 v153, v153
	v_mul_f32_e32 v58, v54, v58
	v_pk_mul_f32 v[62:63], v[62:63], v[136:137]
	s_waitcnt lgkmcnt(14)
	v_pk_fma_f32 v[62:63], v[58:59], v[104:105], v[62:63] op_sel_hi:[0,1,1]
	s_waitcnt lgkmcnt(12)
	v_pk_fma_f32 v[104:105], v[120:121], v[62:63], 0 op_sel_hi:[1,1,0]
	v_pk_mul_f32 v[120:121], v[152:153], v[138:139]
	s_nop 0
	v_pk_fma_f32 v[136:137], v[58:59], v[106:107], v[120:121] op_sel_hi:[0,1,1]
	v_pk_mul_f32 v[106:107], v[54:55], v[10:11] op_sel_hi:[0,1]
	v_exp_f32_e32 v106, v106
	v_exp_f32_e32 v107, v107
	v_pk_mul_f32 v[120:121], v[54:55], v[12:13] op_sel_hi:[0,1]
	v_exp_f32_e32 v120, v120
	v_exp_f32_e32 v121, v121
	v_pk_mul_f32 v[106:107], v[106:107], v[140:141]
	v_pk_fma_f32 v[104:105], v[122:123], v[136:137], v[104:105]
	v_pk_fma_f32 v[138:139], v[58:59], v[108:109], v[106:107] op_sel_hi:[0,1,1]
	v_pk_mul_f32 v[106:107], v[120:121], v[142:143]
	v_pk_mul_f32 v[108:109], v[54:55], v[8:9] op_sel_hi:[0,1]
	v_pk_fma_f32 v[140:141], v[58:59], v[110:111], v[106:107] op_sel_hi:[0,1,1]
	v_pk_mul_f32 v[106:107], v[54:55], v[6:7] op_sel_hi:[0,1]
	v_exp_f32_e32 v106, v106
	v_exp_f32_e32 v107, v107
	v_exp_f32_e32 v108, v108
	v_exp_f32_e32 v109, v109
	s_waitcnt lgkmcnt(11)
	v_pk_fma_f32 v[104:105], v[124:125], v[138:139], v[104:105]
	v_pk_mul_f32 v[106:107], v[106:107], v[144:145]
	v_pk_fma_f32 v[104:105], v[126:127], v[140:141], v[104:105]
	v_pk_fma_f32 v[142:143], v[58:59], v[112:113], v[106:107] op_sel_hi:[0,1,1]
	v_pk_mul_f32 v[106:107], v[108:109], v[146:147]
	v_pk_mul_f32 v[108:109], v[54:55], v[4:5] op_sel_hi:[0,1]
	v_pk_fma_f32 v[144:145], v[58:59], v[114:115], v[106:107] op_sel_hi:[0,1,1]
	v_pk_mul_f32 v[106:107], v[54:55], v[2:3] op_sel_hi:[0,1]
	v_exp_f32_e32 v106, v106
	v_exp_f32_e32 v107, v107
	v_exp_f32_e32 v108, v108
	v_exp_f32_e32 v109, v109
	s_waitcnt lgkmcnt(10)
	v_pk_fma_f32 v[104:105], v[128:129], v[142:143], v[104:105]
	v_pk_mul_f32 v[106:107], v[106:107], v[148:149]
	v_pk_fma_f32 v[104:105], v[130:131], v[144:145], v[104:105]
	v_pk_fma_f32 v[146:147], v[58:59], v[116:117], v[106:107] op_sel_hi:[0,1,1]
	v_pk_mul_f32 v[106:107], v[108:109], v[150:151]
	s_waitcnt lgkmcnt(9)
	v_pk_fma_f32 v[104:105], v[132:133], v[146:147], v[104:105]
	v_pk_fma_f32 v[148:149], v[58:59], v[118:119], v[106:107] op_sel_hi:[0,1,1]
	v_pk_fma_f32 v[104:105], v[134:135], v[148:149], v[104:105]
	s_nop 0
	v_add_f32_e32 v54, v104, v105
	v_fma_mix_f32 v54, v69, v55, v54 op_sel:[0,1,0] op_sel_hi:[0,1,0]
	v_fma_mixlo_f16 v54, v54, v59, 0 op_sel:[0,1,0] op_sel_hi:[0,1,0]
	ds_write_b16 v70, v54 offset:7216
	ds_read_b128 v[104:107], v67 offset:640
	ds_read_b128 v[108:111], v67 offset:656
	ds_read_b128 v[112:115], v67 offset:672
	ds_read_b128 v[116:119], v67 offset:688
	ds_read_b128 v[120:123], v67 offset:704
	ds_read_b128 v[124:127], v67 offset:720
	ds_read_b128 v[128:131], v67 offset:736
	ds_read_b128 v[132:135], v67 offset:752
	v_cvt_f32_f16_e32 v54, v64
	v_cvt_f32_f16_e32 v55, v56
	v_pk_mul_f32 v[150:151], v[54:55], v[14:15] op_sel_hi:[0,1]
	v_exp_f32_e32 v150, v150
	v_exp_f32_e32 v151, v151
	v_pk_mul_f32 v[152:153], v[54:55], v[16:17] op_sel_hi:[0,1]
	v_exp_f32_e32 v152, v152
	v_exp_f32_e32 v153, v153
	v_mul_f32_e32 v58, v54, v55
	v_pk_mul_f32 v[62:63], v[150:151], v[62:63]
	s_waitcnt lgkmcnt(14)
	v_pk_fma_f32 v[62:63], v[58:59], v[72:73], v[62:63] op_sel_hi:[0,1,1]
	s_waitcnt lgkmcnt(12)
	v_pk_fma_f32 v[72:73], v[88:89], v[62:63], 0 op_sel_hi:[1,1,0]
	v_pk_mul_f32 v[88:89], v[152:153], v[136:137]
	s_nop 0
	v_pk_fma_f32 v[136:137], v[58:59], v[74:75], v[88:89] op_sel_hi:[0,1,1]
	v_pk_mul_f32 v[74:75], v[54:55], v[10:11] op_sel_hi:[0,1]
	v_exp_f32_e32 v74, v74
	v_exp_f32_e32 v75, v75
	v_pk_mul_f32 v[88:89], v[54:55], v[12:13] op_sel_hi:[0,1]
	v_exp_f32_e32 v88, v88
	v_exp_f32_e32 v89, v89
	v_pk_mul_f32 v[74:75], v[74:75], v[138:139]
	v_pk_fma_f32 v[72:73], v[90:91], v[136:137], v[72:73]
	v_pk_fma_f32 v[138:139], v[58:59], v[76:77], v[74:75] op_sel_hi:[0,1,1]
	v_pk_mul_f32 v[74:75], v[88:89], v[140:141]
	v_pk_mul_f32 v[76:77], v[54:55], v[8:9] op_sel_hi:[0,1]
	v_pk_fma_f32 v[140:141], v[58:59], v[78:79], v[74:75] op_sel_hi:[0,1,1]
	v_pk_mul_f32 v[74:75], v[54:55], v[6:7] op_sel_hi:[0,1]
	v_exp_f32_e32 v74, v74
	v_exp_f32_e32 v75, v75
	v_exp_f32_e32 v76, v76
	v_exp_f32_e32 v77, v77
	s_waitcnt lgkmcnt(11)
	v_pk_fma_f32 v[72:73], v[92:93], v[138:139], v[72:73]
	v_pk_mul_f32 v[74:75], v[74:75], v[142:143]
	v_pk_fma_f32 v[72:73], v[94:95], v[140:141], v[72:73]
	v_pk_fma_f32 v[142:143], v[58:59], v[80:81], v[74:75] op_sel_hi:[0,1,1]
	v_pk_mul_f32 v[74:75], v[76:77], v[144:145]
	s_waitcnt lgkmcnt(10)
	v_pk_fma_f32 v[72:73], v[96:97], v[142:143], v[72:73]
	v_pk_fma_f32 v[144:145], v[58:59], v[82:83], v[74:75] op_sel_hi:[0,1,1]
	v_pk_mul_f32 v[74:75], v[54:55], v[2:3] op_sel_hi:[0,1]
	v_exp_f32_e32 v74, v74
	v_exp_f32_e32 v75, v75
	v_pk_mul_f32 v[54:55], v[54:55], v[4:5] op_sel_hi:[0,1]
	v_exp_f32_e32 v54, v54
	v_exp_f32_e32 v55, v55
	v_pk_mul_f32 v[74:75], v[74:75], v[146:147]
	v_pk_fma_f32 v[72:73], v[98:99], v[144:145], v[72:73]
	v_pk_fma_f32 v[146:147], v[58:59], v[84:85], v[74:75] op_sel_hi:[0,1,1]
	v_pk_mul_f32 v[54:55], v[54:55], v[148:149]
	s_waitcnt lgkmcnt(9)
	v_pk_fma_f32 v[72:73], v[100:101], v[146:147], v[72:73]
	v_pk_fma_f32 v[54:55], v[58:59], v[86:87], v[54:55] op_sel_hi:[0,1,1]
	v_pk_fma_f32 v[58:59], v[102:103], v[54:55], v[72:73]
	s_nop 0
	v_add_f32_e32 v58, v58, v59
	v_fma_mix_f32 v58, v69, v56, v58 op_sel_hi:[0,1,0]
	v_fma_mixlo_f16 v58, v58, v60, 0 op_sel_hi:[0,1,0]
	ds_write_b16 v70, v58 offset:8256
	ds_read_b128 v[72:75], v67 offset:768
	ds_read_b128 v[76:79], v67 offset:784
	ds_read_b128 v[80:83], v67 offset:800
	ds_read_b128 v[84:87], v67 offset:816
	ds_read_b128 v[88:91], v67 offset:832
	ds_read_b128 v[92:95], v67 offset:848
	ds_read_b128 v[96:99], v67 offset:864
	ds_read_b128 v[100:103], v67 offset:880
	v_cvt_f32_f16_sdwa v58, v64 dst_sel:DWORD dst_unused:UNUSED_PAD src0_sel:WORD_1
	v_cvt_f32_f16_sdwa v59, v56 dst_sel:DWORD dst_unused:UNUSED_PAD src0_sel:WORD_1
	v_pk_mul_f32 v[148:149], v[58:59], v[14:15] op_sel_hi:[0,1]
	v_exp_f32_e32 v148, v148
	v_exp_f32_e32 v149, v149
	v_pk_mul_f32 v[150:151], v[58:59], v[16:17] op_sel_hi:[0,1]
	v_exp_f32_e32 v150, v150
	v_exp_f32_e32 v151, v151
	v_mul_f32_e32 v64, v58, v59
	v_pk_mul_f32 v[62:63], v[148:149], v[62:63]
	s_waitcnt lgkmcnt(14)
	v_pk_fma_f32 v[62:63], v[64:65], v[104:105], v[62:63] op_sel_hi:[0,1,1]
	s_waitcnt lgkmcnt(12)
	v_pk_fma_f32 v[104:105], v[120:121], v[62:63], 0 op_sel_hi:[1,1,0]
	v_pk_mul_f32 v[120:121], v[150:151], v[136:137]
	s_nop 0
	v_pk_fma_f32 v[136:137], v[64:65], v[106:107], v[120:121] op_sel_hi:[0,1,1]
	v_pk_mul_f32 v[106:107], v[58:59], v[10:11] op_sel_hi:[0,1]
	v_exp_f32_e32 v106, v106
	v_exp_f32_e32 v107, v107
	v_pk_mul_f32 v[120:121], v[58:59], v[12:13] op_sel_hi:[0,1]
	v_exp_f32_e32 v120, v120
	v_exp_f32_e32 v121, v121
	v_pk_mul_f32 v[106:107], v[106:107], v[138:139]
	v_pk_fma_f32 v[104:105], v[122:123], v[136:137], v[104:105]
	v_pk_fma_f32 v[138:139], v[64:65], v[108:109], v[106:107] op_sel_hi:[0,1,1]
	v_pk_mul_f32 v[106:107], v[120:121], v[140:141]
	v_pk_mul_f32 v[108:109], v[58:59], v[8:9] op_sel_hi:[0,1]
	v_pk_fma_f32 v[140:141], v[64:65], v[110:111], v[106:107] op_sel_hi:[0,1,1]
	v_pk_mul_f32 v[106:107], v[58:59], v[6:7] op_sel_hi:[0,1]
	v_exp_f32_e32 v106, v106
	v_exp_f32_e32 v107, v107
	v_exp_f32_e32 v108, v108
	v_exp_f32_e32 v109, v109
	s_waitcnt lgkmcnt(11)
	v_pk_fma_f32 v[104:105], v[124:125], v[138:139], v[104:105]
	v_pk_mul_f32 v[106:107], v[106:107], v[142:143]
	v_pk_fma_f32 v[104:105], v[126:127], v[140:141], v[104:105]
	v_pk_fma_f32 v[142:143], v[64:65], v[112:113], v[106:107] op_sel_hi:[0,1,1]
	v_pk_mul_f32 v[106:107], v[108:109], v[144:145]
	s_waitcnt lgkmcnt(10)
	v_pk_fma_f32 v[104:105], v[128:129], v[142:143], v[104:105]
	v_pk_fma_f32 v[144:145], v[64:65], v[114:115], v[106:107] op_sel_hi:[0,1,1]
	v_pk_mul_f32 v[106:107], v[58:59], v[2:3] op_sel_hi:[0,1]
	v_exp_f32_e32 v106, v106
	v_exp_f32_e32 v107, v107
	v_pk_mul_f32 v[58:59], v[58:59], v[4:5] op_sel_hi:[0,1]
	v_exp_f32_e32 v58, v58
	v_exp_f32_e32 v59, v59
	v_pk_mul_f32 v[106:107], v[106:107], v[146:147]
	v_pk_fma_f32 v[104:105], v[130:131], v[144:145], v[104:105]
	v_pk_fma_f32 v[146:147], v[64:65], v[116:117], v[106:107] op_sel_hi:[0,1,1]
	v_pk_mul_f32 v[54:55], v[58:59], v[54:55]
	s_waitcnt lgkmcnt(9)
	v_pk_fma_f32 v[104:105], v[132:133], v[146:147], v[104:105]
	v_pk_fma_f32 v[54:55], v[64:65], v[118:119], v[54:55] op_sel_hi:[0,1,1]
	v_pk_fma_f32 v[58:59], v[134:135], v[54:55], v[104:105]
	s_nop 0
	v_add_f32_e32 v58, v58, v59
	v_fma_mix_f32 v56, v69, v56, v58 op_sel:[0,1,0] op_sel_hi:[0,1,0]
	v_fma_mixlo_f16 v56, v56, v60, 0 op_sel:[0,1,0] op_sel_hi:[0,1,0]
	ds_write_b16 v70, v56 offset:9296
	ds_read_b128 v[104:107], v67 offset:896
	ds_read_b128 v[108:111], v67 offset:912
	ds_read_b128 v[112:115], v67 offset:928
	ds_read_b128 v[116:119], v67 offset:944
	ds_read_b128 v[120:123], v67 offset:960
	ds_read_b128 v[124:127], v67 offset:976
	ds_read_b128 v[128:131], v67 offset:992
	ds_read_b128 v[132:135], v67 offset:1008
	v_cvt_f32_f16_e32 v56, v65
	v_cvt_f32_f16_e32 v58, v57
	v_pk_mul_f32 v[148:149], v[56:57], v[14:15] op_sel_hi:[0,1]
	v_exp_f32_e32 v148, v148
	v_exp_f32_e32 v149, v149
	v_pk_mul_f32 v[150:151], v[56:57], v[16:17] op_sel_hi:[0,1]
	v_exp_f32_e32 v150, v150
	v_exp_f32_e32 v151, v151
	v_mul_f32_e32 v58, v56, v58
	v_pk_mul_f32 v[62:63], v[148:149], v[62:63]
	s_waitcnt lgkmcnt(14)
	v_pk_fma_f32 v[62:63], v[58:59], v[72:73], v[62:63] op_sel_hi:[0,1,1]
	s_waitcnt lgkmcnt(12)
	v_pk_fma_f32 v[72:73], v[88:89], v[62:63], 0 op_sel_hi:[1,1,0]
	v_pk_mul_f32 v[88:89], v[150:151], v[136:137]
	s_nop 0
	v_pk_fma_f32 v[136:137], v[58:59], v[74:75], v[88:89] op_sel_hi:[0,1,1]
	v_pk_mul_f32 v[74:75], v[56:57], v[10:11] op_sel_hi:[0,1]
	v_exp_f32_e32 v74, v74
	v_exp_f32_e32 v75, v75
	v_pk_mul_f32 v[88:89], v[56:57], v[12:13] op_sel_hi:[0,1]
	v_exp_f32_e32 v88, v88
	v_exp_f32_e32 v89, v89
	v_pk_mul_f32 v[74:75], v[74:75], v[138:139]
	v_pk_fma_f32 v[72:73], v[90:91], v[136:137], v[72:73]
	v_pk_fma_f32 v[138:139], v[58:59], v[76:77], v[74:75] op_sel_hi:[0,1,1]
	v_pk_mul_f32 v[74:75], v[88:89], v[140:141]
	v_pk_mul_f32 v[76:77], v[56:57], v[8:9] op_sel_hi:[0,1]
	v_pk_fma_f32 v[140:141], v[58:59], v[78:79], v[74:75] op_sel_hi:[0,1,1]
	v_pk_mul_f32 v[74:75], v[56:57], v[6:7] op_sel_hi:[0,1]
	v_exp_f32_e32 v74, v74
	v_exp_f32_e32 v75, v75
	v_exp_f32_e32 v76, v76
	v_exp_f32_e32 v77, v77
	s_waitcnt lgkmcnt(11)
	v_pk_fma_f32 v[72:73], v[92:93], v[138:139], v[72:73]
	v_pk_mul_f32 v[74:75], v[74:75], v[142:143]
	v_pk_fma_f32 v[72:73], v[94:95], v[140:141], v[72:73]
	v_pk_fma_f32 v[142:143], v[58:59], v[80:81], v[74:75] op_sel_hi:[0,1,1]
	v_pk_mul_f32 v[74:75], v[76:77], v[144:145]
	v_pk_mul_f32 v[76:77], v[56:57], v[4:5] op_sel_hi:[0,1]
	v_pk_fma_f32 v[144:145], v[58:59], v[82:83], v[74:75] op_sel_hi:[0,1,1]
	v_pk_mul_f32 v[74:75], v[56:57], v[2:3] op_sel_hi:[0,1]
	v_exp_f32_e32 v74, v74
	v_exp_f32_e32 v75, v75
	v_exp_f32_e32 v76, v76
	v_exp_f32_e32 v77, v77
	s_waitcnt lgkmcnt(10)
	v_pk_fma_f32 v[72:73], v[96:97], v[142:143], v[72:73]
	v_pk_mul_f32 v[74:75], v[74:75], v[146:147]
	v_pk_fma_f32 v[72:73], v[98:99], v[144:145], v[72:73]
	v_pk_fma_f32 v[146:147], v[58:59], v[84:85], v[74:75] op_sel_hi:[0,1,1]
	v_pk_mul_f32 v[54:55], v[76:77], v[54:55]
	s_waitcnt lgkmcnt(9)
	v_pk_fma_f32 v[72:73], v[100:101], v[146:147], v[72:73]
	v_pk_fma_f32 v[54:55], v[58:59], v[86:87], v[54:55] op_sel_hi:[0,1,1]
	v_pk_fma_f32 v[58:59], v[102:103], v[54:55], v[72:73]
	s_nop 0
	v_add_f32_e32 v56, v58, v59
	v_fma_mix_f32 v56, v69, v57, v56 op_sel_hi:[0,1,0]
	v_fma_mixlo_f16 v56, v56, v61, 0 op_sel_hi:[0,1,0]
	ds_write_b16 v70, v56 offset:10336
	ds_read_b128 v[72:75], v67 offset:1024
	ds_read_b128 v[76:79], v67 offset:1040
	ds_read_b128 v[80:83], v67 offset:1056
	ds_read_b128 v[84:87], v67 offset:1072
	ds_read_b128 v[88:91], v67 offset:1088
	ds_read_b128 v[92:95], v67 offset:1104
	ds_read_b128 v[96:99], v67 offset:1120
	ds_read_b128 v[100:103], v67 offset:1136
	v_cvt_f32_f16_sdwa v56, v65 dst_sel:DWORD dst_unused:UNUSED_PAD src0_sel:WORD_1
	v_cvt_f32_f16_sdwa v58, v57 dst_sel:DWORD dst_unused:UNUSED_PAD src0_sel:WORD_1
	v_pk_mul_f32 v[64:65], v[56:57], v[14:15] op_sel_hi:[0,1]
	v_pk_mul_f32 v[148:149], v[56:57], v[16:17] op_sel_hi:[0,1]
	v_exp_f32_e32 v64, v64
	v_exp_f32_e32 v65, v65
	v_exp_f32_e32 v148, v148
	v_exp_f32_e32 v149, v149
	v_mul_f32_e32 v58, v56, v58
	v_pk_mul_f32 v[62:63], v[64:65], v[62:63]
	v_pk_mul_f32 v[64:65], v[148:149], v[136:137]
	s_waitcnt lgkmcnt(14)
	v_pk_fma_f32 v[136:137], v[58:59], v[106:107], v[64:65] op_sel_hi:[0,1,1]
	v_pk_mul_f32 v[64:65], v[56:57], v[10:11] op_sel_hi:[0,1]
	v_pk_fma_f32 v[150:151], v[58:59], v[104:105], v[62:63] op_sel_hi:[0,1,1]
	v_exp_f32_e32 v64, v64
	v_exp_f32_e32 v65, v65
	v_pk_mul_f32 v[104:105], v[56:57], v[12:13] op_sel_hi:[0,1]
	v_exp_f32_e32 v104, v104
	v_exp_f32_e32 v105, v105
	s_waitcnt lgkmcnt(12)
	v_pk_fma_f32 v[62:63], v[120:121], v[150:151], 0 op_sel_hi:[1,1,0]
	v_pk_mul_f32 v[64:65], v[64:65], v[138:139]
	v_pk_fma_f32 v[62:63], v[122:123], v[136:137], v[62:63]
	v_pk_fma_f32 v[138:139], v[58:59], v[108:109], v[64:65] op_sel_hi:[0,1,1]
	v_pk_mul_f32 v[64:65], v[104:105], v[140:141]
	s_waitcnt lgkmcnt(11)
	v_pk_fma_f32 v[62:63], v[124:125], v[138:139], v[62:63]
	v_pk_fma_f32 v[124:125], v[58:59], v[110:111], v[64:65] op_sel_hi:[0,1,1]
	v_pk_mul_f32 v[64:65], v[56:57], v[6:7] op_sel_hi:[0,1]
	v_exp_f32_e32 v64, v64
	v_exp_f32_e32 v65, v65
	v_pk_mul_f32 v[104:105], v[56:57], v[8:9] op_sel_hi:[0,1]
	v_exp_f32_e32 v104, v104
	v_exp_f32_e32 v105, v105
	v_pk_mul_f32 v[64:65], v[64:65], v[142:143]
	v_pk_fma_f32 v[62:63], v[126:127], v[124:125], v[62:63]
	v_pk_fma_f32 v[126:127], v[58:59], v[112:113], v[64:65] op_sel_hi:[0,1,1]
	v_pk_mul_f32 v[64:65], v[104:105], v[144:145]
	s_waitcnt lgkmcnt(10)
	v_pk_fma_f32 v[62:63], v[128:129], v[126:127], v[62:63]
	v_pk_fma_f32 v[128:129], v[58:59], v[114:115], v[64:65] op_sel_hi:[0,1,1]
	v_pk_mul_f32 v[64:65], v[56:57], v[2:3] op_sel_hi:[0,1]
	v_exp_f32_e32 v64, v64
	v_exp_f32_e32 v65, v65
	v_pk_mul_f32 v[104:105], v[56:57], v[4:5] op_sel_hi:[0,1]
	v_exp_f32_e32 v104, v104
	v_exp_f32_e32 v105, v105
	v_pk_mul_f32 v[64:65], v[64:65], v[146:147]
	v_pk_fma_f32 v[62:63], v[130:131], v[128:129], v[62:63]
	v_pk_fma_f32 v[130:131], v[58:59], v[116:117], v[64:65] op_sel_hi:[0,1,1]
	v_pk_mul_f32 v[54:55], v[104:105], v[54:55]
	s_waitcnt lgkmcnt(9)
	v_pk_fma_f32 v[62:63], v[132:133], v[130:131], v[62:63]
	v_pk_fma_f32 v[132:133], v[58:59], v[118:119], v[54:55] op_sel_hi:[0,1,1]
	v_pk_fma_f32 v[54:55], v[134:135], v[132:133], v[62:63]
	s_nop 0
	v_add_f32_e32 v54, v54, v55
	v_fma_mix_f32 v54, v69, v57, v54 op_sel:[0,1,0] op_sel_hi:[0,1,0]
	v_fma_mixlo_f16 v54, v54, v61, 0 op_sel:[0,1,0] op_sel_hi:[0,1,0]
	ds_write_b16 v70, v54 offset:11376
	ds_read_b128 v[54:57], v67 offset:1152
	ds_read_b128 v[58:61], v67 offset:1168
	ds_read_b128 v[62:65], v67 offset:1184
	ds_read_b128 v[104:107], v67 offset:1200
	ds_read_b128 v[108:111], v67 offset:1216
	ds_read_b128 v[112:115], v67 offset:1232
	ds_read_b128 v[116:119], v67 offset:1248
	ds_read_b128 v[120:123], v67 offset:1264
	s_waitcnt vmcnt(8)
	v_cvt_f32_f16_e32 v134, v50
	s_waitcnt vmcnt(7)
	v_cvt_f32_f16_e32 v71, v42
	v_pk_mul_f32 v[142:143], v[134:135], v[14:15] op_sel_hi:[0,1]
	v_exp_f32_e32 v142, v142
	v_exp_f32_e32 v143, v143
	v_pk_mul_f32 v[144:145], v[134:135], v[16:17] op_sel_hi:[0,1]
	v_exp_f32_e32 v144, v144
	v_exp_f32_e32 v145, v145
	v_mul_f32_e32 v140, v134, v71
	v_pk_mul_f32 v[142:143], v[142:143], v[150:151]
	s_waitcnt lgkmcnt(14)
	v_pk_fma_f32 v[142:143], v[140:141], v[72:73], v[142:143] op_sel_hi:[0,1,1]
	s_waitcnt lgkmcnt(12)
	v_pk_fma_f32 v[72:73], v[88:89], v[142:143], 0 op_sel_hi:[1,1,0]
	v_pk_mul_f32 v[88:89], v[144:145], v[136:137]
	s_nop 0
	v_pk_fma_f32 v[136:137], v[140:141], v[74:75], v[88:89] op_sel_hi:[0,1,1]
	v_pk_mul_f32 v[74:75], v[134:135], v[10:11] op_sel_hi:[0,1]
	v_exp_f32_e32 v74, v74
	v_exp_f32_e32 v75, v75
	v_pk_mul_f32 v[88:89], v[134:135], v[12:13] op_sel_hi:[0,1]
	v_exp_f32_e32 v88, v88
	v_exp_f32_e32 v89, v89
	v_pk_mul_f32 v[74:75], v[74:75], v[138:139]
	v_pk_fma_f32 v[72:73], v[90:91], v[136:137], v[72:73]
	v_pk_fma_f32 v[138:139], v[140:141], v[76:77], v[74:75] op_sel_hi:[0,1,1]
	v_pk_mul_f32 v[74:75], v[88:89], v[124:125]
	v_pk_mul_f32 v[76:77], v[134:135], v[8:9] op_sel_hi:[0,1]
	v_pk_fma_f32 v[124:125], v[140:141], v[78:79], v[74:75] op_sel_hi:[0,1,1]
	v_pk_mul_f32 v[74:75], v[134:135], v[6:7] op_sel_hi:[0,1]
	v_exp_f32_e32 v74, v74
	v_exp_f32_e32 v75, v75
	v_exp_f32_e32 v76, v76
	v_exp_f32_e32 v77, v77
	s_waitcnt lgkmcnt(11)
	v_pk_fma_f32 v[72:73], v[92:93], v[138:139], v[72:73]
	v_pk_mul_f32 v[74:75], v[74:75], v[126:127]
	v_pk_fma_f32 v[72:73], v[94:95], v[124:125], v[72:73]
	v_pk_fma_f32 v[126:127], v[140:141], v[80:81], v[74:75] op_sel_hi:[0,1,1]
	v_pk_mul_f32 v[74:75], v[76:77], v[128:129]
	v_pk_mul_f32 v[76:77], v[134:135], v[4:5] op_sel_hi:[0,1]
	v_pk_fma_f32 v[128:129], v[140:141], v[82:83], v[74:75] op_sel_hi:[0,1,1]
	v_pk_mul_f32 v[74:75], v[134:135], v[2:3] op_sel_hi:[0,1]
	v_exp_f32_e32 v74, v74
	v_exp_f32_e32 v75, v75
	v_exp_f32_e32 v76, v76
	v_exp_f32_e32 v77, v77
	s_waitcnt lgkmcnt(10)
	v_pk_fma_f32 v[72:73], v[96:97], v[126:127], v[72:73]
	v_pk_mul_f32 v[74:75], v[74:75], v[130:131]
	v_pk_fma_f32 v[72:73], v[98:99], v[128:129], v[72:73]
	v_pk_fma_f32 v[130:131], v[140:141], v[84:85], v[74:75] op_sel_hi:[0,1,1]
	v_pk_mul_f32 v[74:75], v[76:77], v[132:133]
	s_waitcnt lgkmcnt(9)
	v_pk_fma_f32 v[72:73], v[100:101], v[130:131], v[72:73]
	v_pk_fma_f32 v[132:133], v[140:141], v[86:87], v[74:75] op_sel_hi:[0,1,1]
	v_pk_fma_f32 v[72:73], v[102:103], v[132:133], v[72:73]
	s_nop 0
	v_add_f32_e32 v71, v72, v73
	v_fma_mix_f32 v71, v69, v42, v71 op_sel_hi:[0,1,0]
	s_waitcnt vmcnt(6)
	v_fma_mixlo_f16 v71, v71, v46, 0 op_sel_hi:[0,1,0]
	ds_write_b16 v70, v71 offset:12416
	ds_read_b128 v[72:75], v67 offset:1280
	ds_read_b128 v[76:79], v67 offset:1296
	ds_read_b128 v[80:83], v67 offset:1312
	ds_read_b128 v[84:87], v67 offset:1328
	ds_read_b128 v[88:91], v67 offset:1344
	ds_read_b128 v[92:95], v67 offset:1360
	ds_read_b128 v[96:99], v67 offset:1376
	ds_read_b128 v[100:103], v67 offset:1392
	v_cvt_f32_f16_sdwa v50, v50 dst_sel:DWORD dst_unused:UNUSED_PAD src0_sel:WORD_1
	v_cvt_f32_f16_sdwa v71, v42 dst_sel:DWORD dst_unused:UNUSED_PAD src0_sel:WORD_1
	v_pk_mul_f32 v[140:141], v[50:51], v[14:15] op_sel_hi:[0,1]
	v_exp_f32_e32 v140, v140
	v_exp_f32_e32 v141, v141
	v_pk_mul_f32 v[144:145], v[50:51], v[16:17] op_sel_hi:[0,1]
	v_exp_f32_e32 v144, v144
	v_exp_f32_e32 v145, v145
	v_mul_f32_e32 v134, v50, v71
	v_pk_mul_f32 v[140:141], v[140:141], v[142:143]
	s_waitcnt lgkmcnt(14)
	v_pk_fma_f32 v[140:141], v[134:135], v[54:55], v[140:141] op_sel_hi:[0,1,1]
	s_waitcnt lgkmcnt(12)
	v_pk_fma_f32 v[54:55], v[108:109], v[140:141], 0 op_sel_hi:[1,1,0]
	v_pk_mul_f32 v[108:109], v[144:145], v[136:137]
	s_nop 0
	v_pk_fma_f32 v[136:137], v[134:135], v[56:57], v[108:109] op_sel_hi:[0,1,1]
	v_pk_mul_f32 v[56:57], v[50:51], v[10:11] op_sel_hi:[0,1]
	v_exp_f32_e32 v56, v56
	v_exp_f32_e32 v57, v57
	v_pk_mul_f32 v[108:109], v[50:51], v[12:13] op_sel_hi:[0,1]
	v_exp_f32_e32 v108, v108
	v_exp_f32_e32 v109, v109
	v_pk_mul_f32 v[56:57], v[56:57], v[138:139]
	v_pk_fma_f32 v[54:55], v[110:111], v[136:137], v[54:55]
	v_pk_fma_f32 v[138:139], v[134:135], v[58:59], v[56:57] op_sel_hi:[0,1,1]
	v_pk_mul_f32 v[56:57], v[108:109], v[124:125]
	v_pk_mul_f32 v[58:59], v[50:51], v[8:9] op_sel_hi:[0,1]
	v_pk_fma_f32 v[124:125], v[134:135], v[60:61], v[56:57] op_sel_hi:[0,1,1]
	v_pk_mul_f32 v[56:57], v[50:51], v[6:7] op_sel_hi:[0,1]
	v_exp_f32_e32 v56, v56
	v_exp_f32_e32 v57, v57
	v_exp_f32_e32 v58, v58
	v_exp_f32_e32 v59, v59
	s_waitcnt lgkmcnt(11)
	v_pk_fma_f32 v[54:55], v[112:113], v[138:139], v[54:55]
	v_pk_mul_f32 v[56:57], v[56:57], v[126:127]
	v_pk_fma_f32 v[54:55], v[114:115], v[124:125], v[54:55]
	v_pk_fma_f32 v[126:127], v[134:135], v[62:63], v[56:57] op_sel_hi:[0,1,1]
	v_pk_mul_f32 v[56:57], v[58:59], v[128:129]
	v_pk_mul_f32 v[58:59], v[50:51], v[4:5] op_sel_hi:[0,1]
	v_pk_fma_f32 v[128:129], v[134:135], v[64:65], v[56:57] op_sel_hi:[0,1,1]
	v_pk_mul_f32 v[56:57], v[50:51], v[2:3] op_sel_hi:[0,1]
	v_exp_f32_e32 v56, v56
	v_exp_f32_e32 v57, v57
	v_exp_f32_e32 v58, v58
	v_exp_f32_e32 v59, v59
	s_waitcnt lgkmcnt(10)
	v_pk_fma_f32 v[54:55], v[116:117], v[126:127], v[54:55]
	v_pk_mul_f32 v[56:57], v[56:57], v[130:131]
	v_pk_fma_f32 v[54:55], v[118:119], v[128:129], v[54:55]
	v_pk_fma_f32 v[130:131], v[134:135], v[104:105], v[56:57] op_sel_hi:[0,1,1]
	v_pk_mul_f32 v[56:57], v[58:59], v[132:133]
	s_waitcnt lgkmcnt(9)
	v_pk_fma_f32 v[54:55], v[120:121], v[130:131], v[54:55]
	v_pk_fma_f32 v[132:133], v[134:135], v[106:107], v[56:57] op_sel_hi:[0,1,1]
	v_pk_fma_f32 v[54:55], v[122:123], v[132:133], v[54:55]
	s_nop 0
	v_add_f32_e32 v50, v54, v55
	v_fma_mix_f32 v42, v69, v42, v50 op_sel:[0,1,0] op_sel_hi:[0,1,0]
	v_fma_mixlo_f16 v42, v42, v46, 0 op_sel:[0,1,0] op_sel_hi:[0,1,0]
	ds_write_b16 v70, v42 offset:13456
	ds_read_b128 v[54:57], v67 offset:1408
	ds_read_b128 v[58:61], v67 offset:1424
	ds_read_b128 v[62:65], v67 offset:1440
	ds_read_b128 v[104:107], v67 offset:1456
	ds_read_b128 v[108:111], v67 offset:1472
	ds_read_b128 v[112:115], v67 offset:1488
	ds_read_b128 v[116:119], v67 offset:1504
	ds_read_b128 v[120:123], v67 offset:1520
	v_cvt_f32_f16_e32 v42, v51
	v_cvt_f32_f16_e32 v46, v43
	v_pk_mul_f32 v[134:135], v[42:43], v[14:15] op_sel_hi:[0,1]
	v_exp_f32_e32 v134, v134
	v_exp_f32_e32 v135, v135
	v_pk_mul_f32 v[142:143], v[42:43], v[16:17] op_sel_hi:[0,1]
	v_exp_f32_e32 v142, v142
	v_exp_f32_e32 v143, v143
	v_mul_f32_e32 v46, v42, v46
	v_pk_mul_f32 v[134:135], v[134:135], v[140:141]
	s_waitcnt lgkmcnt(14)
	v_pk_fma_f32 v[134:135], v[46:47], v[72:73], v[134:135] op_sel_hi:[0,1,1]
	s_waitcnt lgkmcnt(12)
	v_pk_fma_f32 v[72:73], v[88:89], v[134:135], 0 op_sel_hi:[1,1,0]
	v_pk_mul_f32 v[88:89], v[142:143], v[136:137]
	s_nop 0
	v_pk_fma_f32 v[136:137], v[46:47], v[74:75], v[88:89] op_sel_hi:[0,1,1]
	v_pk_mul_f32 v[74:75], v[42:43], v[10:11] op_sel_hi:[0,1]
	v_exp_f32_e32 v74, v74
	v_exp_f32_e32 v75, v75
	v_pk_mul_f32 v[88:89], v[42:43], v[12:13] op_sel_hi:[0,1]
	v_exp_f32_e32 v88, v88
	v_exp_f32_e32 v89, v89
	v_pk_mul_f32 v[74:75], v[74:75], v[138:139]
	v_pk_fma_f32 v[72:73], v[90:91], v[136:137], v[72:73]
	v_pk_fma_f32 v[138:139], v[46:47], v[76:77], v[74:75] op_sel_hi:[0,1,1]
	v_pk_mul_f32 v[74:75], v[88:89], v[124:125]
	v_pk_mul_f32 v[76:77], v[42:43], v[8:9] op_sel_hi:[0,1]
	v_pk_fma_f32 v[124:125], v[46:47], v[78:79], v[74:75] op_sel_hi:[0,1,1]
	v_pk_mul_f32 v[74:75], v[42:43], v[6:7] op_sel_hi:[0,1]
	v_exp_f32_e32 v74, v74
	v_exp_f32_e32 v75, v75
	v_exp_f32_e32 v76, v76
	v_exp_f32_e32 v77, v77
	s_waitcnt lgkmcnt(11)
	v_pk_fma_f32 v[72:73], v[92:93], v[138:139], v[72:73]
	v_pk_mul_f32 v[74:75], v[74:75], v[126:127]
	v_pk_fma_f32 v[72:73], v[94:95], v[124:125], v[72:73]
	v_pk_fma_f32 v[126:127], v[46:47], v[80:81], v[74:75] op_sel_hi:[0,1,1]
	v_pk_mul_f32 v[74:75], v[76:77], v[128:129]
	v_pk_mul_f32 v[76:77], v[42:43], v[4:5] op_sel_hi:[0,1]
	v_pk_fma_f32 v[128:129], v[46:47], v[82:83], v[74:75] op_sel_hi:[0,1,1]
	v_pk_mul_f32 v[74:75], v[42:43], v[2:3] op_sel_hi:[0,1]
	v_exp_f32_e32 v74, v74
	v_exp_f32_e32 v75, v75
	v_exp_f32_e32 v76, v76
	v_exp_f32_e32 v77, v77
	s_waitcnt lgkmcnt(10)
	v_pk_fma_f32 v[72:73], v[96:97], v[126:127], v[72:73]
	v_pk_mul_f32 v[74:75], v[74:75], v[130:131]
	v_pk_fma_f32 v[72:73], v[98:99], v[128:129], v[72:73]
	v_pk_fma_f32 v[130:131], v[46:47], v[84:85], v[74:75] op_sel_hi:[0,1,1]
	v_pk_mul_f32 v[74:75], v[76:77], v[132:133]
	s_waitcnt lgkmcnt(9)
	v_pk_fma_f32 v[72:73], v[100:101], v[130:131], v[72:73]
	v_pk_fma_f32 v[132:133], v[46:47], v[86:87], v[74:75] op_sel_hi:[0,1,1]
	v_pk_fma_f32 v[72:73], v[102:103], v[132:133], v[72:73]
	s_nop 0
	v_add_f32_e32 v42, v72, v73
	v_fma_mix_f32 v42, v69, v43, v42 op_sel_hi:[0,1,0]
	v_fma_mixlo_f16 v42, v42, v47, 0 op_sel_hi:[0,1,0]
	ds_write_b16 v70, v42 offset:14496
	ds_read_b128 v[72:75], v67 offset:1536
	ds_read_b128 v[76:79], v67 offset:1552
	ds_read_b128 v[80:83], v67 offset:1568
	ds_read_b128 v[84:87], v67 offset:1584
	ds_read_b128 v[88:91], v67 offset:1600
	ds_read_b128 v[92:95], v67 offset:1616
	ds_read_b128 v[96:99], v67 offset:1632
	ds_read_b128 v[100:103], v67 offset:1648
	v_cvt_f32_f16_sdwa v42, v51 dst_sel:DWORD dst_unused:UNUSED_PAD src0_sel:WORD_1
	v_cvt_f32_f16_sdwa v46, v43 dst_sel:DWORD dst_unused:UNUSED_PAD src0_sel:WORD_1
	v_pk_mul_f32 v[50:51], v[42:43], v[14:15] op_sel_hi:[0,1]
	v_exp_f32_e32 v50, v50
	v_exp_f32_e32 v51, v51
	v_pk_mul_f32 v[140:141], v[42:43], v[16:17] op_sel_hi:[0,1]
	v_exp_f32_e32 v140, v140
	v_exp_f32_e32 v141, v141
	v_mul_f32_e32 v46, v42, v46
	v_pk_mul_f32 v[50:51], v[50:51], v[134:135]
	s_waitcnt lgkmcnt(14)
	v_pk_fma_f32 v[50:51], v[46:47], v[54:55], v[50:51] op_sel_hi:[0,1,1]
	s_waitcnt lgkmcnt(12)
	v_pk_fma_f32 v[54:55], v[108:109], v[50:51], 0 op_sel_hi:[1,1,0]
	v_pk_mul_f32 v[108:109], v[140:141], v[136:137]
	s_nop 0
	v_pk_fma_f32 v[134:135], v[46:47], v[56:57], v[108:109] op_sel_hi:[0,1,1]
	v_pk_mul_f32 v[56:57], v[42:43], v[10:11] op_sel_hi:[0,1]
	v_exp_f32_e32 v56, v56
	v_exp_f32_e32 v57, v57
	v_pk_mul_f32 v[108:109], v[42:43], v[12:13] op_sel_hi:[0,1]
	v_exp_f32_e32 v108, v108
	v_exp_f32_e32 v109, v109
	v_pk_mul_f32 v[56:57], v[56:57], v[138:139]
	v_pk_fma_f32 v[54:55], v[110:111], v[134:135], v[54:55]
	v_pk_fma_f32 v[136:137], v[46:47], v[58:59], v[56:57] op_sel_hi:[0,1,1]
	v_pk_mul_f32 v[56:57], v[108:109], v[124:125]
	v_pk_mul_f32 v[58:59], v[42:43], v[8:9] op_sel_hi:[0,1]
	v_pk_fma_f32 v[124:125], v[46:47], v[60:61], v[56:57] op_sel_hi:[0,1,1]
	v_pk_mul_f32 v[56:57], v[42:43], v[6:7] op_sel_hi:[0,1]
	v_exp_f32_e32 v56, v56
	v_exp_f32_e32 v57, v57
	v_exp_f32_e32 v58, v58
	v_exp_f32_e32 v59, v59
	s_waitcnt lgkmcnt(11)
	v_pk_fma_f32 v[54:55], v[112:113], v[136:137], v[54:55]
	v_pk_mul_f32 v[56:57], v[56:57], v[126:127]
	v_pk_fma_f32 v[54:55], v[114:115], v[124:125], v[54:55]
	v_pk_fma_f32 v[126:127], v[46:47], v[62:63], v[56:57] op_sel_hi:[0,1,1]
	v_pk_mul_f32 v[56:57], v[58:59], v[128:129]
	v_pk_mul_f32 v[58:59], v[42:43], v[4:5] op_sel_hi:[0,1]
	v_pk_fma_f32 v[128:129], v[46:47], v[64:65], v[56:57] op_sel_hi:[0,1,1]
	v_pk_mul_f32 v[56:57], v[42:43], v[2:3] op_sel_hi:[0,1]
	v_exp_f32_e32 v56, v56
	v_exp_f32_e32 v57, v57
	v_exp_f32_e32 v58, v58
	v_exp_f32_e32 v59, v59
	s_waitcnt lgkmcnt(10)
	v_pk_fma_f32 v[54:55], v[116:117], v[126:127], v[54:55]
	v_pk_mul_f32 v[56:57], v[56:57], v[130:131]
	v_pk_fma_f32 v[54:55], v[118:119], v[128:129], v[54:55]
	v_pk_fma_f32 v[130:131], v[46:47], v[104:105], v[56:57] op_sel_hi:[0,1,1]
	v_pk_mul_f32 v[56:57], v[58:59], v[132:133]
	s_waitcnt lgkmcnt(9)
	v_pk_fma_f32 v[54:55], v[120:121], v[130:131], v[54:55]
	v_pk_fma_f32 v[132:133], v[46:47], v[106:107], v[56:57] op_sel_hi:[0,1,1]
	v_pk_fma_f32 v[54:55], v[122:123], v[132:133], v[54:55]
	s_nop 0
	v_add_f32_e32 v42, v54, v55
	v_fma_mix_f32 v42, v69, v43, v42 op_sel:[0,1,0] op_sel_hi:[0,1,0]
	v_fma_mixlo_f16 v42, v42, v47, 0 op_sel:[0,1,0] op_sel_hi:[0,1,0]
	ds_write_b16 v70, v42 offset:15536
	ds_read_b128 v[54:57], v67 offset:1664
	ds_read_b128 v[58:61], v67 offset:1680
	ds_read_b128 v[62:65], v67 offset:1696
	ds_read_b128 v[104:107], v67 offset:1712
	ds_read_b128 v[108:111], v67 offset:1728
	ds_read_b128 v[112:115], v67 offset:1744
	ds_read_b128 v[116:119], v67 offset:1760
	ds_read_b128 v[120:123], v67 offset:1776
	v_cvt_f32_f16_e32 v42, v52
	v_cvt_f32_f16_e32 v43, v44
	v_pk_mul_f32 v[138:139], v[42:43], v[14:15] op_sel_hi:[0,1]
	v_exp_f32_e32 v138, v138
	v_exp_f32_e32 v139, v139
	v_pk_mul_f32 v[140:141], v[42:43], v[16:17] op_sel_hi:[0,1]
	v_exp_f32_e32 v140, v140
	v_exp_f32_e32 v141, v141
	v_mul_f32_e32 v46, v42, v43
	v_pk_mul_f32 v[50:51], v[138:139], v[50:51]
	s_waitcnt lgkmcnt(14)
	v_pk_fma_f32 v[50:51], v[46:47], v[72:73], v[50:51] op_sel_hi:[0,1,1]
	s_waitcnt lgkmcnt(12)
	v_pk_fma_f32 v[72:73], v[88:89], v[50:51], 0 op_sel_hi:[1,1,0]
	v_pk_mul_f32 v[88:89], v[140:141], v[134:135]
	s_nop 0
	v_pk_fma_f32 v[134:135], v[46:47], v[74:75], v[88:89] op_sel_hi:[0,1,1]
	v_pk_mul_f32 v[74:75], v[42:43], v[10:11] op_sel_hi:[0,1]
	v_exp_f32_e32 v74, v74
	v_exp_f32_e32 v75, v75
	v_pk_mul_f32 v[88:89], v[42:43], v[12:13] op_sel_hi:[0,1]
	v_exp_f32_e32 v88, v88
	v_exp_f32_e32 v89, v89
	v_pk_mul_f32 v[74:75], v[74:75], v[136:137]
	v_pk_fma_f32 v[72:73], v[90:91], v[134:135], v[72:73]
	v_pk_fma_f32 v[136:137], v[46:47], v[76:77], v[74:75] op_sel_hi:[0,1,1]
	v_pk_mul_f32 v[74:75], v[88:89], v[124:125]
	v_pk_mul_f32 v[76:77], v[42:43], v[8:9] op_sel_hi:[0,1]
	v_pk_fma_f32 v[124:125], v[46:47], v[78:79], v[74:75] op_sel_hi:[0,1,1]
	v_pk_mul_f32 v[74:75], v[42:43], v[6:7] op_sel_hi:[0,1]
	v_exp_f32_e32 v74, v74
	v_exp_f32_e32 v75, v75
	v_exp_f32_e32 v76, v76
	v_exp_f32_e32 v77, v77
	s_waitcnt lgkmcnt(11)
	v_pk_fma_f32 v[72:73], v[92:93], v[136:137], v[72:73]
	v_pk_mul_f32 v[74:75], v[74:75], v[126:127]
	v_pk_fma_f32 v[72:73], v[94:95], v[124:125], v[72:73]
	v_pk_fma_f32 v[126:127], v[46:47], v[80:81], v[74:75] op_sel_hi:[0,1,1]
	v_pk_mul_f32 v[74:75], v[76:77], v[128:129]
	s_waitcnt lgkmcnt(10)
	v_pk_fma_f32 v[72:73], v[96:97], v[126:127], v[72:73]
	v_pk_fma_f32 v[128:129], v[46:47], v[82:83], v[74:75] op_sel_hi:[0,1,1]
	v_pk_mul_f32 v[74:75], v[42:43], v[2:3] op_sel_hi:[0,1]
	v_exp_f32_e32 v74, v74
	v_exp_f32_e32 v75, v75
	v_pk_mul_f32 v[42:43], v[42:43], v[4:5] op_sel_hi:[0,1]
	v_exp_f32_e32 v42, v42
	v_exp_f32_e32 v43, v43
	v_pk_mul_f32 v[74:75], v[74:75], v[130:131]
	v_pk_fma_f32 v[72:73], v[98:99], v[128:129], v[72:73]
	v_pk_fma_f32 v[130:131], v[46:47], v[84:85], v[74:75] op_sel_hi:[0,1,1]
	v_pk_mul_f32 v[42:43], v[42:43], v[132:133]
	s_waitcnt lgkmcnt(9)
	v_pk_fma_f32 v[72:73], v[100:101], v[130:131], v[72:73]
	v_pk_fma_f32 v[42:43], v[46:47], v[86:87], v[42:43] op_sel_hi:[0,1,1]
	v_pk_fma_f32 v[46:47], v[102:103], v[42:43], v[72:73]
	s_nop 0
	v_add_f32_e32 v46, v46, v47
	v_fma_mix_f32 v46, v69, v44, v46 op_sel_hi:[0,1,0]
	v_fma_mixlo_f16 v46, v46, v48, 0 op_sel_hi:[0,1,0]
	ds_write_b16 v70, v46 offset:16576
	ds_read_b128 v[72:75], v67 offset:1792
	ds_read_b128 v[76:79], v67 offset:1808
	ds_read_b128 v[80:83], v67 offset:1824
	ds_read_b128 v[84:87], v67 offset:1840
	ds_read_b128 v[88:91], v67 offset:1856
	ds_read_b128 v[92:95], v67 offset:1872
	ds_read_b128 v[96:99], v67 offset:1888
	ds_read_b128 v[100:103], v67 offset:1904
	v_cvt_f32_f16_sdwa v46, v52 dst_sel:DWORD dst_unused:UNUSED_PAD src0_sel:WORD_1
	v_cvt_f32_f16_sdwa v47, v44 dst_sel:DWORD dst_unused:UNUSED_PAD src0_sel:WORD_1
	v_pk_mul_f32 v[132:133], v[46:47], v[14:15] op_sel_hi:[0,1]
	v_exp_f32_e32 v132, v132
	v_exp_f32_e32 v133, v133
	v_pk_mul_f32 v[138:139], v[46:47], v[16:17] op_sel_hi:[0,1]
	v_exp_f32_e32 v138, v138
	v_exp_f32_e32 v139, v139
	v_mul_f32_e32 v52, v46, v47
	v_pk_mul_f32 v[50:51], v[132:133], v[50:51]
	s_waitcnt lgkmcnt(14)
	v_pk_fma_f32 v[50:51], v[52:53], v[54:55], v[50:51] op_sel_hi:[0,1,1]
	s_waitcnt lgkmcnt(12)
	v_pk_fma_f32 v[54:55], v[108:109], v[50:51], 0 op_sel_hi:[1,1,0]
	v_pk_mul_f32 v[108:109], v[138:139], v[134:135]
	s_nop 0
	v_pk_fma_f32 v[132:133], v[52:53], v[56:57], v[108:109] op_sel_hi:[0,1,1]
	v_pk_mul_f32 v[56:57], v[46:47], v[10:11] op_sel_hi:[0,1]
	v_exp_f32_e32 v56, v56
	v_exp_f32_e32 v57, v57
	v_pk_mul_f32 v[108:109], v[46:47], v[12:13] op_sel_hi:[0,1]
	v_exp_f32_e32 v108, v108
	v_exp_f32_e32 v109, v109
	v_pk_mul_f32 v[56:57], v[56:57], v[136:137]
	v_pk_fma_f32 v[54:55], v[110:111], v[132:133], v[54:55]
	v_pk_fma_f32 v[134:135], v[52:53], v[58:59], v[56:57] op_sel_hi:[0,1,1]
	v_pk_mul_f32 v[56:57], v[108:109], v[124:125]
	v_pk_mul_f32 v[58:59], v[46:47], v[8:9] op_sel_hi:[0,1]
	v_pk_fma_f32 v[124:125], v[52:53], v[60:61], v[56:57] op_sel_hi:[0,1,1]
	v_pk_mul_f32 v[56:57], v[46:47], v[6:7] op_sel_hi:[0,1]
	v_exp_f32_e32 v56, v56
	v_exp_f32_e32 v57, v57
	v_exp_f32_e32 v58, v58
	v_exp_f32_e32 v59, v59
	s_waitcnt lgkmcnt(11)
	v_pk_fma_f32 v[54:55], v[112:113], v[134:135], v[54:55]
	v_pk_mul_f32 v[56:57], v[56:57], v[126:127]
	v_pk_fma_f32 v[54:55], v[114:115], v[124:125], v[54:55]
	v_pk_fma_f32 v[126:127], v[52:53], v[62:63], v[56:57] op_sel_hi:[0,1,1]
	v_pk_mul_f32 v[56:57], v[58:59], v[128:129]
	s_waitcnt lgkmcnt(10)
	v_pk_fma_f32 v[54:55], v[116:117], v[126:127], v[54:55]
	v_pk_fma_f32 v[128:129], v[52:53], v[64:65], v[56:57] op_sel_hi:[0,1,1]
	v_pk_mul_f32 v[56:57], v[46:47], v[2:3] op_sel_hi:[0,1]
	v_exp_f32_e32 v56, v56
	v_exp_f32_e32 v57, v57
	v_pk_mul_f32 v[46:47], v[46:47], v[4:5] op_sel_hi:[0,1]
	v_exp_f32_e32 v46, v46
	v_exp_f32_e32 v47, v47
	v_pk_mul_f32 v[56:57], v[56:57], v[130:131]
	v_pk_fma_f32 v[54:55], v[118:119], v[128:129], v[54:55]
	v_pk_fma_f32 v[130:131], v[52:53], v[104:105], v[56:57] op_sel_hi:[0,1,1]
	v_pk_mul_f32 v[42:43], v[46:47], v[42:43]
	s_waitcnt lgkmcnt(9)
	v_pk_fma_f32 v[54:55], v[120:121], v[130:131], v[54:55]
	v_pk_fma_f32 v[42:43], v[52:53], v[106:107], v[42:43] op_sel_hi:[0,1,1]
	v_pk_fma_f32 v[46:47], v[122:123], v[42:43], v[54:55]
	s_nop 0
	v_add_f32_e32 v46, v46, v47
	v_fma_mix_f32 v44, v69, v44, v46 op_sel:[0,1,0] op_sel_hi:[0,1,0]
	v_fma_mixlo_f16 v44, v44, v48, 0 op_sel:[0,1,0] op_sel_hi:[0,1,0]
	ds_write_b16 v70, v44 offset:17616
	ds_read_b128 v[54:57], v67 offset:1920
	ds_read_b128 v[58:61], v67 offset:1936
	ds_read_b128 v[62:65], v67 offset:1952
	ds_read_b128 v[104:107], v67 offset:1968
	ds_read_b128 v[108:111], v67 offset:1984
	ds_read_b128 v[112:115], v67 offset:2000
	ds_read_b128 v[116:119], v67 offset:2016
	ds_read_b128 v[120:123], v67 offset:2032
	v_cvt_f32_f16_e32 v44, v53
	v_cvt_f32_f16_e32 v46, v45
	v_pk_mul_f32 v[136:137], v[44:45], v[14:15] op_sel_hi:[0,1]
	v_exp_f32_e32 v136, v136
	v_exp_f32_e32 v137, v137
	v_pk_mul_f32 v[138:139], v[44:45], v[16:17] op_sel_hi:[0,1]
	v_exp_f32_e32 v138, v138
	v_exp_f32_e32 v139, v139
	v_mul_f32_e32 v46, v44, v46
	v_pk_mul_f32 v[50:51], v[136:137], v[50:51]
	s_waitcnt lgkmcnt(14)
	v_pk_fma_f32 v[50:51], v[46:47], v[72:73], v[50:51] op_sel_hi:[0,1,1]
	s_waitcnt lgkmcnt(12)
	v_pk_fma_f32 v[72:73], v[88:89], v[50:51], 0 op_sel_hi:[1,1,0]
	v_pk_mul_f32 v[88:89], v[138:139], v[132:133]
	s_nop 0
	v_pk_fma_f32 v[132:133], v[46:47], v[74:75], v[88:89] op_sel_hi:[0,1,1]
	v_pk_mul_f32 v[74:75], v[44:45], v[10:11] op_sel_hi:[0,1]
	v_exp_f32_e32 v74, v74
	v_exp_f32_e32 v75, v75
	v_pk_mul_f32 v[88:89], v[44:45], v[12:13] op_sel_hi:[0,1]
	v_exp_f32_e32 v88, v88
	v_exp_f32_e32 v89, v89
	v_pk_mul_f32 v[74:75], v[74:75], v[134:135]
	v_pk_fma_f32 v[72:73], v[90:91], v[132:133], v[72:73]
	v_pk_fma_f32 v[134:135], v[46:47], v[76:77], v[74:75] op_sel_hi:[0,1,1]
	v_pk_mul_f32 v[74:75], v[88:89], v[124:125]
	v_pk_mul_f32 v[76:77], v[44:45], v[8:9] op_sel_hi:[0,1]
	v_pk_fma_f32 v[124:125], v[46:47], v[78:79], v[74:75] op_sel_hi:[0,1,1]
	v_pk_mul_f32 v[74:75], v[44:45], v[6:7] op_sel_hi:[0,1]
	v_exp_f32_e32 v74, v74
	v_exp_f32_e32 v75, v75
	v_exp_f32_e32 v76, v76
	v_exp_f32_e32 v77, v77
	s_waitcnt lgkmcnt(11)
	v_pk_fma_f32 v[72:73], v[92:93], v[134:135], v[72:73]
	v_pk_mul_f32 v[74:75], v[74:75], v[126:127]
	v_pk_fma_f32 v[72:73], v[94:95], v[124:125], v[72:73]
	v_pk_fma_f32 v[126:127], v[46:47], v[80:81], v[74:75] op_sel_hi:[0,1,1]
	v_pk_mul_f32 v[74:75], v[76:77], v[128:129]
	v_pk_mul_f32 v[76:77], v[44:45], v[4:5] op_sel_hi:[0,1]
	v_pk_fma_f32 v[128:129], v[46:47], v[82:83], v[74:75] op_sel_hi:[0,1,1]
	v_pk_mul_f32 v[74:75], v[44:45], v[2:3] op_sel_hi:[0,1]
	v_exp_f32_e32 v74, v74
	v_exp_f32_e32 v75, v75
	v_exp_f32_e32 v76, v76
	v_exp_f32_e32 v77, v77
	s_waitcnt lgkmcnt(10)
	v_pk_fma_f32 v[72:73], v[96:97], v[126:127], v[72:73]
	v_pk_mul_f32 v[74:75], v[74:75], v[130:131]
	v_pk_fma_f32 v[72:73], v[98:99], v[128:129], v[72:73]
	v_pk_fma_f32 v[130:131], v[46:47], v[84:85], v[74:75] op_sel_hi:[0,1,1]
	v_pk_mul_f32 v[42:43], v[76:77], v[42:43]
	s_waitcnt lgkmcnt(9)
	v_pk_fma_f32 v[72:73], v[100:101], v[130:131], v[72:73]
	v_pk_fma_f32 v[42:43], v[46:47], v[86:87], v[42:43] op_sel_hi:[0,1,1]
	v_pk_fma_f32 v[46:47], v[102:103], v[42:43], v[72:73]
	s_nop 0
	v_add_f32_e32 v44, v46, v47
	v_fma_mix_f32 v44, v69, v45, v44 op_sel_hi:[0,1,0]
	v_fma_mixlo_f16 v44, v44, v49, 0 op_sel_hi:[0,1,0]
	ds_write_b16 v70, v44 offset:18656
	ds_read_b128 v[72:75], v67 offset:2048
	ds_read_b128 v[76:79], v67 offset:2064
	ds_read_b128 v[80:83], v67 offset:2080
	ds_read_b128 v[84:87], v67 offset:2096
	ds_read_b128 v[88:91], v67 offset:2112
	ds_read_b128 v[92:95], v67 offset:2128
	ds_read_b128 v[96:99], v67 offset:2144
	ds_read_b128 v[100:103], v67 offset:2160
	v_cvt_f32_f16_sdwa v44, v53 dst_sel:DWORD dst_unused:UNUSED_PAD src0_sel:WORD_1
	v_cvt_f32_f16_sdwa v46, v45 dst_sel:DWORD dst_unused:UNUSED_PAD src0_sel:WORD_1
	v_pk_mul_f32 v[52:53], v[44:45], v[14:15] op_sel_hi:[0,1]
	v_pk_mul_f32 v[136:137], v[44:45], v[16:17] op_sel_hi:[0,1]
	v_exp_f32_e32 v52, v52
	v_exp_f32_e32 v53, v53
	v_exp_f32_e32 v136, v136
	v_exp_f32_e32 v137, v137
	v_mul_f32_e32 v46, v44, v46
	v_pk_mul_f32 v[50:51], v[52:53], v[50:51]
	v_pk_mul_f32 v[52:53], v[136:137], v[132:133]
	s_waitcnt lgkmcnt(14)
	v_pk_fma_f32 v[132:133], v[46:47], v[56:57], v[52:53] op_sel_hi:[0,1,1]
	v_pk_mul_f32 v[52:53], v[44:45], v[10:11] op_sel_hi:[0,1]
	v_pk_fma_f32 v[138:139], v[46:47], v[54:55], v[50:51] op_sel_hi:[0,1,1]
	v_exp_f32_e32 v52, v52
	v_exp_f32_e32 v53, v53
	v_pk_mul_f32 v[54:55], v[44:45], v[12:13] op_sel_hi:[0,1]
	v_exp_f32_e32 v54, v54
	v_exp_f32_e32 v55, v55
	s_waitcnt lgkmcnt(12)
	v_pk_fma_f32 v[50:51], v[108:109], v[138:139], 0 op_sel_hi:[1,1,0]
	v_pk_mul_f32 v[52:53], v[52:53], v[134:135]
	v_pk_fma_f32 v[50:51], v[110:111], v[132:133], v[50:51]
	v_pk_fma_f32 v[134:135], v[46:47], v[58:59], v[52:53] op_sel_hi:[0,1,1]
	v_pk_mul_f32 v[52:53], v[54:55], v[124:125]
	s_waitcnt lgkmcnt(11)
	v_pk_fma_f32 v[50:51], v[112:113], v[134:135], v[50:51]
	v_pk_fma_f32 v[112:113], v[46:47], v[60:61], v[52:53] op_sel_hi:[0,1,1]
	v_pk_mul_f32 v[52:53], v[44:45], v[6:7] op_sel_hi:[0,1]
	v_exp_f32_e32 v52, v52
	v_exp_f32_e32 v53, v53
	v_pk_mul_f32 v[54:55], v[44:45], v[8:9] op_sel_hi:[0,1]
	v_exp_f32_e32 v54, v54
	v_exp_f32_e32 v55, v55
	v_pk_mul_f32 v[52:53], v[52:53], v[126:127]
	v_pk_fma_f32 v[50:51], v[114:115], v[112:113], v[50:51]
	v_pk_fma_f32 v[114:115], v[46:47], v[62:63], v[52:53] op_sel_hi:[0,1,1]
	v_pk_mul_f32 v[52:53], v[54:55], v[128:129]
	s_waitcnt lgkmcnt(10)
	v_pk_fma_f32 v[50:51], v[116:117], v[114:115], v[50:51]
	v_pk_fma_f32 v[116:117], v[46:47], v[64:65], v[52:53] op_sel_hi:[0,1,1]
	v_pk_mul_f32 v[52:53], v[44:45], v[2:3] op_sel_hi:[0,1]
	v_exp_f32_e32 v52, v52
	v_exp_f32_e32 v53, v53
	v_pk_mul_f32 v[54:55], v[44:45], v[4:5] op_sel_hi:[0,1]
	v_exp_f32_e32 v54, v54
	v_exp_f32_e32 v55, v55
	v_pk_mul_f32 v[52:53], v[52:53], v[130:131]
	v_pk_fma_f32 v[50:51], v[118:119], v[116:117], v[50:51]
	v_pk_fma_f32 v[118:119], v[46:47], v[104:105], v[52:53] op_sel_hi:[0,1,1]
	v_pk_mul_f32 v[42:43], v[54:55], v[42:43]
	s_waitcnt lgkmcnt(9)
	v_pk_fma_f32 v[50:51], v[120:121], v[118:119], v[50:51]
	v_pk_fma_f32 v[120:121], v[46:47], v[106:107], v[42:43] op_sel_hi:[0,1,1]
	v_pk_fma_f32 v[42:43], v[122:123], v[120:121], v[50:51]
	s_nop 0
	v_add_f32_e32 v42, v42, v43
	v_fma_mix_f32 v42, v69, v45, v42 op_sel:[0,1,0] op_sel_hi:[0,1,0]
	v_fma_mixlo_f16 v42, v42, v49, 0 op_sel:[0,1,0] op_sel_hi:[0,1,0]
	ds_write_b16 v70, v42 offset:19696
	ds_read_b128 v[42:45], v67 offset:2176
	ds_read_b128 v[46:49], v67 offset:2192
	ds_read_b128 v[50:53], v67 offset:2208
	ds_read_b128 v[54:57], v67 offset:2224
	ds_read_b128 v[58:61], v67 offset:2240
	ds_read_b128 v[62:65], v67 offset:2256
	ds_read_b128 v[104:107], v67 offset:2272
	ds_read_b128 v[108:111], v67 offset:2288
	s_waitcnt vmcnt(5)
	v_cvt_f32_f16_e32 v122, v38
	s_waitcnt vmcnt(4)
	v_cvt_f32_f16_e32 v71, v30
	v_pk_mul_f32 v[126:127], v[122:123], v[14:15] op_sel_hi:[0,1]
	v_exp_f32_e32 v126, v126
	v_exp_f32_e32 v127, v127
	v_pk_mul_f32 v[128:129], v[122:123], v[16:17] op_sel_hi:[0,1]
	v_exp_f32_e32 v128, v128
	v_exp_f32_e32 v129, v129
	v_mul_f32_e32 v124, v122, v71
	v_pk_mul_f32 v[126:127], v[126:127], v[138:139]
	s_waitcnt lgkmcnt(14)
	v_pk_fma_f32 v[126:127], v[124:125], v[72:73], v[126:127] op_sel_hi:[0,1,1]
	s_waitcnt lgkmcnt(12)
	v_pk_fma_f32 v[72:73], v[88:89], v[126:127], 0 op_sel_hi:[1,1,0]
	v_pk_mul_f32 v[88:89], v[128:129], v[132:133]
	s_nop 0
	v_pk_fma_f32 v[128:129], v[124:125], v[74:75], v[88:89] op_sel_hi:[0,1,1]
	v_pk_mul_f32 v[74:75], v[122:123], v[10:11] op_sel_hi:[0,1]
	v_exp_f32_e32 v74, v74
	v_exp_f32_e32 v75, v75
	v_pk_mul_f32 v[88:89], v[122:123], v[12:13] op_sel_hi:[0,1]
	v_exp_f32_e32 v88, v88
	v_exp_f32_e32 v89, v89
	v_pk_mul_f32 v[74:75], v[74:75], v[134:135]
	v_pk_fma_f32 v[72:73], v[90:91], v[128:129], v[72:73]
	v_pk_fma_f32 v[130:131], v[124:125], v[76:77], v[74:75] op_sel_hi:[0,1,1]
	v_pk_mul_f32 v[74:75], v[88:89], v[112:113]
	v_pk_mul_f32 v[76:77], v[122:123], v[8:9] op_sel_hi:[0,1]
	v_pk_fma_f32 v[112:113], v[124:125], v[78:79], v[74:75] op_sel_hi:[0,1,1]
	v_pk_mul_f32 v[74:75], v[122:123], v[6:7] op_sel_hi:[0,1]
	v_exp_f32_e32 v74, v74
	v_exp_f32_e32 v75, v75
	v_exp_f32_e32 v76, v76
	v_exp_f32_e32 v77, v77
	s_waitcnt lgkmcnt(11)
	v_pk_fma_f32 v[72:73], v[92:93], v[130:131], v[72:73]
	v_pk_mul_f32 v[74:75], v[74:75], v[114:115]
	v_pk_fma_f32 v[72:73], v[94:95], v[112:113], v[72:73]
	v_pk_fma_f32 v[114:115], v[124:125], v[80:81], v[74:75] op_sel_hi:[0,1,1]
	v_pk_mul_f32 v[74:75], v[76:77], v[116:117]
	v_pk_mul_f32 v[76:77], v[122:123], v[4:5] op_sel_hi:[0,1]
	v_pk_fma_f32 v[116:117], v[124:125], v[82:83], v[74:75] op_sel_hi:[0,1,1]
	v_pk_mul_f32 v[74:75], v[122:123], v[2:3] op_sel_hi:[0,1]
	v_exp_f32_e32 v74, v74
	v_exp_f32_e32 v75, v75
	v_exp_f32_e32 v76, v76
	v_exp_f32_e32 v77, v77
	s_waitcnt lgkmcnt(10)
	v_pk_fma_f32 v[72:73], v[96:97], v[114:115], v[72:73]
	v_pk_mul_f32 v[74:75], v[74:75], v[118:119]
	v_pk_fma_f32 v[72:73], v[98:99], v[116:117], v[72:73]
	v_pk_fma_f32 v[118:119], v[124:125], v[84:85], v[74:75] op_sel_hi:[0,1,1]
	v_pk_mul_f32 v[74:75], v[76:77], v[120:121]
	s_waitcnt lgkmcnt(9)
	v_pk_fma_f32 v[72:73], v[100:101], v[118:119], v[72:73]
	v_pk_fma_f32 v[120:121], v[124:125], v[86:87], v[74:75] op_sel_hi:[0,1,1]
	v_pk_fma_f32 v[72:73], v[102:103], v[120:121], v[72:73]
	s_nop 0
	v_add_f32_e32 v71, v72, v73
	v_fma_mix_f32 v71, v69, v30, v71 op_sel_hi:[0,1,0]
	s_waitcnt vmcnt(3)
	v_fma_mixlo_f16 v71, v71, v34, 0 op_sel_hi:[0,1,0]
	ds_write_b16 v70, v71 offset:20736
	ds_read_b128 v[72:75], v67 offset:2304
	ds_read_b128 v[76:79], v67 offset:2320
	ds_read_b128 v[80:83], v67 offset:2336
	ds_read_b128 v[84:87], v67 offset:2352
	ds_read_b128 v[88:91], v67 offset:2368
	ds_read_b128 v[92:95], v67 offset:2384
	ds_read_b128 v[96:99], v67 offset:2400
	ds_read_b128 v[100:103], v67 offset:2416
	v_cvt_f32_f16_sdwa v38, v38 dst_sel:DWORD dst_unused:UNUSED_PAD src0_sel:WORD_1
	v_cvt_f32_f16_sdwa v71, v30 dst_sel:DWORD dst_unused:UNUSED_PAD src0_sel:WORD_1
	v_pk_mul_f32 v[124:125], v[38:39], v[14:15] op_sel_hi:[0,1]
	v_exp_f32_e32 v124, v124
	v_exp_f32_e32 v125, v125
	v_pk_mul_f32 v[132:133], v[38:39], v[16:17] op_sel_hi:[0,1]
	v_exp_f32_e32 v132, v132
	v_exp_f32_e32 v133, v133
	v_mul_f32_e32 v122, v38, v71
	v_pk_mul_f32 v[124:125], v[124:125], v[126:127]
	s_waitcnt lgkmcnt(14)
	v_pk_fma_f32 v[124:125], v[122:123], v[42:43], v[124:125] op_sel_hi:[0,1,1]
	s_waitcnt lgkmcnt(12)
	v_pk_fma_f32 v[42:43], v[58:59], v[124:125], 0 op_sel_hi:[1,1,0]
	v_pk_mul_f32 v[58:59], v[132:133], v[128:129]
	s_nop 0
	v_pk_fma_f32 v[126:127], v[122:123], v[44:45], v[58:59] op_sel_hi:[0,1,1]
	v_pk_mul_f32 v[44:45], v[38:39], v[10:11] op_sel_hi:[0,1]
	v_exp_f32_e32 v44, v44
	v_exp_f32_e32 v45, v45
	v_pk_mul_f32 v[58:59], v[38:39], v[12:13] op_sel_hi:[0,1]
	v_exp_f32_e32 v58, v58
	v_exp_f32_e32 v59, v59
	v_pk_mul_f32 v[44:45], v[44:45], v[130:131]
	v_pk_fma_f32 v[42:43], v[60:61], v[126:127], v[42:43]
	v_pk_fma_f32 v[128:129], v[122:123], v[46:47], v[44:45] op_sel_hi:[0,1,1]
	v_pk_mul_f32 v[44:45], v[58:59], v[112:113]
	v_pk_mul_f32 v[46:47], v[38:39], v[8:9] op_sel_hi:[0,1]
	v_pk_fma_f32 v[112:113], v[122:123], v[48:49], v[44:45] op_sel_hi:[0,1,1]
	v_pk_mul_f32 v[44:45], v[38:39], v[6:7] op_sel_hi:[0,1]
	v_exp_f32_e32 v44, v44
	v_exp_f32_e32 v45, v45
	v_exp_f32_e32 v46, v46
	v_exp_f32_e32 v47, v47
	s_waitcnt lgkmcnt(11)
	v_pk_fma_f32 v[42:43], v[62:63], v[128:129], v[42:43]
	v_pk_mul_f32 v[44:45], v[44:45], v[114:115]
	v_pk_fma_f32 v[42:43], v[64:65], v[112:113], v[42:43]
	v_pk_fma_f32 v[114:115], v[122:123], v[50:51], v[44:45] op_sel_hi:[0,1,1]
	v_pk_mul_f32 v[44:45], v[46:47], v[116:117]
	v_pk_mul_f32 v[46:47], v[38:39], v[4:5] op_sel_hi:[0,1]
	v_pk_fma_f32 v[116:117], v[122:123], v[52:53], v[44:45] op_sel_hi:[0,1,1]
	v_pk_mul_f32 v[44:45], v[38:39], v[2:3] op_sel_hi:[0,1]
	v_exp_f32_e32 v44, v44
	v_exp_f32_e32 v45, v45
	v_exp_f32_e32 v46, v46
	v_exp_f32_e32 v47, v47
	s_waitcnt lgkmcnt(10)
	v_pk_fma_f32 v[42:43], v[104:105], v[114:115], v[42:43]
	v_pk_mul_f32 v[44:45], v[44:45], v[118:119]
	v_pk_fma_f32 v[42:43], v[106:107], v[116:117], v[42:43]
	v_pk_fma_f32 v[118:119], v[122:123], v[54:55], v[44:45] op_sel_hi:[0,1,1]
	v_pk_mul_f32 v[44:45], v[46:47], v[120:121]
	s_waitcnt lgkmcnt(9)
	v_pk_fma_f32 v[42:43], v[108:109], v[118:119], v[42:43]
	v_pk_fma_f32 v[120:121], v[122:123], v[56:57], v[44:45] op_sel_hi:[0,1,1]
	v_pk_fma_f32 v[42:43], v[110:111], v[120:121], v[42:43]
	s_nop 0
	v_add_f32_e32 v38, v42, v43
	v_fma_mix_f32 v30, v69, v30, v38 op_sel:[0,1,0] op_sel_hi:[0,1,0]
	v_fma_mixlo_f16 v30, v30, v34, 0 op_sel:[0,1,0] op_sel_hi:[0,1,0]
	ds_write_b16 v70, v30 offset:21776
	ds_read_b128 v[42:45], v67 offset:2432
	ds_read_b128 v[46:49], v67 offset:2448
	ds_read_b128 v[50:53], v67 offset:2464
	ds_read_b128 v[54:57], v67 offset:2480
	ds_read_b128 v[58:61], v67 offset:2496
	ds_read_b128 v[62:65], v67 offset:2512
	ds_read_b128 v[104:107], v67 offset:2528
	ds_read_b128 v[108:111], v67 offset:2544
	v_cvt_f32_f16_e32 v30, v39
	v_cvt_f32_f16_e32 v34, v31
	v_pk_mul_f32 v[122:123], v[30:31], v[14:15] op_sel_hi:[0,1]
	v_exp_f32_e32 v122, v122
	v_exp_f32_e32 v123, v123
	v_pk_mul_f32 v[130:131], v[30:31], v[16:17] op_sel_hi:[0,1]
	v_exp_f32_e32 v130, v130
	v_exp_f32_e32 v131, v131
	v_mul_f32_e32 v34, v30, v34
	v_pk_mul_f32 v[122:123], v[122:123], v[124:125]
	s_waitcnt lgkmcnt(14)
	v_pk_fma_f32 v[122:123], v[34:35], v[72:73], v[122:123] op_sel_hi:[0,1,1]
	s_waitcnt lgkmcnt(12)
	v_pk_fma_f32 v[72:73], v[88:89], v[122:123], 0 op_sel_hi:[1,1,0]
	v_pk_mul_f32 v[88:89], v[130:131], v[126:127]
	s_nop 0
	v_pk_fma_f32 v[124:125], v[34:35], v[74:75], v[88:89] op_sel_hi:[0,1,1]
	v_pk_mul_f32 v[74:75], v[30:31], v[10:11] op_sel_hi:[0,1]
	v_exp_f32_e32 v74, v74
	v_exp_f32_e32 v75, v75
	v_pk_mul_f32 v[88:89], v[30:31], v[12:13] op_sel_hi:[0,1]
	v_exp_f32_e32 v88, v88
	v_exp_f32_e32 v89, v89
	v_pk_mul_f32 v[74:75], v[74:75], v[128:129]
	v_pk_fma_f32 v[72:73], v[90:91], v[124:125], v[72:73]
	v_pk_fma_f32 v[126:127], v[34:35], v[76:77], v[74:75] op_sel_hi:[0,1,1]
	v_pk_mul_f32 v[74:75], v[88:89], v[112:113]
	v_pk_mul_f32 v[76:77], v[30:31], v[8:9] op_sel_hi:[0,1]
	v_pk_fma_f32 v[112:113], v[34:35], v[78:79], v[74:75] op_sel_hi:[0,1,1]
	v_pk_mul_f32 v[74:75], v[30:31], v[6:7] op_sel_hi:[0,1]
	v_exp_f32_e32 v74, v74
	v_exp_f32_e32 v75, v75
	v_exp_f32_e32 v76, v76
	v_exp_f32_e32 v77, v77
	s_waitcnt lgkmcnt(11)
	v_pk_fma_f32 v[72:73], v[92:93], v[126:127], v[72:73]
	v_pk_mul_f32 v[74:75], v[74:75], v[114:115]
	v_pk_fma_f32 v[72:73], v[94:95], v[112:113], v[72:73]
	v_pk_fma_f32 v[114:115], v[34:35], v[80:81], v[74:75] op_sel_hi:[0,1,1]
	v_pk_mul_f32 v[74:75], v[76:77], v[116:117]
	v_pk_mul_f32 v[76:77], v[30:31], v[4:5] op_sel_hi:[0,1]
	v_pk_fma_f32 v[116:117], v[34:35], v[82:83], v[74:75] op_sel_hi:[0,1,1]
	v_pk_mul_f32 v[74:75], v[30:31], v[2:3] op_sel_hi:[0,1]
	v_exp_f32_e32 v74, v74
	v_exp_f32_e32 v75, v75
	v_exp_f32_e32 v76, v76
	v_exp_f32_e32 v77, v77
	s_waitcnt lgkmcnt(10)
	v_pk_fma_f32 v[72:73], v[96:97], v[114:115], v[72:73]
	v_pk_mul_f32 v[74:75], v[74:75], v[118:119]
	v_pk_fma_f32 v[72:73], v[98:99], v[116:117], v[72:73]
	v_pk_fma_f32 v[118:119], v[34:35], v[84:85], v[74:75] op_sel_hi:[0,1,1]
	v_pk_mul_f32 v[74:75], v[76:77], v[120:121]
	s_waitcnt lgkmcnt(9)
	v_pk_fma_f32 v[72:73], v[100:101], v[118:119], v[72:73]
	v_pk_fma_f32 v[120:121], v[34:35], v[86:87], v[74:75] op_sel_hi:[0,1,1]
	v_pk_fma_f32 v[72:73], v[102:103], v[120:121], v[72:73]
	s_nop 0
	v_add_f32_e32 v30, v72, v73
	v_fma_mix_f32 v30, v69, v31, v30 op_sel_hi:[0,1,0]
	v_fma_mixlo_f16 v30, v30, v35, 0 op_sel_hi:[0,1,0]
	ds_write_b16 v70, v30 offset:22816
	ds_read_b128 v[72:75], v67 offset:2560
	ds_read_b128 v[76:79], v67 offset:2576
	ds_read_b128 v[80:83], v67 offset:2592
	ds_read_b128 v[84:87], v67 offset:2608
	ds_read_b128 v[88:91], v67 offset:2624
	ds_read_b128 v[92:95], v67 offset:2640
	ds_read_b128 v[96:99], v67 offset:2656
	ds_read_b128 v[100:103], v67 offset:2672
	v_cvt_f32_f16_sdwa v30, v39 dst_sel:DWORD dst_unused:UNUSED_PAD src0_sel:WORD_1
	v_cvt_f32_f16_sdwa v34, v31 dst_sel:DWORD dst_unused:UNUSED_PAD src0_sel:WORD_1
	v_pk_mul_f32 v[38:39], v[30:31], v[14:15] op_sel_hi:[0,1]
	v_exp_f32_e32 v38, v38
	v_exp_f32_e32 v39, v39
	v_pk_mul_f32 v[128:129], v[30:31], v[16:17] op_sel_hi:[0,1]
	v_exp_f32_e32 v128, v128
	v_exp_f32_e32 v129, v129
	v_mul_f32_e32 v34, v30, v34
	v_pk_mul_f32 v[38:39], v[38:39], v[122:123]
	s_waitcnt lgkmcnt(14)
	v_pk_fma_f32 v[38:39], v[34:35], v[42:43], v[38:39] op_sel_hi:[0,1,1]
	s_waitcnt lgkmcnt(12)
	v_pk_fma_f32 v[42:43], v[58:59], v[38:39], 0 op_sel_hi:[1,1,0]
	v_pk_mul_f32 v[58:59], v[128:129], v[124:125]
	s_nop 0
	v_pk_fma_f32 v[122:123], v[34:35], v[44:45], v[58:59] op_sel_hi:[0,1,1]
	v_pk_mul_f32 v[44:45], v[30:31], v[10:11] op_sel_hi:[0,1]
	v_exp_f32_e32 v44, v44
	v_exp_f32_e32 v45, v45
	v_pk_mul_f32 v[58:59], v[30:31], v[12:13] op_sel_hi:[0,1]
	v_exp_f32_e32 v58, v58
	v_exp_f32_e32 v59, v59
	v_pk_mul_f32 v[44:45], v[44:45], v[126:127]
	v_pk_fma_f32 v[42:43], v[60:61], v[122:123], v[42:43]
	v_pk_fma_f32 v[124:125], v[34:35], v[46:47], v[44:45] op_sel_hi:[0,1,1]
	v_pk_mul_f32 v[44:45], v[58:59], v[112:113]
	v_pk_mul_f32 v[46:47], v[30:31], v[8:9] op_sel_hi:[0,1]
	v_pk_fma_f32 v[112:113], v[34:35], v[48:49], v[44:45] op_sel_hi:[0,1,1]
	v_pk_mul_f32 v[44:45], v[30:31], v[6:7] op_sel_hi:[0,1]
	v_exp_f32_e32 v44, v44
	v_exp_f32_e32 v45, v45
	v_exp_f32_e32 v46, v46
	v_exp_f32_e32 v47, v47
	s_waitcnt lgkmcnt(11)
	v_pk_fma_f32 v[42:43], v[62:63], v[124:125], v[42:43]
	v_pk_mul_f32 v[44:45], v[44:45], v[114:115]
	v_pk_fma_f32 v[42:43], v[64:65], v[112:113], v[42:43]
	v_pk_fma_f32 v[114:115], v[34:35], v[50:51], v[44:45] op_sel_hi:[0,1,1]
	v_pk_mul_f32 v[44:45], v[46:47], v[116:117]
	v_pk_mul_f32 v[46:47], v[30:31], v[4:5] op_sel_hi:[0,1]
	v_pk_fma_f32 v[116:117], v[34:35], v[52:53], v[44:45] op_sel_hi:[0,1,1]
	v_pk_mul_f32 v[44:45], v[30:31], v[2:3] op_sel_hi:[0,1]
	v_exp_f32_e32 v44, v44
	v_exp_f32_e32 v45, v45
	v_exp_f32_e32 v46, v46
	v_exp_f32_e32 v47, v47
	s_waitcnt lgkmcnt(10)
	v_pk_fma_f32 v[42:43], v[104:105], v[114:115], v[42:43]
	v_pk_mul_f32 v[44:45], v[44:45], v[118:119]
	v_pk_fma_f32 v[42:43], v[106:107], v[116:117], v[42:43]
	v_pk_fma_f32 v[118:119], v[34:35], v[54:55], v[44:45] op_sel_hi:[0,1,1]
	v_pk_mul_f32 v[44:45], v[46:47], v[120:121]
	s_waitcnt lgkmcnt(9)
	v_pk_fma_f32 v[42:43], v[108:109], v[118:119], v[42:43]
	v_pk_fma_f32 v[120:121], v[34:35], v[56:57], v[44:45] op_sel_hi:[0,1,1]
	v_pk_fma_f32 v[42:43], v[110:111], v[120:121], v[42:43]
	s_nop 0
	v_add_f32_e32 v30, v42, v43
	v_fma_mix_f32 v30, v69, v31, v30 op_sel:[0,1,0] op_sel_hi:[0,1,0]
	v_fma_mixlo_f16 v30, v30, v35, 0 op_sel:[0,1,0] op_sel_hi:[0,1,0]
	ds_write_b16 v70, v30 offset:23856
	ds_read_b128 v[42:45], v67 offset:2688
	ds_read_b128 v[46:49], v67 offset:2704
	ds_read_b128 v[50:53], v67 offset:2720
	ds_read_b128 v[54:57], v67 offset:2736
	ds_read_b128 v[58:61], v67 offset:2752
	ds_read_b128 v[62:65], v67 offset:2768
	ds_read_b128 v[104:107], v67 offset:2784
	ds_read_b128 v[108:111], v67 offset:2800
	v_cvt_f32_f16_e32 v30, v40
	v_cvt_f32_f16_e32 v31, v32
	v_pk_mul_f32 v[126:127], v[30:31], v[14:15] op_sel_hi:[0,1]
	v_exp_f32_e32 v126, v126
	v_exp_f32_e32 v127, v127
	v_pk_mul_f32 v[128:129], v[30:31], v[16:17] op_sel_hi:[0,1]
	v_exp_f32_e32 v128, v128
	v_exp_f32_e32 v129, v129
	v_mul_f32_e32 v34, v30, v31
	v_pk_mul_f32 v[38:39], v[126:127], v[38:39]
	s_waitcnt lgkmcnt(14)
	v_pk_fma_f32 v[38:39], v[34:35], v[72:73], v[38:39] op_sel_hi:[0,1,1]
	s_waitcnt lgkmcnt(12)
	v_pk_fma_f32 v[72:73], v[88:89], v[38:39], 0 op_sel_hi:[1,1,0]
	v_pk_mul_f32 v[88:89], v[128:129], v[122:123]
	s_nop 0
	v_pk_fma_f32 v[122:123], v[34:35], v[74:75], v[88:89] op_sel_hi:[0,1,1]
	v_pk_mul_f32 v[74:75], v[30:31], v[10:11] op_sel_hi:[0,1]
	v_exp_f32_e32 v74, v74
	v_exp_f32_e32 v75, v75
	v_pk_mul_f32 v[88:89], v[30:31], v[12:13] op_sel_hi:[0,1]
	v_exp_f32_e32 v88, v88
	v_exp_f32_e32 v89, v89
	v_pk_mul_f32 v[74:75], v[74:75], v[124:125]
	v_pk_fma_f32 v[72:73], v[90:91], v[122:123], v[72:73]
	v_pk_fma_f32 v[124:125], v[34:35], v[76:77], v[74:75] op_sel_hi:[0,1,1]
	v_pk_mul_f32 v[74:75], v[88:89], v[112:113]
	v_pk_mul_f32 v[76:77], v[30:31], v[8:9] op_sel_hi:[0,1]
	v_pk_fma_f32 v[112:113], v[34:35], v[78:79], v[74:75] op_sel_hi:[0,1,1]
	v_pk_mul_f32 v[74:75], v[30:31], v[6:7] op_sel_hi:[0,1]
	v_exp_f32_e32 v74, v74
	v_exp_f32_e32 v75, v75
	v_exp_f32_e32 v76, v76
	v_exp_f32_e32 v77, v77
	s_waitcnt lgkmcnt(11)
	v_pk_fma_f32 v[72:73], v[92:93], v[124:125], v[72:73]
	v_pk_mul_f32 v[74:75], v[74:75], v[114:115]
	v_pk_fma_f32 v[72:73], v[94:95], v[112:113], v[72:73]
	v_pk_fma_f32 v[114:115], v[34:35], v[80:81], v[74:75] op_sel_hi:[0,1,1]
	v_pk_mul_f32 v[74:75], v[76:77], v[116:117]
	s_waitcnt lgkmcnt(10)
	v_pk_fma_f32 v[72:73], v[96:97], v[114:115], v[72:73]
	v_pk_fma_f32 v[116:117], v[34:35], v[82:83], v[74:75] op_sel_hi:[0,1,1]
	v_pk_mul_f32 v[74:75], v[30:31], v[2:3] op_sel_hi:[0,1]
	v_exp_f32_e32 v74, v74
	v_exp_f32_e32 v75, v75
	v_pk_mul_f32 v[30:31], v[30:31], v[4:5] op_sel_hi:[0,1]
	v_exp_f32_e32 v30, v30
	v_exp_f32_e32 v31, v31
	v_pk_mul_f32 v[74:75], v[74:75], v[118:119]
	v_pk_fma_f32 v[72:73], v[98:99], v[116:117], v[72:73]
	v_pk_fma_f32 v[118:119], v[34:35], v[84:85], v[74:75] op_sel_hi:[0,1,1]
	v_pk_mul_f32 v[30:31], v[30:31], v[120:121]
	s_waitcnt lgkmcnt(9)
	v_pk_fma_f32 v[72:73], v[100:101], v[118:119], v[72:73]
	v_pk_fma_f32 v[30:31], v[34:35], v[86:87], v[30:31] op_sel_hi:[0,1,1]
	v_pk_fma_f32 v[34:35], v[102:103], v[30:31], v[72:73]
	s_nop 0
	v_add_f32_e32 v34, v34, v35
	v_fma_mix_f32 v34, v69, v32, v34 op_sel_hi:[0,1,0]
	v_fma_mixlo_f16 v34, v34, v36, 0 op_sel_hi:[0,1,0]
	ds_write_b16 v70, v34 offset:24896
	ds_read_b128 v[72:75], v67 offset:2816
	ds_read_b128 v[76:79], v67 offset:2832
	ds_read_b128 v[80:83], v67 offset:2848
	ds_read_b128 v[84:87], v67 offset:2864
	ds_read_b128 v[88:91], v67 offset:2880
	ds_read_b128 v[92:95], v67 offset:2896
	ds_read_b128 v[96:99], v67 offset:2912
	ds_read_b128 v[100:103], v67 offset:2928
	v_cvt_f32_f16_sdwa v34, v40 dst_sel:DWORD dst_unused:UNUSED_PAD src0_sel:WORD_1
	v_cvt_f32_f16_sdwa v35, v32 dst_sel:DWORD dst_unused:UNUSED_PAD src0_sel:WORD_1
	v_pk_mul_f32 v[120:121], v[34:35], v[14:15] op_sel_hi:[0,1]
	v_exp_f32_e32 v120, v120
	v_exp_f32_e32 v121, v121
	v_pk_mul_f32 v[126:127], v[34:35], v[16:17] op_sel_hi:[0,1]
	v_exp_f32_e32 v126, v126
	v_exp_f32_e32 v127, v127
	v_mul_f32_e32 v40, v34, v35
	v_pk_mul_f32 v[38:39], v[120:121], v[38:39]
	s_waitcnt lgkmcnt(14)
	v_pk_fma_f32 v[38:39], v[40:41], v[42:43], v[38:39] op_sel_hi:[0,1,1]
	s_waitcnt lgkmcnt(12)
	v_pk_fma_f32 v[42:43], v[58:59], v[38:39], 0 op_sel_hi:[1,1,0]
	v_pk_mul_f32 v[58:59], v[126:127], v[122:123]
	s_nop 0
	v_pk_fma_f32 v[120:121], v[40:41], v[44:45], v[58:59] op_sel_hi:[0,1,1]
	v_pk_mul_f32 v[44:45], v[34:35], v[10:11] op_sel_hi:[0,1]
	v_exp_f32_e32 v44, v44
	v_exp_f32_e32 v45, v45
	v_pk_mul_f32 v[58:59], v[34:35], v[12:13] op_sel_hi:[0,1]
	v_exp_f32_e32 v58, v58
	v_exp_f32_e32 v59, v59
	v_pk_mul_f32 v[44:45], v[44:45], v[124:125]
	v_pk_fma_f32 v[42:43], v[60:61], v[120:121], v[42:43]
	v_pk_fma_f32 v[122:123], v[40:41], v[46:47], v[44:45] op_sel_hi:[0,1,1]
	v_pk_mul_f32 v[44:45], v[58:59], v[112:113]
	v_pk_mul_f32 v[46:47], v[34:35], v[8:9] op_sel_hi:[0,1]
	v_pk_fma_f32 v[112:113], v[40:41], v[48:49], v[44:45] op_sel_hi:[0,1,1]
	v_pk_mul_f32 v[44:45], v[34:35], v[6:7] op_sel_hi:[0,1]
	v_exp_f32_e32 v44, v44
	v_exp_f32_e32 v45, v45
	v_exp_f32_e32 v46, v46
	v_exp_f32_e32 v47, v47
	s_waitcnt lgkmcnt(11)
	v_pk_fma_f32 v[42:43], v[62:63], v[122:123], v[42:43]
	v_pk_mul_f32 v[44:45], v[44:45], v[114:115]
	v_pk_fma_f32 v[42:43], v[64:65], v[112:113], v[42:43]
	v_pk_fma_f32 v[114:115], v[40:41], v[50:51], v[44:45] op_sel_hi:[0,1,1]
	v_pk_mul_f32 v[44:45], v[46:47], v[116:117]
	s_waitcnt lgkmcnt(10)
	v_pk_fma_f32 v[42:43], v[104:105], v[114:115], v[42:43]
	v_pk_fma_f32 v[116:117], v[40:41], v[52:53], v[44:45] op_sel_hi:[0,1,1]
	v_pk_mul_f32 v[44:45], v[34:35], v[2:3] op_sel_hi:[0,1]
	v_exp_f32_e32 v44, v44
	v_exp_f32_e32 v45, v45
	v_pk_mul_f32 v[34:35], v[34:35], v[4:5] op_sel_hi:[0,1]
	v_exp_f32_e32 v34, v34
	v_exp_f32_e32 v35, v35
	v_pk_mul_f32 v[44:45], v[44:45], v[118:119]
	v_pk_fma_f32 v[42:43], v[106:107], v[116:117], v[42:43]
	v_pk_fma_f32 v[118:119], v[40:41], v[54:55], v[44:45] op_sel_hi:[0,1,1]
	v_pk_mul_f32 v[30:31], v[34:35], v[30:31]
	s_waitcnt lgkmcnt(9)
	v_pk_fma_f32 v[42:43], v[108:109], v[118:119], v[42:43]
	v_pk_fma_f32 v[30:31], v[40:41], v[56:57], v[30:31] op_sel_hi:[0,1,1]
	v_pk_fma_f32 v[34:35], v[110:111], v[30:31], v[42:43]
	s_nop 0
	v_add_f32_e32 v34, v34, v35
	v_fma_mix_f32 v32, v69, v32, v34 op_sel:[0,1,0] op_sel_hi:[0,1,0]
	v_fma_mixlo_f16 v32, v32, v36, 0 op_sel:[0,1,0] op_sel_hi:[0,1,0]
	ds_write_b16 v70, v32 offset:25936
	ds_read_b128 v[42:45], v67 offset:2944
	ds_read_b128 v[46:49], v67 offset:2960
	ds_read_b128 v[50:53], v67 offset:2976
	ds_read_b128 v[54:57], v67 offset:2992
	ds_read_b128 v[58:61], v67 offset:3008
	ds_read_b128 v[62:65], v67 offset:3024
	ds_read_b128 v[104:107], v67 offset:3040
	ds_read_b128 v[108:111], v67 offset:3056
	v_cvt_f32_f16_e32 v32, v41
	v_cvt_f32_f16_e32 v34, v33
	v_pk_mul_f32 v[124:125], v[32:33], v[14:15] op_sel_hi:[0,1]
	v_exp_f32_e32 v124, v124
	v_exp_f32_e32 v125, v125
	v_pk_mul_f32 v[126:127], v[32:33], v[16:17] op_sel_hi:[0,1]
	v_exp_f32_e32 v126, v126
	v_exp_f32_e32 v127, v127
	v_mul_f32_e32 v34, v32, v34
	v_pk_mul_f32 v[38:39], v[124:125], v[38:39]
	s_waitcnt lgkmcnt(14)
	v_pk_fma_f32 v[38:39], v[34:35], v[72:73], v[38:39] op_sel_hi:[0,1,1]
	s_waitcnt lgkmcnt(12)
	v_pk_fma_f32 v[72:73], v[88:89], v[38:39], 0 op_sel_hi:[1,1,0]
	v_pk_mul_f32 v[88:89], v[126:127], v[120:121]
	s_nop 0
	v_pk_fma_f32 v[120:121], v[34:35], v[74:75], v[88:89] op_sel_hi:[0,1,1]
	v_pk_mul_f32 v[74:75], v[32:33], v[10:11] op_sel_hi:[0,1]
	v_exp_f32_e32 v74, v74
	v_exp_f32_e32 v75, v75
	v_pk_mul_f32 v[88:89], v[32:33], v[12:13] op_sel_hi:[0,1]
	v_exp_f32_e32 v88, v88
	v_exp_f32_e32 v89, v89
	v_pk_mul_f32 v[74:75], v[74:75], v[122:123]
	v_pk_fma_f32 v[72:73], v[90:91], v[120:121], v[72:73]
	v_pk_fma_f32 v[122:123], v[34:35], v[76:77], v[74:75] op_sel_hi:[0,1,1]
	v_pk_mul_f32 v[74:75], v[88:89], v[112:113]
	v_pk_mul_f32 v[76:77], v[32:33], v[8:9] op_sel_hi:[0,1]
	v_pk_fma_f32 v[112:113], v[34:35], v[78:79], v[74:75] op_sel_hi:[0,1,1]
	v_pk_mul_f32 v[74:75], v[32:33], v[6:7] op_sel_hi:[0,1]
	v_exp_f32_e32 v74, v74
	v_exp_f32_e32 v75, v75
	v_exp_f32_e32 v76, v76
	v_exp_f32_e32 v77, v77
	s_waitcnt lgkmcnt(11)
	v_pk_fma_f32 v[72:73], v[92:93], v[122:123], v[72:73]
	v_pk_mul_f32 v[74:75], v[74:75], v[114:115]
	v_pk_fma_f32 v[72:73], v[94:95], v[112:113], v[72:73]
	v_pk_fma_f32 v[114:115], v[34:35], v[80:81], v[74:75] op_sel_hi:[0,1,1]
	v_pk_mul_f32 v[74:75], v[76:77], v[116:117]
	v_pk_mul_f32 v[76:77], v[32:33], v[4:5] op_sel_hi:[0,1]
	v_pk_fma_f32 v[116:117], v[34:35], v[82:83], v[74:75] op_sel_hi:[0,1,1]
	v_pk_mul_f32 v[74:75], v[32:33], v[2:3] op_sel_hi:[0,1]
	v_exp_f32_e32 v74, v74
	v_exp_f32_e32 v75, v75
	v_exp_f32_e32 v76, v76
	v_exp_f32_e32 v77, v77
	s_waitcnt lgkmcnt(10)
	v_pk_fma_f32 v[72:73], v[96:97], v[114:115], v[72:73]
	v_pk_mul_f32 v[74:75], v[74:75], v[118:119]
	v_pk_fma_f32 v[72:73], v[98:99], v[116:117], v[72:73]
	v_pk_fma_f32 v[118:119], v[34:35], v[84:85], v[74:75] op_sel_hi:[0,1,1]
	v_pk_mul_f32 v[30:31], v[76:77], v[30:31]
	s_waitcnt lgkmcnt(9)
	v_pk_fma_f32 v[72:73], v[100:101], v[118:119], v[72:73]
	v_pk_fma_f32 v[30:31], v[34:35], v[86:87], v[30:31] op_sel_hi:[0,1,1]
	v_pk_fma_f32 v[34:35], v[102:103], v[30:31], v[72:73]
	s_nop 0
	v_add_f32_e32 v32, v34, v35
	v_fma_mix_f32 v32, v69, v33, v32 op_sel_hi:[0,1,0]
	v_fma_mixlo_f16 v32, v32, v37, 0 op_sel_hi:[0,1,0]
	ds_write_b16 v70, v32 offset:26976
	ds_read_b128 v[72:75], v67 offset:3072
	ds_read_b128 v[76:79], v67 offset:3088
	ds_read_b128 v[80:83], v67 offset:3104
	ds_read_b128 v[84:87], v67 offset:3120
	ds_read_b128 v[88:91], v67 offset:3136
	ds_read_b128 v[92:95], v67 offset:3152
	ds_read_b128 v[96:99], v67 offset:3168
	ds_read_b128 v[100:103], v67 offset:3184
	v_cvt_f32_f16_sdwa v32, v41 dst_sel:DWORD dst_unused:UNUSED_PAD src0_sel:WORD_1
	v_cvt_f32_f16_sdwa v34, v33 dst_sel:DWORD dst_unused:UNUSED_PAD src0_sel:WORD_1
	v_pk_mul_f32 v[40:41], v[32:33], v[14:15] op_sel_hi:[0,1]
	v_pk_mul_f32 v[124:125], v[32:33], v[16:17] op_sel_hi:[0,1]
	v_exp_f32_e32 v40, v40
	v_exp_f32_e32 v41, v41
	v_exp_f32_e32 v124, v124
	v_exp_f32_e32 v125, v125
	v_mul_f32_e32 v34, v32, v34
	v_pk_mul_f32 v[38:39], v[40:41], v[38:39]
	v_pk_mul_f32 v[40:41], v[124:125], v[120:121]
	s_waitcnt lgkmcnt(14)
	v_pk_fma_f32 v[120:121], v[34:35], v[44:45], v[40:41] op_sel_hi:[0,1,1]
	v_pk_mul_f32 v[40:41], v[32:33], v[10:11] op_sel_hi:[0,1]
	v_pk_fma_f32 v[126:127], v[34:35], v[42:43], v[38:39] op_sel_hi:[0,1,1]
	v_exp_f32_e32 v40, v40
	v_exp_f32_e32 v41, v41
	v_pk_mul_f32 v[42:43], v[32:33], v[12:13] op_sel_hi:[0,1]
	v_exp_f32_e32 v42, v42
	v_exp_f32_e32 v43, v43
	s_waitcnt lgkmcnt(12)
	v_pk_fma_f32 v[38:39], v[58:59], v[126:127], 0 op_sel_hi:[1,1,0]
	v_pk_mul_f32 v[40:41], v[40:41], v[122:123]
	v_pk_fma_f32 v[38:39], v[60:61], v[120:121], v[38:39]
	v_pk_fma_f32 v[122:123], v[34:35], v[46:47], v[40:41] op_sel_hi:[0,1,1]
	v_pk_mul_f32 v[40:41], v[42:43], v[112:113]
	s_waitcnt lgkmcnt(11)
	v_pk_fma_f32 v[38:39], v[62:63], v[122:123], v[38:39]
	v_pk_fma_f32 v[62:63], v[34:35], v[48:49], v[40:41] op_sel_hi:[0,1,1]
	v_pk_mul_f32 v[40:41], v[32:33], v[6:7] op_sel_hi:[0,1]
	v_exp_f32_e32 v40, v40
	v_exp_f32_e32 v41, v41
	v_pk_mul_f32 v[42:43], v[32:33], v[8:9] op_sel_hi:[0,1]
	v_exp_f32_e32 v42, v42
	v_exp_f32_e32 v43, v43
	v_pk_mul_f32 v[40:41], v[40:41], v[114:115]
	v_pk_fma_f32 v[38:39], v[64:65], v[62:63], v[38:39]
	v_pk_fma_f32 v[64:65], v[34:35], v[50:51], v[40:41] op_sel_hi:[0,1,1]
	v_pk_mul_f32 v[40:41], v[42:43], v[116:117]
	s_waitcnt lgkmcnt(10)
	v_pk_fma_f32 v[38:39], v[104:105], v[64:65], v[38:39]
	v_pk_fma_f32 v[104:105], v[34:35], v[52:53], v[40:41] op_sel_hi:[0,1,1]
	v_pk_mul_f32 v[40:41], v[32:33], v[2:3] op_sel_hi:[0,1]
	v_exp_f32_e32 v40, v40
	v_exp_f32_e32 v41, v41
	v_pk_mul_f32 v[42:43], v[32:33], v[4:5] op_sel_hi:[0,1]
	v_exp_f32_e32 v42, v42
	v_exp_f32_e32 v43, v43
	v_pk_mul_f32 v[40:41], v[40:41], v[118:119]
	v_pk_fma_f32 v[38:39], v[106:107], v[104:105], v[38:39]
	v_pk_fma_f32 v[106:107], v[34:35], v[54:55], v[40:41] op_sel_hi:[0,1,1]
	v_pk_mul_f32 v[30:31], v[42:43], v[30:31]
	s_waitcnt lgkmcnt(9)
	v_pk_fma_f32 v[38:39], v[108:109], v[106:107], v[38:39]
	v_pk_fma_f32 v[108:109], v[34:35], v[56:57], v[30:31] op_sel_hi:[0,1,1]
	v_pk_fma_f32 v[30:31], v[110:111], v[108:109], v[38:39]
	s_nop 0
	v_add_f32_e32 v30, v30, v31
	v_fma_mix_f32 v30, v69, v33, v30 op_sel:[0,1,0] op_sel_hi:[0,1,0]
	v_fma_mixlo_f16 v30, v30, v37, 0 op_sel:[0,1,0] op_sel_hi:[0,1,0]
	ds_write_b16 v70, v30 offset:28016
	ds_read_b128 v[30:33], v67 offset:3200
	ds_read_b128 v[34:37], v67 offset:3216
	ds_read_b128 v[38:41], v67 offset:3232
	ds_read_b128 v[42:45], v67 offset:3248
	ds_read_b128 v[46:49], v67 offset:3264
	ds_read_b128 v[50:53], v67 offset:3280
	ds_read_b128 v[54:57], v67 offset:3296
	ds_read_b128 v[58:61], v67 offset:3312
	s_waitcnt vmcnt(2)
	v_cvt_f32_f16_e32 v110, v26
	s_waitcnt vmcnt(1)
	v_cvt_f32_f16_e32 v71, v18
	v_pk_mul_f32 v[114:115], v[110:111], v[14:15] op_sel_hi:[0,1]
	v_exp_f32_e32 v114, v114
	v_exp_f32_e32 v115, v115
	v_pk_mul_f32 v[116:117], v[110:111], v[16:17] op_sel_hi:[0,1]
	v_exp_f32_e32 v116, v116
	v_exp_f32_e32 v117, v117
	v_mul_f32_e32 v112, v110, v71
	v_pk_mul_f32 v[114:115], v[114:115], v[126:127]
	s_waitcnt lgkmcnt(14)
	v_pk_fma_f32 v[114:115], v[112:113], v[72:73], v[114:115] op_sel_hi:[0,1,1]
	s_waitcnt lgkmcnt(12)
	v_pk_fma_f32 v[72:73], v[88:89], v[114:115], 0 op_sel_hi:[1,1,0]
	v_pk_mul_f32 v[88:89], v[116:117], v[120:121]
	s_nop 0
	v_pk_fma_f32 v[116:117], v[112:113], v[74:75], v[88:89] op_sel_hi:[0,1,1]
	v_pk_mul_f32 v[74:75], v[110:111], v[10:11] op_sel_hi:[0,1]
	v_exp_f32_e32 v74, v74
	v_exp_f32_e32 v75, v75
	v_pk_mul_f32 v[88:89], v[110:111], v[12:13] op_sel_hi:[0,1]
	v_exp_f32_e32 v88, v88
	v_exp_f32_e32 v89, v89
	v_pk_mul_f32 v[74:75], v[74:75], v[122:123]
	v_pk_fma_f32 v[72:73], v[90:91], v[116:117], v[72:73]
	v_pk_fma_f32 v[118:119], v[112:113], v[76:77], v[74:75] op_sel_hi:[0,1,1]
	v_pk_mul_f32 v[62:63], v[88:89], v[62:63]
	s_waitcnt lgkmcnt(11)
	v_pk_fma_f32 v[72:73], v[92:93], v[118:119], v[72:73]
	v_pk_fma_f32 v[120:121], v[112:113], v[78:79], v[62:63] op_sel_hi:[0,1,1]
	v_pk_fma_f32 v[62:63], v[94:95], v[120:121], v[72:73]
	v_pk_mul_f32 v[72:73], v[110:111], v[6:7] op_sel_hi:[0,1]
	v_exp_f32_e32 v72, v72
	v_exp_f32_e32 v73, v73
	v_pk_mul_f32 v[74:75], v[110:111], v[8:9] op_sel_hi:[0,1]
	v_exp_f32_e32 v74, v74
	v_exp_f32_e32 v75, v75
	v_pk_mul_f32 v[64:65], v[72:73], v[64:65]
	v_pk_mul_f32 v[72:73], v[110:111], v[4:5] op_sel_hi:[0,1]
	v_pk_fma_f32 v[122:123], v[112:113], v[80:81], v[64:65] op_sel_hi:[0,1,1]
	v_pk_mul_f32 v[64:65], v[74:75], v[104:105]
	v_exp_f32_e32 v72, v72
	v_pk_fma_f32 v[104:105], v[112:113], v[82:83], v[64:65] op_sel_hi:[0,1,1]
	v_pk_mul_f32 v[64:65], v[110:111], v[2:3] op_sel_hi:[0,1]
	v_exp_f32_e32 v64, v64
	v_exp_f32_e32 v65, v65
	v_exp_f32_e32 v73, v73
	s_waitcnt lgkmcnt(10)
	v_pk_fma_f32 v[62:63], v[96:97], v[122:123], v[62:63]
	v_pk_mul_f32 v[64:65], v[64:65], v[106:107]
	v_pk_fma_f32 v[62:63], v[98:99], v[104:105], v[62:63]
	v_pk_fma_f32 v[106:107], v[112:113], v[84:85], v[64:65] op_sel_hi:[0,1,1]
	v_pk_mul_f32 v[64:65], v[72:73], v[108:109]
	s_waitcnt lgkmcnt(9)
	v_pk_fma_f32 v[62:63], v[100:101], v[106:107], v[62:63]
	v_pk_fma_f32 v[100:101], v[112:113], v[86:87], v[64:65] op_sel_hi:[0,1,1]
	v_pk_fma_f32 v[62:63], v[102:103], v[100:101], v[62:63]
	s_nop 0
	v_add_f32_e32 v62, v62, v63
	v_fma_mix_f32 v62, v69, v18, v62 op_sel_hi:[0,1,0]
	s_waitcnt vmcnt(0)
	v_fma_mixlo_f16 v62, v62, v22, 0 op_sel_hi:[0,1,0]
	ds_write_b16 v70, v62 offset:29056
	v_lshrrev_b32_e32 v176, 6, v0
	v_and_b32_e32 v177, 48, v0
	v_lshl_or_b32 v176, v176, 7, v177
	v_and_b32_e32 v177, 15, v0
	v_or_b32_e32 v177, s24, v177
	v_lshl_or_b32 v176, v177, 10, v176
	v_add_u32_e32 v177, 0x4000, v176
	global_load_dwordx4 v[160:163], v176, s[28:29]
	global_load_dwordx4 v[164:167], v176, s[28:29] offset:64
	global_load_dwordx4 v[168:171], v177, s[28:29]
	global_load_dwordx4 v[172:175], v177, s[28:29] offset:64
	ds_read_b128 v[62:65], v67 offset:3328
	ds_read_b128 v[72:75], v67 offset:3344
	ds_read_b128 v[76:79], v67 offset:3360
	ds_read_b128 v[80:83], v67 offset:3376
	ds_read_b128 v[84:87], v67 offset:3392
	ds_read_b128 v[88:91], v67 offset:3408
	ds_read_b128 v[92:95], v67 offset:3424
	ds_read_b128 v[96:99], v67 offset:3440
	v_cvt_f32_f16_sdwa v26, v26 dst_sel:DWORD dst_unused:UNUSED_PAD src0_sel:WORD_1
	v_cvt_f32_f16_sdwa v71, v18 dst_sel:DWORD dst_unused:UNUSED_PAD src0_sel:WORD_1
	v_pk_mul_f32 v[108:109], v[26:27], v[14:15] op_sel_hi:[0,1]
	v_exp_f32_e32 v108, v108
	v_exp_f32_e32 v109, v109
	v_pk_mul_f32 v[110:111], v[26:27], v[16:17] op_sel_hi:[0,1]
	v_exp_f32_e32 v110, v110
	v_exp_f32_e32 v111, v111
	v_mul_f32_e32 v102, v26, v71
	v_pk_mul_f32 v[108:109], v[108:109], v[114:115]
	s_waitcnt lgkmcnt(14)
	v_pk_fma_f32 v[108:109], v[102:103], v[30:31], v[108:109] op_sel_hi:[0,1,1]
	s_waitcnt lgkmcnt(12)
	v_pk_fma_f32 v[30:31], v[46:47], v[108:109], 0 op_sel_hi:[1,1,0]
	v_pk_mul_f32 v[46:47], v[110:111], v[116:117]
	s_nop 0
	v_pk_fma_f32 v[110:111], v[102:103], v[32:33], v[46:47] op_sel_hi:[0,1,1]
	v_pk_mul_f32 v[32:33], v[26:27], v[10:11] op_sel_hi:[0,1]
	v_exp_f32_e32 v32, v32
	v_exp_f32_e32 v33, v33
	v_pk_mul_f32 v[46:47], v[26:27], v[12:13] op_sel_hi:[0,1]
	v_exp_f32_e32 v46, v46
	v_exp_f32_e32 v47, v47
	v_pk_mul_f32 v[32:33], v[32:33], v[118:119]
	v_pk_fma_f32 v[30:31], v[48:49], v[110:111], v[30:31]
	v_pk_fma_f32 v[112:113], v[102:103], v[34:35], v[32:33] op_sel_hi:[0,1,1]
	v_pk_mul_f32 v[32:33], v[46:47], v[120:121]
	v_pk_mul_f32 v[34:35], v[26:27], v[8:9] op_sel_hi:[0,1]
	v_pk_fma_f32 v[114:115], v[102:103], v[36:37], v[32:33] op_sel_hi:[0,1,1]
	v_pk_mul_f32 v[32:33], v[26:27], v[6:7] op_sel_hi:[0,1]
	v_exp_f32_e32 v32, v32
	v_exp_f32_e32 v33, v33
	v_exp_f32_e32 v34, v34
	v_exp_f32_e32 v35, v35
	s_waitcnt lgkmcnt(11)
	v_pk_fma_f32 v[30:31], v[50:51], v[112:113], v[30:31]
	v_pk_mul_f32 v[32:33], v[32:33], v[122:123]
	v_pk_fma_f32 v[30:31], v[52:53], v[114:115], v[30:31]
	v_pk_fma_f32 v[116:117], v[102:103], v[38:39], v[32:33] op_sel_hi:[0,1,1]
	v_pk_mul_f32 v[32:33], v[34:35], v[104:105]
	v_pk_mul_f32 v[34:35], v[26:27], v[4:5] op_sel_hi:[0,1]
	v_pk_fma_f32 v[104:105], v[102:103], v[40:41], v[32:33] op_sel_hi:[0,1,1]
	v_pk_mul_f32 v[32:33], v[26:27], v[2:3] op_sel_hi:[0,1]
	v_exp_f32_e32 v32, v32
	v_exp_f32_e32 v33, v33
	v_exp_f32_e32 v34, v34
	v_exp_f32_e32 v35, v35
	s_waitcnt lgkmcnt(10)
	v_pk_fma_f32 v[30:31], v[54:55], v[116:117], v[30:31]
	v_pk_mul_f32 v[32:33], v[32:33], v[106:107]
	v_pk_fma_f32 v[30:31], v[56:57], v[104:105], v[30:31]
	v_pk_fma_f32 v[106:107], v[102:103], v[42:43], v[32:33] op_sel_hi:[0,1,1]
	v_pk_mul_f32 v[32:33], v[34:35], v[100:101]
	s_waitcnt lgkmcnt(9)
	v_pk_fma_f32 v[30:31], v[58:59], v[106:107], v[30:31]
	v_pk_fma_f32 v[100:101], v[102:103], v[44:45], v[32:33] op_sel_hi:[0,1,1]
	v_pk_fma_f32 v[30:31], v[60:61], v[100:101], v[30:31]
	s_nop 0
	v_add_f32_e32 v26, v30, v31
	v_fma_mix_f32 v18, v69, v18, v26 op_sel:[0,1,0] op_sel_hi:[0,1,0]
	v_fma_mixlo_f16 v18, v18, v22, 0 op_sel:[0,1,0] op_sel_hi:[0,1,0]
	ds_write_b16 v70, v18 offset:30096
	ds_read_b128 v[30:33], v67 offset:3456
	ds_read_b128 v[34:37], v67 offset:3472
	ds_read_b128 v[38:41], v67 offset:3488
	ds_read_b128 v[42:45], v67 offset:3504
	ds_read_b128 v[46:49], v67 offset:3520
	ds_read_b128 v[50:53], v67 offset:3536
	ds_read_b128 v[54:57], v67 offset:3552
	ds_read_b128 v[58:61], v67 offset:3568
	v_cvt_f32_f16_e32 v18, v27
	v_cvt_f32_f16_e32 v22, v19
	v_pk_mul_f32 v[102:103], v[18:19], v[14:15] op_sel_hi:[0,1]
	v_exp_f32_e32 v102, v102
	v_exp_f32_e32 v103, v103
	v_pk_mul_f32 v[118:119], v[18:19], v[16:17] op_sel_hi:[0,1]
	v_exp_f32_e32 v118, v118
	v_exp_f32_e32 v119, v119
	v_mul_f32_e32 v22, v18, v22
	v_pk_mul_f32 v[102:103], v[102:103], v[108:109]
	s_waitcnt lgkmcnt(14)
	v_pk_fma_f32 v[102:103], v[22:23], v[62:63], v[102:103] op_sel_hi:[0,1,1]
	s_waitcnt lgkmcnt(12)
	v_pk_fma_f32 v[62:63], v[84:85], v[102:103], 0 op_sel_hi:[1,1,0]
	v_pk_mul_f32 v[84:85], v[118:119], v[110:111]
	s_nop 0
	v_pk_fma_f32 v[108:109], v[22:23], v[64:65], v[84:85] op_sel_hi:[0,1,1]
	v_pk_mul_f32 v[64:65], v[18:19], v[10:11] op_sel_hi:[0,1]
	v_exp_f32_e32 v64, v64
	v_exp_f32_e32 v65, v65
	v_pk_mul_f32 v[84:85], v[18:19], v[12:13] op_sel_hi:[0,1]
	v_exp_f32_e32 v84, v84
	v_exp_f32_e32 v85, v85
	v_pk_mul_f32 v[64:65], v[64:65], v[112:113]
	v_pk_fma_f32 v[62:63], v[86:87], v[108:109], v[62:63]
	v_pk_fma_f32 v[110:111], v[22:23], v[72:73], v[64:65] op_sel_hi:[0,1,1]
	v_pk_mul_f32 v[64:65], v[84:85], v[114:115]
	v_pk_mul_f32 v[72:73], v[18:19], v[8:9] op_sel_hi:[0,1]
	v_pk_fma_f32 v[112:113], v[22:23], v[74:75], v[64:65] op_sel_hi:[0,1,1]
	v_pk_mul_f32 v[64:65], v[18:19], v[6:7] op_sel_hi:[0,1]
	v_exp_f32_e32 v64, v64
	v_exp_f32_e32 v65, v65
	v_exp_f32_e32 v72, v72
	v_exp_f32_e32 v73, v73
	s_waitcnt lgkmcnt(11)
	v_pk_fma_f32 v[62:63], v[88:89], v[110:111], v[62:63]
	v_pk_mul_f32 v[64:65], v[64:65], v[116:117]
	v_pk_fma_f32 v[62:63], v[90:91], v[112:113], v[62:63]
	v_pk_fma_f32 v[114:115], v[22:23], v[76:77], v[64:65] op_sel_hi:[0,1,1]
	v_pk_mul_f32 v[64:65], v[72:73], v[104:105]
	v_pk_mul_f32 v[72:73], v[18:19], v[4:5] op_sel_hi:[0,1]
	v_pk_fma_f32 v[104:105], v[22:23], v[78:79], v[64:65] op_sel_hi:[0,1,1]
	v_pk_mul_f32 v[64:65], v[18:19], v[2:3] op_sel_hi:[0,1]
	v_exp_f32_e32 v64, v64
	v_exp_f32_e32 v65, v65
	v_exp_f32_e32 v72, v72
	v_exp_f32_e32 v73, v73
	s_waitcnt lgkmcnt(10)
	v_pk_fma_f32 v[62:63], v[92:93], v[114:115], v[62:63]
	v_pk_mul_f32 v[64:65], v[64:65], v[106:107]
	v_pk_fma_f32 v[62:63], v[94:95], v[104:105], v[62:63]
	v_pk_fma_f32 v[106:107], v[22:23], v[80:81], v[64:65] op_sel_hi:[0,1,1]
	v_pk_mul_f32 v[64:65], v[72:73], v[100:101]
	s_waitcnt lgkmcnt(9)
	v_pk_fma_f32 v[62:63], v[96:97], v[106:107], v[62:63]
	v_pk_fma_f32 v[100:101], v[22:23], v[82:83], v[64:65] op_sel_hi:[0,1,1]
	v_pk_fma_f32 v[62:63], v[98:99], v[100:101], v[62:63]
	s_nop 0
	v_add_f32_e32 v18, v62, v63
	v_fma_mix_f32 v18, v69, v19, v18 op_sel_hi:[0,1,0]
	v_fma_mixlo_f16 v18, v18, v23, 0 op_sel_hi:[0,1,0]
	ds_write_b16 v70, v18 offset:31136
	ds_read_b128 v[62:65], v67 offset:3584
	ds_read_b128 v[72:75], v67 offset:3600
	ds_read_b128 v[76:79], v67 offset:3616
	ds_read_b128 v[80:83], v67 offset:3632
	ds_read_b128 v[84:87], v67 offset:3648
	ds_read_b128 v[88:91], v67 offset:3664
	ds_read_b128 v[92:95], v67 offset:3680
	ds_read_b128 v[96:99], v67 offset:3696
	v_cvt_f32_f16_sdwa v18, v27 dst_sel:DWORD dst_unused:UNUSED_PAD src0_sel:WORD_1
	v_cvt_f32_f16_sdwa v22, v19 dst_sel:DWORD dst_unused:UNUSED_PAD src0_sel:WORD_1
	v_pk_mul_f32 v[26:27], v[18:19], v[14:15] op_sel_hi:[0,1]
	v_exp_f32_e32 v26, v26
	v_exp_f32_e32 v27, v27
	v_pk_mul_f32 v[116:117], v[18:19], v[16:17] op_sel_hi:[0,1]
	v_exp_f32_e32 v116, v116
	v_exp_f32_e32 v117, v117
	v_mul_f32_e32 v22, v18, v22
	v_pk_mul_f32 v[26:27], v[26:27], v[102:103]
	s_waitcnt lgkmcnt(14)
	v_pk_fma_f32 v[26:27], v[22:23], v[30:31], v[26:27] op_sel_hi:[0,1,1]
	s_waitcnt lgkmcnt(12)
	v_pk_fma_f32 v[30:31], v[46:47], v[26:27], 0 op_sel_hi:[1,1,0]
	v_pk_mul_f32 v[46:47], v[116:117], v[108:109]
	s_nop 0
	v_pk_fma_f32 v[102:103], v[22:23], v[32:33], v[46:47] op_sel_hi:[0,1,1]
	v_pk_mul_f32 v[32:33], v[18:19], v[10:11] op_sel_hi:[0,1]
	v_exp_f32_e32 v32, v32
	v_exp_f32_e32 v33, v33
	v_pk_mul_f32 v[46:47], v[18:19], v[12:13] op_sel_hi:[0,1]
	v_exp_f32_e32 v46, v46
	v_exp_f32_e32 v47, v47
	v_pk_mul_f32 v[32:33], v[32:33], v[110:111]
	v_pk_fma_f32 v[30:31], v[48:49], v[102:103], v[30:31]
	v_pk_fma_f32 v[108:109], v[22:23], v[34:35], v[32:33] op_sel_hi:[0,1,1]
	v_pk_mul_f32 v[32:33], v[46:47], v[112:113]
	v_pk_mul_f32 v[34:35], v[18:19], v[8:9] op_sel_hi:[0,1]
	v_pk_fma_f32 v[110:111], v[22:23], v[36:37], v[32:33] op_sel_hi:[0,1,1]
	v_pk_mul_f32 v[32:33], v[18:19], v[6:7] op_sel_hi:[0,1]
	v_exp_f32_e32 v32, v32
	v_exp_f32_e32 v33, v33
	v_exp_f32_e32 v34, v34
	v_exp_f32_e32 v35, v35
	s_waitcnt lgkmcnt(11)
	v_pk_fma_f32 v[30:31], v[50:51], v[108:109], v[30:31]
	v_pk_mul_f32 v[32:33], v[32:33], v[114:115]
	v_pk_fma_f32 v[30:31], v[52:53], v[110:111], v[30:31]
	v_pk_fma_f32 v[112:113], v[22:23], v[38:39], v[32:33] op_sel_hi:[0,1,1]
	v_pk_mul_f32 v[32:33], v[34:35], v[104:105]
	v_pk_mul_f32 v[34:35], v[18:19], v[4:5] op_sel_hi:[0,1]
	v_pk_fma_f32 v[104:105], v[22:23], v[40:41], v[32:33] op_sel_hi:[0,1,1]
	v_pk_mul_f32 v[32:33], v[18:19], v[2:3] op_sel_hi:[0,1]
	v_exp_f32_e32 v32, v32
	v_exp_f32_e32 v33, v33
	v_exp_f32_e32 v34, v34
	v_exp_f32_e32 v35, v35
	s_waitcnt lgkmcnt(10)
	v_pk_fma_f32 v[30:31], v[54:55], v[112:113], v[30:31]
	v_pk_mul_f32 v[32:33], v[32:33], v[106:107]
	v_pk_fma_f32 v[30:31], v[56:57], v[104:105], v[30:31]
	v_pk_fma_f32 v[106:107], v[22:23], v[42:43], v[32:33] op_sel_hi:[0,1,1]
	v_pk_mul_f32 v[32:33], v[34:35], v[100:101]
	s_waitcnt lgkmcnt(9)
	v_pk_fma_f32 v[30:31], v[58:59], v[106:107], v[30:31]
	v_pk_fma_f32 v[100:101], v[22:23], v[44:45], v[32:33] op_sel_hi:[0,1,1]
	v_pk_fma_f32 v[30:31], v[60:61], v[100:101], v[30:31]
	s_nop 0
	v_add_f32_e32 v18, v30, v31
	v_fma_mix_f32 v18, v69, v19, v18 op_sel:[0,1,0] op_sel_hi:[0,1,0]
	v_fma_mixlo_f16 v18, v18, v23, 0 op_sel:[0,1,0] op_sel_hi:[0,1,0]
	ds_write_b16 v70, v18 offset:32176
	ds_read_b128 v[30:33], v67 offset:3712
	ds_read_b128 v[34:37], v67 offset:3728
	ds_read_b128 v[38:41], v67 offset:3744
	ds_read_b128 v[42:45], v67 offset:3760
	ds_read_b128 v[46:49], v67 offset:3776
	ds_read_b128 v[50:53], v67 offset:3792
	ds_read_b128 v[54:57], v67 offset:3808
	ds_read_b128 v[58:61], v67 offset:3824
	v_cvt_f32_f16_e32 v18, v28
	v_cvt_f32_f16_e32 v19, v20
	v_pk_mul_f32 v[114:115], v[18:19], v[14:15] op_sel_hi:[0,1]
	v_exp_f32_e32 v114, v114
	v_exp_f32_e32 v115, v115
	v_pk_mul_f32 v[116:117], v[18:19], v[16:17] op_sel_hi:[0,1]
	v_exp_f32_e32 v116, v116
	v_exp_f32_e32 v117, v117
	v_mul_f32_e32 v22, v18, v19
	v_pk_mul_f32 v[26:27], v[114:115], v[26:27]
	s_waitcnt lgkmcnt(14)
	v_pk_fma_f32 v[26:27], v[22:23], v[62:63], v[26:27] op_sel_hi:[0,1,1]
	s_waitcnt lgkmcnt(12)
	v_pk_fma_f32 v[62:63], v[84:85], v[26:27], 0 op_sel_hi:[1,1,0]
	v_pk_mul_f32 v[84:85], v[116:117], v[102:103]
	s_nop 0
	v_pk_fma_f32 v[102:103], v[22:23], v[64:65], v[84:85] op_sel_hi:[0,1,1]
	v_pk_mul_f32 v[64:65], v[18:19], v[10:11] op_sel_hi:[0,1]
	v_exp_f32_e32 v64, v64
	v_exp_f32_e32 v65, v65
	v_pk_mul_f32 v[84:85], v[18:19], v[12:13] op_sel_hi:[0,1]
	v_exp_f32_e32 v84, v84
	v_exp_f32_e32 v85, v85
	v_pk_mul_f32 v[64:65], v[64:65], v[108:109]
	v_pk_fma_f32 v[62:63], v[86:87], v[102:103], v[62:63]
	v_pk_fma_f32 v[108:109], v[22:23], v[72:73], v[64:65] op_sel_hi:[0,1,1]
	v_pk_mul_f32 v[64:65], v[84:85], v[110:111]
	v_pk_mul_f32 v[72:73], v[18:19], v[8:9] op_sel_hi:[0,1]
	v_pk_fma_f32 v[110:111], v[22:23], v[74:75], v[64:65] op_sel_hi:[0,1,1]
	v_pk_mul_f32 v[64:65], v[18:19], v[6:7] op_sel_hi:[0,1]
	v_exp_f32_e32 v64, v64
	v_exp_f32_e32 v65, v65
	v_exp_f32_e32 v72, v72
	v_exp_f32_e32 v73, v73
	s_waitcnt lgkmcnt(11)
	v_pk_fma_f32 v[62:63], v[88:89], v[108:109], v[62:63]
	v_pk_mul_f32 v[64:65], v[64:65], v[112:113]
	v_pk_fma_f32 v[62:63], v[90:91], v[110:111], v[62:63]
	v_pk_fma_f32 v[112:113], v[22:23], v[76:77], v[64:65] op_sel_hi:[0,1,1]
	v_pk_mul_f32 v[64:65], v[72:73], v[104:105]
	s_waitcnt lgkmcnt(10)
	v_pk_fma_f32 v[62:63], v[92:93], v[112:113], v[62:63]
	v_pk_fma_f32 v[104:105], v[22:23], v[78:79], v[64:65] op_sel_hi:[0,1,1]
	v_pk_mul_f32 v[64:65], v[18:19], v[2:3] op_sel_hi:[0,1]
	v_exp_f32_e32 v64, v64
	v_exp_f32_e32 v65, v65
	v_pk_mul_f32 v[18:19], v[18:19], v[4:5] op_sel_hi:[0,1]
	v_exp_f32_e32 v18, v18
	v_exp_f32_e32 v19, v19
	v_pk_mul_f32 v[64:65], v[64:65], v[106:107]
	v_pk_fma_f32 v[62:63], v[94:95], v[104:105], v[62:63]
	v_pk_fma_f32 v[106:107], v[22:23], v[80:81], v[64:65] op_sel_hi:[0,1,1]
	v_pk_mul_f32 v[18:19], v[18:19], v[100:101]
	s_waitcnt lgkmcnt(9)
	v_pk_fma_f32 v[62:63], v[96:97], v[106:107], v[62:63]
	v_pk_fma_f32 v[18:19], v[22:23], v[82:83], v[18:19] op_sel_hi:[0,1,1]
	v_pk_fma_f32 v[22:23], v[98:99], v[18:19], v[62:63]
	s_nop 0
	v_add_f32_e32 v22, v22, v23
	v_fma_mix_f32 v22, v69, v20, v22 op_sel_hi:[0,1,0]
	v_fma_mixlo_f16 v22, v22, v24, 0 op_sel_hi:[0,1,0]
	ds_write_b16 v70, v22 offset:33216
	ds_read_b128 v[62:65], v67 offset:3840
	ds_read_b128 v[72:75], v67 offset:3856
	ds_read_b128 v[76:79], v67 offset:3872
	ds_read_b128 v[80:83], v67 offset:3888
	ds_read_b128 v[84:87], v67 offset:3904
	ds_read_b128 v[88:91], v67 offset:3920
	ds_read_b128 v[92:95], v67 offset:3936
	ds_read_b128 v[96:99], v67 offset:3952
	v_cvt_f32_f16_sdwa v22, v28 dst_sel:DWORD dst_unused:UNUSED_PAD src0_sel:WORD_1
	v_cvt_f32_f16_sdwa v23, v20 dst_sel:DWORD dst_unused:UNUSED_PAD src0_sel:WORD_1
	v_pk_mul_f32 v[100:101], v[22:23], v[14:15] op_sel_hi:[0,1]
	v_exp_f32_e32 v100, v100
	v_exp_f32_e32 v101, v101
	v_pk_mul_f32 v[114:115], v[22:23], v[16:17] op_sel_hi:[0,1]
	v_exp_f32_e32 v114, v114
	v_exp_f32_e32 v115, v115
	v_mul_f32_e32 v28, v22, v23
	v_pk_mul_f32 v[26:27], v[100:101], v[26:27]
	s_waitcnt lgkmcnt(14)
	v_pk_fma_f32 v[26:27], v[28:29], v[30:31], v[26:27] op_sel_hi:[0,1,1]
	s_waitcnt lgkmcnt(12)
	v_pk_fma_f32 v[30:31], v[46:47], v[26:27], 0 op_sel_hi:[1,1,0]
	v_pk_mul_f32 v[46:47], v[114:115], v[102:103]
	s_nop 0
	v_pk_fma_f32 v[100:101], v[28:29], v[32:33], v[46:47] op_sel_hi:[0,1,1]
	v_pk_mul_f32 v[32:33], v[22:23], v[10:11] op_sel_hi:[0,1]
	v_exp_f32_e32 v32, v32
	v_exp_f32_e32 v33, v33
	v_pk_mul_f32 v[46:47], v[22:23], v[12:13] op_sel_hi:[0,1]
	v_exp_f32_e32 v46, v46
	v_exp_f32_e32 v47, v47
	v_pk_mul_f32 v[32:33], v[32:33], v[108:109]
	v_pk_fma_f32 v[30:31], v[48:49], v[100:101], v[30:31]
	v_pk_fma_f32 v[102:103], v[28:29], v[34:35], v[32:33] op_sel_hi:[0,1,1]
	v_pk_mul_f32 v[32:33], v[46:47], v[110:111]
	v_pk_mul_f32 v[34:35], v[22:23], v[8:9] op_sel_hi:[0,1]
	v_pk_fma_f32 v[108:109], v[28:29], v[36:37], v[32:33] op_sel_hi:[0,1,1]
	v_pk_mul_f32 v[32:33], v[22:23], v[6:7] op_sel_hi:[0,1]
	v_exp_f32_e32 v32, v32
	v_exp_f32_e32 v33, v33
	v_exp_f32_e32 v34, v34
	v_exp_f32_e32 v35, v35
	s_waitcnt lgkmcnt(11)
	v_pk_fma_f32 v[30:31], v[50:51], v[102:103], v[30:31]
	v_pk_mul_f32 v[32:33], v[32:33], v[112:113]
	v_pk_fma_f32 v[30:31], v[52:53], v[108:109], v[30:31]
	v_pk_fma_f32 v[110:111], v[28:29], v[38:39], v[32:33] op_sel_hi:[0,1,1]
	v_pk_mul_f32 v[32:33], v[34:35], v[104:105]
	s_waitcnt lgkmcnt(10)
	v_pk_fma_f32 v[30:31], v[54:55], v[110:111], v[30:31]
	v_pk_fma_f32 v[104:105], v[28:29], v[40:41], v[32:33] op_sel_hi:[0,1,1]
	v_pk_mul_f32 v[32:33], v[22:23], v[2:3] op_sel_hi:[0,1]
	v_exp_f32_e32 v32, v32
	v_exp_f32_e32 v33, v33
	v_pk_mul_f32 v[22:23], v[22:23], v[4:5] op_sel_hi:[0,1]
	v_exp_f32_e32 v22, v22
	v_exp_f32_e32 v23, v23
	v_pk_mul_f32 v[32:33], v[32:33], v[106:107]
	v_pk_fma_f32 v[30:31], v[56:57], v[104:105], v[30:31]
	v_pk_fma_f32 v[106:107], v[28:29], v[42:43], v[32:33] op_sel_hi:[0,1,1]
	v_pk_mul_f32 v[18:19], v[22:23], v[18:19]
	s_waitcnt lgkmcnt(9)
	v_pk_fma_f32 v[30:31], v[58:59], v[106:107], v[30:31]
	v_pk_fma_f32 v[18:19], v[28:29], v[44:45], v[18:19] op_sel_hi:[0,1,1]
	v_pk_fma_f32 v[22:23], v[60:61], v[18:19], v[30:31]
	s_nop 0
	v_add_f32_e32 v22, v22, v23
	v_fma_mix_f32 v20, v69, v20, v22 op_sel:[0,1,0] op_sel_hi:[0,1,0]
	v_fma_mixlo_f16 v20, v20, v24, 0 op_sel:[0,1,0] op_sel_hi:[0,1,0]
	ds_write_b16 v70, v20 offset:34256
	ds_read_b128 v[30:33], v67 offset:3968
	ds_read_b128 v[34:37], v67 offset:3984
	ds_read_b128 v[38:41], v67 offset:4000
	ds_read_b128 v[42:45], v67 offset:4016
	ds_read_b128 v[46:49], v67 offset:4032
	ds_read_b128 v[50:53], v67 offset:4048
	ds_read_b128 v[54:57], v67 offset:4064
	ds_read_b128 v[58:61], v67 offset:4080
	v_cvt_f32_f16_e32 v20, v29
	v_cvt_f32_f16_e32 v22, v21
	v_pk_mul_f32 v[112:113], v[20:21], v[14:15] op_sel_hi:[0,1]
	v_exp_f32_e32 v112, v112
	v_exp_f32_e32 v113, v113
	v_pk_mul_f32 v[114:115], v[20:21], v[16:17] op_sel_hi:[0,1]
	v_exp_f32_e32 v114, v114
	v_exp_f32_e32 v115, v115
	v_mul_f32_e32 v22, v20, v22
	v_pk_mul_f32 v[26:27], v[112:113], v[26:27]
	s_waitcnt lgkmcnt(14)
	v_pk_fma_f32 v[26:27], v[22:23], v[62:63], v[26:27] op_sel_hi:[0,1,1]
	s_waitcnt lgkmcnt(12)
	v_pk_fma_f32 v[62:63], v[84:85], v[26:27], 0 op_sel_hi:[1,1,0]
	v_pk_mul_f32 v[84:85], v[114:115], v[100:101]
	s_nop 0
	v_pk_fma_f32 v[64:65], v[22:23], v[64:65], v[84:85] op_sel_hi:[0,1,1]
	v_pk_mul_f32 v[84:85], v[20:21], v[10:11] op_sel_hi:[0,1]
	v_pk_fma_f32 v[62:63], v[86:87], v[64:65], v[62:63]
	v_exp_f32_e32 v84, v84
	v_exp_f32_e32 v85, v85
	v_pk_mul_f32 v[86:87], v[20:21], v[12:13] op_sel_hi:[0,1]
	v_exp_f32_e32 v86, v86
	v_exp_f32_e32 v87, v87
	v_pk_mul_f32 v[84:85], v[84:85], v[102:103]
	s_nop 0
	v_pk_fma_f32 v[72:73], v[22:23], v[72:73], v[84:85] op_sel_hi:[0,1,1]
	v_pk_mul_f32 v[84:85], v[86:87], v[108:109]
	v_pk_mul_f32 v[86:87], v[20:21], v[8:9] op_sel_hi:[0,1]
	v_pk_fma_f32 v[74:75], v[22:23], v[74:75], v[84:85] op_sel_hi:[0,1,1]
	v_pk_mul_f32 v[84:85], v[20:21], v[6:7] op_sel_hi:[0,1]
	v_exp_f32_e32 v84, v84
	v_exp_f32_e32 v85, v85
	v_exp_f32_e32 v86, v86
	v_exp_f32_e32 v87, v87
	s_waitcnt lgkmcnt(11)
	v_pk_fma_f32 v[62:63], v[88:89], v[72:73], v[62:63]
	v_pk_mul_f32 v[84:85], v[84:85], v[110:111]
	v_pk_fma_f32 v[62:63], v[90:91], v[74:75], v[62:63]
	v_pk_fma_f32 v[76:77], v[22:23], v[76:77], v[84:85] op_sel_hi:[0,1,1]
	v_pk_mul_f32 v[84:85], v[86:87], v[104:105]
	v_pk_mul_f32 v[86:87], v[20:21], v[4:5] op_sel_hi:[0,1]
	v_pk_fma_f32 v[78:79], v[22:23], v[78:79], v[84:85] op_sel_hi:[0,1,1]
	v_pk_mul_f32 v[84:85], v[20:21], v[2:3] op_sel_hi:[0,1]
	v_exp_f32_e32 v84, v84
	v_exp_f32_e32 v85, v85
	v_exp_f32_e32 v86, v86
	v_exp_f32_e32 v87, v87
	s_waitcnt lgkmcnt(10)
	v_pk_fma_f32 v[62:63], v[92:93], v[76:77], v[62:63]
	v_pk_mul_f32 v[84:85], v[84:85], v[106:107]
	v_pk_fma_f32 v[62:63], v[94:95], v[78:79], v[62:63]
	v_pk_fma_f32 v[80:81], v[22:23], v[80:81], v[84:85] op_sel_hi:[0,1,1]
	v_pk_mul_f32 v[18:19], v[86:87], v[18:19]
	s_waitcnt lgkmcnt(9)
	v_pk_fma_f32 v[62:63], v[96:97], v[80:81], v[62:63]
	v_pk_fma_f32 v[18:19], v[22:23], v[82:83], v[18:19] op_sel_hi:[0,1,1]
	v_pk_fma_f32 v[22:23], v[98:99], v[18:19], v[62:63]
	s_nop 0
	v_add_f32_e32 v20, v22, v23
	v_fma_mix_f32 v20, v69, v21, v20 op_sel_hi:[0,1,0]
	v_fma_mixlo_f16 v20, v20, v25, 0 op_sel_hi:[0,1,0]
	ds_write_b16 v70, v20 offset:35296
	v_cvt_f32_f16_sdwa v20, v29 dst_sel:DWORD dst_unused:UNUSED_PAD src0_sel:WORD_1
	v_cvt_f32_f16_sdwa v22, v21 dst_sel:DWORD dst_unused:UNUSED_PAD src0_sel:WORD_1
	v_pk_mul_f32 v[14:15], v[20:21], v[14:15] op_sel_hi:[0,1]
	v_exp_f32_e32 v14, v14
	v_exp_f32_e32 v15, v15
	v_pk_mul_f32 v[16:17], v[20:21], v[16:17] op_sel_hi:[0,1]
	v_exp_f32_e32 v16, v16
	v_exp_f32_e32 v17, v17
	v_pk_mul_f32 v[10:11], v[20:21], v[10:11] op_sel_hi:[0,1]
	v_exp_f32_e32 v10, v10
	v_exp_f32_e32 v11, v11
	v_pk_mul_f32 v[12:13], v[20:21], v[12:13] op_sel_hi:[0,1]
	v_exp_f32_e32 v12, v12
	v_exp_f32_e32 v13, v13
	v_pk_mul_f32 v[6:7], v[20:21], v[6:7] op_sel_hi:[0,1]
	v_mul_f32_e32 v22, v20, v22
	v_pk_mul_f32 v[14:15], v[14:15], v[26:27]
	v_exp_f32_e32 v6, v6
	v_exp_f32_e32 v7, v7
	v_pk_mul_f32 v[8:9], v[20:21], v[8:9] op_sel_hi:[0,1]
	s_waitcnt lgkmcnt(8)
	v_pk_fma_f32 v[14:15], v[22:23], v[30:31], v[14:15] op_sel_hi:[0,1,1]
	v_pk_mul_f32 v[16:17], v[16:17], v[64:65]
	v_exp_f32_e32 v8, v8
	v_exp_f32_e32 v9, v9
	v_pk_mul_f32 v[2:3], v[20:21], v[2:3] op_sel_hi:[0,1]
	s_waitcnt lgkmcnt(4)
	v_pk_fma_f32 v[14:15], v[46:47], v[14:15], 0 op_sel_hi:[1,1,0]
	v_pk_fma_f32 v[16:17], v[22:23], v[32:33], v[16:17] op_sel_hi:[0,1,1]
	v_pk_mul_f32 v[10:11], v[10:11], v[72:73]
	v_exp_f32_e32 v2, v2
	v_exp_f32_e32 v3, v3
	v_pk_mul_f32 v[4:5], v[20:21], v[4:5] op_sel_hi:[0,1]
	v_pk_fma_f32 v[14:15], v[48:49], v[16:17], v[14:15]
	v_pk_fma_f32 v[10:11], v[22:23], v[34:35], v[10:11] op_sel_hi:[0,1,1]
	v_pk_mul_f32 v[12:13], v[12:13], v[74:75]
	v_exp_f32_e32 v4, v4
	v_exp_f32_e32 v5, v5
	s_waitcnt lgkmcnt(3)
	v_pk_fma_f32 v[10:11], v[50:51], v[10:11], v[14:15]
	v_pk_fma_f32 v[12:13], v[22:23], v[36:37], v[12:13] op_sel_hi:[0,1,1]
	v_pk_mul_f32 v[6:7], v[6:7], v[76:77]
	v_pk_fma_f32 v[10:11], v[52:53], v[12:13], v[10:11]
	v_pk_fma_f32 v[6:7], v[22:23], v[38:39], v[6:7] op_sel_hi:[0,1,1]
	v_pk_mul_f32 v[8:9], v[8:9], v[78:79]
	s_waitcnt lgkmcnt(2)
	v_pk_fma_f32 v[6:7], v[54:55], v[6:7], v[10:11]
	v_pk_fma_f32 v[8:9], v[22:23], v[40:41], v[8:9] op_sel_hi:[0,1,1]
	v_pk_mul_f32 v[2:3], v[2:3], v[80:81]
	v_pk_fma_f32 v[6:7], v[56:57], v[8:9], v[6:7]
	v_pk_fma_f32 v[2:3], v[22:23], v[42:43], v[2:3] op_sel_hi:[0,1,1]
	v_pk_mul_f32 v[4:5], v[4:5], v[18:19]
	s_waitcnt lgkmcnt(1)
	v_pk_fma_f32 v[2:3], v[58:59], v[2:3], v[6:7]
	v_pk_fma_f32 v[4:5], v[22:23], v[44:45], v[4:5] op_sel_hi:[0,1,1]
	v_pk_fma_f32 v[2:3], v[60:61], v[4:5], v[2:3]
	s_nop 0
	v_add_f32_e32 v2, v2, v3
	v_fma_mix_f32 v2, v69, v21, v2 op_sel:[0,1,0] op_sel_hi:[0,1,0]
	v_fma_mixlo_f16 v2, v2, v25, 0 op_sel:[0,1,0] op_sel_hi:[0,1,0]
	ds_write_b16 v70, v2 offset:36336
	v_lshlrev_b32_e32 v2, 9, v0
	v_and_b32_e32 v2, 0x38000, v2
	v_mov_b32_e32 v3, v67
	v_and_b32_e32 v28, 63, v0
	v_lshl_add_u64 v[2:3], s[6:7], 0, v[2:3]
	v_lshlrev_b32_e32 v18, 4, v28
	v_mov_b32_e32 v19, v67
	s_bfe_u32 s6, s2, 0x40003
	v_lshl_add_u64 v[20:21], v[2:3], 0, v[18:19]
	s_lshl_b32 s26, s6, 10
	v_lshl_add_u64 v[2:3], v[20:21], 0, s[26:27]
	v_add_co_u32_e64 v4, s[2:3], s20, v2
	s_lshl_b32 s4, s6, 6
	s_nop 0
	v_addc_co_u32_e64 v5, s[2:3], 0, v3, s[2:3]
	s_add_i32 s2, s4, 64
	s_and_b32 s3, s2, 0x3c0
	s_lshl_b32 s26, s3, 4
	s_lshl_b32 s2, s2, 4
	global_load_dwordx4 v[30:33], v[2:3], off
	global_load_dwordx4 v[34:37], v[4:5], off
	v_lshl_add_u64 v[2:3], v[20:21], 0, s[26:27]
	s_or_b32 s26, s2, 0x4000
	s_add_i32 s2, s4, 0x80
	s_and_b32 s3, s2, 0x3c0
	v_lshl_add_u64 v[4:5], v[20:21], 0, s[26:27]
	s_lshl_b32 s26, s3, 4
	s_lshl_b32 s2, s2, 4
	global_load_dwordx4 v[38:41], v[2:3], off
	global_load_dwordx4 v[42:45], v[4:5], off
	v_lshl_add_u64 v[2:3], v[20:21], 0, s[26:27]
	s_or_b32 s26, s2, 0x4000
	s_add_i32 s2, s4, 0xc0
	s_and_b32 s3, s2, 0x3c0
	v_lshl_add_u64 v[4:5], v[20:21], 0, s[26:27]
	s_lshl_b32 s26, s3, 4
	s_lshl_b32 s2, s2, 4
	global_load_dwordx4 v[46:49], v[2:3], off
	global_load_dwordx4 v[50:53], v[4:5], off
	v_lshl_add_u64 v[2:3], v[20:21], 0, s[26:27]
	s_or_b32 s26, s2, 0x4000
	s_add_i32 s2, s4, 0x100
	s_and_b32 s3, s2, 0x3c0
	v_lshl_add_u64 v[4:5], v[20:21], 0, s[26:27]
	s_lshl_b32 s26, s3, 4
	s_lshl_b32 s2, s2, 4
	global_load_dwordx4 v[54:57], v[2:3], off
	global_load_dwordx4 v[58:61], v[4:5], off
	v_lshl_add_u64 v[2:3], v[20:21], 0, s[26:27]
	s_or_b32 s26, s2, 0x4000
	s_add_i32 s2, s4, 0x140
	s_and_b32 s3, s2, 0x3c0
	v_lshl_add_u64 v[4:5], v[20:21], 0, s[26:27]
	s_lshl_b32 s26, s3, 4
	s_lshl_b32 s2, s2, 4
	global_load_dwordx4 v[62:65], v[2:3], off
	global_load_dwordx4 v[70:73], v[4:5], off
	v_lshl_add_u64 v[2:3], v[20:21], 0, s[26:27]
	s_or_b32 s26, s2, 0x4000
	s_add_i32 s2, s4, 0x180
	s_and_b32 s3, s2, 0x3c0
	v_lshl_add_u64 v[4:5], v[20:21], 0, s[26:27]
	s_lshl_b32 s26, s3, 4
	s_lshl_b32 s2, s2, 4
	global_load_dwordx4 v[74:77], v[2:3], off
	global_load_dwordx4 v[78:81], v[4:5], off
	v_lshl_add_u64 v[2:3], v[20:21], 0, s[26:27]
	s_or_b32 s26, s2, 0x4000
	s_add_i32 s2, s4, 0x1c0
	s_and_b32 s3, s2, 0x3c0
	v_lshl_add_u64 v[4:5], v[20:21], 0, s[26:27]
	s_lshl_b32 s26, s3, 4
	s_lshl_b32 s2, s2, 4
	v_lshl_add_u64 v[22:23], v[20:21], 0, s[26:27]
	s_or_b32 s26, s2, 0x4000
	s_xor_b32 s5, s4, 0x200
	v_lshl_add_u64 v[24:25], v[20:21], 0, s[26:27]
	s_lshl_b32 s26, s5, 4
	global_load_dwordx4 v[14:17], v[2:3], off
	global_load_dwordx4 v[10:13], v[4:5], off
	global_load_dwordx4 v[6:9], v[22:23], off
	s_nop 0
	global_load_dwordx4 v[2:5], v[24:25], off
	v_lshl_add_u64 v[22:23], v[20:21], 0, s[26:27]
	v_add_co_u32_e64 v24, s[2:3], s20, v22
	s_waitcnt lgkmcnt(0)
	s_barrier
	v_addc_co_u32_e64 v25, s[2:3], 0, v23, s[2:3]
	global_load_dwordx4 v[82:85], v[22:23], off
	global_load_dwordx4 v[86:89], v[24:25], off
	v_lshrrev_b32_e32 v19, 6, v0
	v_and_b32_e32 v29, 15, v0
	v_lshlrev_b32_e32 v22, 7, v19
	v_mov_b32_e32 v23, v67
	v_and_b32_e32 v90, 48, v0
	s_movk_i32 s2, 0x410
	v_or_b32_e32 v26, s24, v29
	v_lshl_add_u64 v[24:25], s[28:29], 0, v[22:23]
	v_mov_b32_e32 v91, v67
	v_mov_b32_e32 v27, v67
	v_mad_u32_u24 v23, v29, s2, v90
	v_lshl_add_u64 v[98:99], v[24:25], 0, v[90:91]
	v_lshlrev_b64 v[24:25], 10, v[26:27]
	v_add_u32_e32 v27, s4, v23
	ds_read_b128 v[90:93], v27 offset:4096
	ds_read_b128 v[94:97], v27 offset:20736
	v_or_b32_e32 v26, 16, v26
	v_mov_b32_e32 v27, v67
	v_lshlrev_b64 v[26:27], 10, v[26:27]
	v_lshl_add_u64 v[24:25], v[98:99], 0, v[24:25]
	v_lshl_add_u64 v[26:27], v[98:99], 0, v[26:27]
	s_lshl_b32 s3, s6, 5
	s_setprio 1
	s_waitcnt vmcnt(17) lgkmcnt(1)
	v_mfma_f32_16x16x32_f16 v[98:101], v[30:33], v[90:93], 0
	s_waitcnt lgkmcnt(0)
	v_mfma_f32_16x16x32_f16 v[30:33], v[30:33], v[94:97], 0
	s_waitcnt vmcnt(16)
	v_mfma_f32_16x16x32_f16 v[90:93], v[34:37], v[90:93], 0
	v_mfma_f32_16x16x32_f16 v[34:37], v[34:37], v[94:97], 0
	s_setprio 0
	s_add_i32 s6, s4, 0x240
	s_and_b32 s7, s6, 0x3c0
	s_lshl_b32 s26, s7, 4
	s_lshl_b32 s6, s6, 4
	v_lshl_add_u64 v[106:107], v[20:21], 0, s[26:27]
	s_or_b32 s26, s6, 0x4000
	v_lshl_add_u64 v[108:109], v[20:21], 0, s[26:27]
	global_load_dwordx4 v[94:97], v[106:107], off
	global_load_dwordx4 v[102:105], v[108:109], off
	s_add_i32 s6, s3, 32
	s_and_b32 s6, s6, 0x1e0
	v_lshl_add_u32 v29, s6, 1, v23
	ds_read_b128 v[106:109], v29 offset:4096
	ds_read_b128 v[110:113], v29 offset:20736
	s_setprio 1
	s_waitcnt vmcnt(17) lgkmcnt(1)
	v_mfma_f32_16x16x32_f16 v[98:101], v[38:41], v[106:109], v[98:101]
	s_waitcnt lgkmcnt(0)
	v_mfma_f32_16x16x32_f16 v[30:33], v[38:41], v[110:113], v[30:33]
	s_waitcnt vmcnt(16)
	v_mfma_f32_16x16x32_f16 v[38:41], v[42:45], v[106:109], v[90:93]
	v_mfma_f32_16x16x32_f16 v[34:37], v[42:45], v[110:113], v[34:37]
	s_setprio 0
	s_add_i32 s6, s4, 0x280
	s_and_b32 s7, s6, 0x3c0
	s_lshl_b32 s26, s7, 4
	s_lshl_b32 s6, s6, 4
	v_lshl_add_u64 v[106:107], v[20:21], 0, s[26:27]
	s_or_b32 s26, s6, 0x4000
	v_lshl_add_u64 v[108:109], v[20:21], 0, s[26:27]
	global_load_dwordx4 v[42:45], v[106:107], off
	global_load_dwordx4 v[90:93], v[108:109], off
	s_add_i32 s6, s3, 64
	s_and_b32 s6, s6, 0x1e0
	v_lshl_add_u32 v29, s6, 1, v23
	ds_read_b128 v[106:109], v29 offset:4096
	ds_read_b128 v[110:113], v29 offset:20736
	s_setprio 1
	s_waitcnt vmcnt(17) lgkmcnt(1)
	v_mfma_f32_16x16x32_f16 v[98:101], v[46:49], v[106:109], v[98:101]
	s_waitcnt lgkmcnt(0)
	v_mfma_f32_16x16x32_f16 v[30:33], v[46:49], v[110:113], v[30:33]
	s_waitcnt vmcnt(16)
	v_mfma_f32_16x16x32_f16 v[38:41], v[50:53], v[106:109], v[38:41]
	v_mfma_f32_16x16x32_f16 v[34:37], v[50:53], v[110:113], v[34:37]
	s_setprio 0
	s_add_i32 s6, s4, 0x2c0
	s_and_b32 s7, s6, 0x3c0
	s_lshl_b32 s26, s7, 4
	s_lshl_b32 s6, s6, 4
	v_lshl_add_u64 v[106:107], v[20:21], 0, s[26:27]
	s_or_b32 s26, s6, 0x4000
	v_lshl_add_u64 v[108:109], v[20:21], 0, s[26:27]
	global_load_dwordx4 v[46:49], v[106:107], off
	global_load_dwordx4 v[50:53], v[108:109], off
	s_add_i32 s6, s3, 0x60
	s_and_b32 s6, s6, 0x1e0
	v_lshl_add_u32 v29, s6, 1, v23
	ds_read_b128 v[106:109], v29 offset:4096
	ds_read_b128 v[110:113], v29 offset:20736
	s_setprio 1
	s_waitcnt vmcnt(17) lgkmcnt(1)
	v_mfma_f32_16x16x32_f16 v[98:101], v[54:57], v[106:109], v[98:101]
	s_waitcnt lgkmcnt(0)
	v_mfma_f32_16x16x32_f16 v[30:33], v[54:57], v[110:113], v[30:33]
	s_waitcnt vmcnt(16)
	v_mfma_f32_16x16x32_f16 v[38:41], v[58:61], v[106:109], v[38:41]
	v_mfma_f32_16x16x32_f16 v[34:37], v[58:61], v[110:113], v[34:37]
	s_setprio 0
	s_add_i32 s6, s4, 0x300
	s_and_b32 s7, s6, 0x3c0
	s_lshl_b32 s26, s7, 4
	s_lshl_b32 s6, s6, 4
	v_lshl_add_u64 v[106:107], v[20:21], 0, s[26:27]
	s_or_b32 s26, s6, 0x4000
	v_lshl_add_u64 v[108:109], v[20:21], 0, s[26:27]
	global_load_dwordx4 v[54:57], v[106:107], off
	global_load_dwordx4 v[58:61], v[108:109], off
	s_add_i32 s6, s3, 0x80
	s_and_b32 s6, s6, 0x1e0
	v_lshl_add_u32 v29, s6, 1, v23
	ds_read_b128 v[106:109], v29 offset:4096
	ds_read_b128 v[110:113], v29 offset:20736
	s_setprio 1
	s_waitcnt vmcnt(17) lgkmcnt(1)
	v_mfma_f32_16x16x32_f16 v[98:101], v[62:65], v[106:109], v[98:101]
	s_waitcnt lgkmcnt(0)
	v_mfma_f32_16x16x32_f16 v[30:33], v[62:65], v[110:113], v[30:33]
	s_waitcnt vmcnt(16)
	v_mfma_f32_16x16x32_f16 v[38:41], v[70:73], v[106:109], v[38:41]
	v_mfma_f32_16x16x32_f16 v[34:37], v[70:73], v[110:113], v[34:37]
	s_setprio 0
	s_add_i32 s6, s4, 0x340
	s_and_b32 s7, s6, 0x3c0
	s_lshl_b32 s26, s7, 4
	s_lshl_b32 s6, s6, 4
	v_lshl_add_u64 v[106:107], v[20:21], 0, s[26:27]
	s_or_b32 s26, s6, 0x4000
	v_lshl_add_u64 v[108:109], v[20:21], 0, s[26:27]
	global_load_dwordx4 v[62:65], v[106:107], off
	global_load_dwordx4 v[70:73], v[108:109], off
	s_add_i32 s6, s3, 0xa0
	s_and_b32 s6, s6, 0x1e0
	v_lshl_add_u32 v29, s6, 1, v23
	ds_read_b128 v[106:109], v29 offset:4096
	ds_read_b128 v[110:113], v29 offset:20736
	s_setprio 1
	s_waitcnt vmcnt(17) lgkmcnt(1)
	v_mfma_f32_16x16x32_f16 v[98:101], v[74:77], v[106:109], v[98:101]
	s_waitcnt lgkmcnt(0)
	v_mfma_f32_16x16x32_f16 v[30:33], v[74:77], v[110:113], v[30:33]
	s_waitcnt vmcnt(16)
	v_mfma_f32_16x16x32_f16 v[38:41], v[78:81], v[106:109], v[38:41]
	v_mfma_f32_16x16x32_f16 v[34:37], v[78:81], v[110:113], v[34:37]
	s_setprio 0
	s_add_i32 s6, s4, 0x380
	s_and_b32 s7, s6, 0x3c0
	s_lshl_b32 s26, s7, 4
	s_lshl_b32 s6, s6, 4
	v_lshl_add_u64 v[106:107], v[20:21], 0, s[26:27]
	s_or_b32 s26, s6, 0x4000
	v_lshl_add_u64 v[108:109], v[20:21], 0, s[26:27]
	global_load_dwordx4 v[74:77], v[106:107], off
	global_load_dwordx4 v[78:81], v[108:109], off
	s_add_i32 s6, s3, 0xc0
	s_and_b32 s6, s6, 0x1e0
	v_lshl_add_u32 v29, s6, 1, v23
	ds_read_b128 v[106:109], v29 offset:4096
	ds_read_b128 v[110:113], v29 offset:20736
	s_setprio 1
	s_waitcnt vmcnt(17) lgkmcnt(1)
	v_mfma_f32_16x16x32_f16 v[98:101], v[14:17], v[106:109], v[98:101]
	s_waitcnt lgkmcnt(0)
	v_mfma_f32_16x16x32_f16 v[14:17], v[14:17], v[110:113], v[30:33]
	s_waitcnt vmcnt(16)
	v_mfma_f32_16x16x32_f16 v[30:33], v[10:13], v[106:109], v[38:41]
	v_mfma_f32_16x16x32_f16 v[10:13], v[10:13], v[110:113], v[34:37]
	s_setprio 0
	s_addk_i32 s4, 0x3c0
	s_and_b32 s6, s4, 0x3c0
	s_lshl_b32 s26, s6, 4
	s_lshl_b32 s4, s4, 4
	v_lshl_add_u64 v[106:107], v[20:21], 0, s[26:27]
	s_or_b32 s26, s4, 0x4000
	v_lshl_add_u64 v[20:21], v[20:21], 0, s[26:27]
	global_load_dwordx4 v[34:37], v[106:107], off
	global_load_dwordx4 v[38:41], v[20:21], off
	s_add_i32 s4, s3, 0xe0
	s_and_b32 s4, s4, 0x1e0
	v_lshl_add_u32 v20, s4, 1, v23
	ds_read_b128 v[106:109], v20 offset:4096
	ds_read_b128 v[110:113], v20 offset:20736
	s_setprio 1
	s_waitcnt vmcnt(17) lgkmcnt(1)
	v_mfma_f32_16x16x32_f16 v[98:101], v[6:9], v[106:109], v[98:101]
	s_waitcnt lgkmcnt(0)
	v_mfma_f32_16x16x32_f16 v[6:9], v[6:9], v[110:113], v[14:17]
	s_waitcnt vmcnt(16)
	v_mfma_f32_16x16x32_f16 v[14:17], v[2:5], v[106:109], v[30:33]
	v_mfma_f32_16x16x32_f16 v[2:5], v[2:5], v[110:113], v[10:13]
	s_setprio 0
	v_add_u32_e32 v20, s5, v23
	s_nop 0
	ds_read_b128 v[10:13], v20 offset:4096
	ds_read_b128 v[30:33], v20 offset:20736
	s_setprio 1
	s_waitcnt vmcnt(15) lgkmcnt(1)
	v_mfma_f32_16x16x32_f16 v[98:101], v[82:85], v[10:13], v[98:101]
	s_waitcnt vmcnt(14)
	v_mfma_f32_16x16x32_f16 v[10:13], v[86:89], v[10:13], v[14:17]
	s_waitcnt lgkmcnt(0)
	v_mfma_f32_16x16x32_f16 v[6:9], v[82:85], v[30:33], v[6:9]
	v_mfma_f32_16x16x32_f16 v[2:5], v[86:89], v[30:33], v[2:5]
	s_setprio 0
	s_add_i32 s4, s3, 0x120
	s_and_b32 s4, s4, 0x1e0
	v_lshl_add_u32 v20, s4, 1, v23
	ds_read_b128 v[14:17], v20 offset:4096
	ds_read_b128 v[30:33], v20 offset:20736
	s_setprio 1
	s_waitcnt vmcnt(12) lgkmcnt(1)
	v_mfma_f32_16x16x32_f16 v[10:13], v[102:105], v[14:17], v[10:13]
	v_mfma_f32_16x16x32_f16 v[82:85], v[94:97], v[14:17], v[98:101]
	s_waitcnt lgkmcnt(0)
	v_mfma_f32_16x16x32_f16 v[6:9], v[94:97], v[30:33], v[6:9]
	v_mfma_f32_16x16x32_f16 v[2:5], v[102:105], v[30:33], v[2:5]
	s_setprio 0
	s_add_i32 s4, s3, 0x140
	s_and_b32 s4, s4, 0x1e0
	v_lshl_add_u32 v20, s4, 1, v23
	ds_read_b128 v[14:17], v20 offset:4096
	ds_read_b128 v[30:33], v20 offset:20736
	s_setprio 1
	s_waitcnt vmcnt(10) lgkmcnt(1)
	v_mfma_f32_16x16x32_f16 v[10:13], v[90:93], v[14:17], v[10:13]
	v_mfma_f32_16x16x32_f16 v[82:85], v[42:45], v[14:17], v[82:85]
	s_waitcnt lgkmcnt(0)
	v_mfma_f32_16x16x32_f16 v[6:9], v[42:45], v[30:33], v[6:9]
	v_mfma_f32_16x16x32_f16 v[2:5], v[90:93], v[30:33], v[2:5]
	s_setprio 0
	s_add_i32 s4, s3, 0x160
	s_and_b32 s4, s4, 0x1e0
	v_lshl_add_u32 v20, s4, 1, v23
	ds_read_b128 v[14:17], v20 offset:4096
	ds_read_b128 v[30:33], v20 offset:20736
	s_setprio 1
	s_waitcnt vmcnt(8) lgkmcnt(1)
	v_mfma_f32_16x16x32_f16 v[10:13], v[50:53], v[14:17], v[10:13]
	v_mfma_f32_16x16x32_f16 v[42:45], v[46:49], v[14:17], v[82:85]
	s_waitcnt lgkmcnt(0)
	v_mfma_f32_16x16x32_f16 v[6:9], v[46:49], v[30:33], v[6:9]
	v_mfma_f32_16x16x32_f16 v[2:5], v[50:53], v[30:33], v[2:5]
	s_setprio 0
	s_add_i32 s4, s3, 0x180
	s_and_b32 s4, s4, 0x1e0
	v_lshl_add_u32 v20, s4, 1, v23
	ds_read_b128 v[14:17], v20 offset:4096
	ds_read_b128 v[30:33], v20 offset:20736
	s_setprio 1
	s_waitcnt vmcnt(6) lgkmcnt(1)
	v_mfma_f32_16x16x32_f16 v[10:13], v[58:61], v[14:17], v[10:13]
	v_mfma_f32_16x16x32_f16 v[42:45], v[54:57], v[14:17], v[42:45]
	s_waitcnt lgkmcnt(0)
	v_mfma_f32_16x16x32_f16 v[6:9], v[54:57], v[30:33], v[6:9]
	v_mfma_f32_16x16x32_f16 v[2:5], v[58:61], v[30:33], v[2:5]
	s_setprio 0
	s_add_i32 s4, s3, 0x1a0
	s_and_b32 s4, s4, 0x1e0
	v_lshl_add_u32 v20, s4, 1, v23
	ds_read_b128 v[14:17], v20 offset:4096
	ds_read_b128 v[30:33], v20 offset:20736
	s_setprio 1
	s_waitcnt vmcnt(4) lgkmcnt(1)
	v_mfma_f32_16x16x32_f16 v[10:13], v[70:73], v[14:17], v[10:13]
	v_mfma_f32_16x16x32_f16 v[42:45], v[62:65], v[14:17], v[42:45]
	s_waitcnt lgkmcnt(0)
	v_mfma_f32_16x16x32_f16 v[6:9], v[62:65], v[30:33], v[6:9]
	v_mfma_f32_16x16x32_f16 v[2:5], v[70:73], v[30:33], v[2:5]
	s_setprio 0
	s_add_i32 s4, s3, 0x1c0
	s_and_b32 s4, s4, 0x1e0
	v_lshl_add_u32 v20, s4, 1, v23
	ds_read_b128 v[14:17], v20 offset:4096
	ds_read_b128 v[30:33], v20 offset:20736
	s_setprio 1
	s_waitcnt vmcnt(2) lgkmcnt(1)
	v_mfma_f32_16x16x32_f16 v[10:13], v[78:81], v[14:17], v[10:13]
	v_mfma_f32_16x16x32_f16 v[42:45], v[74:77], v[14:17], v[42:45]
	s_waitcnt lgkmcnt(0)
	v_mfma_f32_16x16x32_f16 v[6:9], v[74:77], v[30:33], v[6:9]
	v_mfma_f32_16x16x32_f16 v[2:5], v[78:81], v[30:33], v[2:5]
	s_setprio 0
	s_addk_i32 s3, 0x1e0
	s_and_b32 s3, s3, 0x1e0
	v_lshl_add_u32 v20, s3, 1, v23
	ds_read_b128 v[14:17], v20 offset:4096
	ds_read_b128 v[30:33], v20 offset:20736
	s_setprio 1
	s_waitcnt vmcnt(1) lgkmcnt(1)
	v_mfma_f32_16x16x32_f16 v[42:45], v[34:37], v[14:17], v[42:45]
	s_waitcnt vmcnt(0)
	v_mfma_f32_16x16x32_f16 v[14:17], v[38:41], v[14:17], v[10:13]
	s_waitcnt lgkmcnt(0)
	v_mfma_f32_16x16x32_f16 v[34:37], v[34:37], v[30:33], v[6:9]
	v_mfma_f32_16x16x32_f16 v[30:33], v[38:41], v[30:33], v[2:5]
	s_setprio 0
	v_lshlrev_b32_e32 v13, 2, v19
	s_movk_i32 s3, 0x1040
	v_add_u32_e32 v12, v23, v22
	v_mov_b32_e32 v21, v67
	v_mov_b32_e32 v23, v67
	v_mad_u32_u24 v29, v19, s3, v18
	v_add_u32_e32 v20, s24, v13
	v_or_b32_e32 v19, 2, v13
	v_add_u32_e32 v22, v68, v13
	global_load_dwordx4 v[2:5], v18, s[12:13]
	global_load_dwordx4 v[6:9], v18, s[14:15]
	v_lshl_add_u64 v[26:27], v[20:21], 2, s[10:11]
	v_mad_u32_u24 v60, v19, s2, v18
	v_lshl_add_u64 v[58:59], v[22:23], 2, s[10:11]
	s_mov_b32 s4, 0x3727c5ac
	v_mov_b64_e32 v[10:11], s[4:5]
	s_mov_b32 s6, 0x3b800000
	s_mov_b32 s7, 0x800000
	s_waitcnt vmcnt(5)
	v_pk_add_f32 v[18:19], v[160:161], v[42:43]
	v_pk_add_f32 v[20:21], v[162:163], v[44:45]
	s_waitcnt vmcnt(4)
	v_pk_add_f32 v[14:15], v[164:165], v[14:15]
	v_pk_add_f32 v[16:17], v[166:167], v[16:17]
	s_waitcnt vmcnt(3)
	v_pk_add_f32 v[22:23], v[168:169], v[34:35]
	v_pk_add_f32 v[24:25], v[170:171], v[36:37]
	s_waitcnt vmcnt(2)
	v_pk_add_f32 v[30:31], v[172:173], v[30:31]
	v_pk_add_f32 v[32:33], v[174:175], v[32:33]
	ds_write_b128 v12, v[18:21] offset:37376
	ds_write_b128 v12, v[14:17] offset:37440
	ds_write_b128 v12, v[22:25] offset:54016
	ds_write_b128 v12, v[30:33] offset:54080
	s_waitcnt lgkmcnt(0)
	s_barrier
	ds_read_b128 v[14:17], v29 offset:37376
	ds_read_b128 v[18:21], v29 offset:38416
	ds_read_b128 v[22:25], v60 offset:37376
	global_load_dwordx2 v[30:31], v[26:27], off
	global_load_dwordx2 v[32:33], v[58:59], off offset:8
	s_waitcnt lgkmcnt(2)
	v_add_f32_e32 v12, v14, v15
	s_waitcnt lgkmcnt(1)
	v_add_f32_e32 v26, v18, v19
	s_waitcnt lgkmcnt(0)
	v_add_f32_e32 v27, v22, v23
	v_add_f32_e32 v12, v12, v16
	v_add_f32_e32 v26, v26, v20
	v_add_f32_e32 v27, v27, v24
	v_add_f32_e32 v12, v12, v17
	v_add_f32_e32 v26, v26, v21
	v_add_f32_e32 v27, v27, v25
	v_add_f32_dpp v12, v12, v12 quad_perm:[1,0,3,2] row_mask:0xf bank_mask:0xf bound_ctrl:1
	v_add_f32_dpp v26, v26, v26 quad_perm:[1,0,3,2] row_mask:0xf bank_mask:0xf bound_ctrl:1
	v_add_f32_dpp v27, v27, v27 quad_perm:[1,0,3,2] row_mask:0xf bank_mask:0xf bound_ctrl:1
	v_add_f32_dpp v12, v12, v12 quad_perm:[2,3,0,1] row_mask:0xf bank_mask:0xf bound_ctrl:1
	v_add_f32_dpp v26, v26, v26 quad_perm:[2,3,0,1] row_mask:0xf bank_mask:0xf bound_ctrl:1
	v_add_f32_dpp v27, v27, v27 quad_perm:[2,3,0,1] row_mask:0xf bank_mask:0xf bound_ctrl:1
	v_add_f32_dpp v12, v12, v12 row_half_mirror row_mask:0xf bank_mask:0xf bound_ctrl:1
	v_add_f32_dpp v26, v26, v26 row_half_mirror row_mask:0xf bank_mask:0xf bound_ctrl:1
	v_add_f32_dpp v27, v27, v27 row_half_mirror row_mask:0xf bank_mask:0xf bound_ctrl:1
	v_add_f32_dpp v12, v12, v12 row_mirror row_mask:0xf bank_mask:0xf bound_ctrl:1
	v_add_f32_dpp v26, v26, v26 row_mirror row_mask:0xf bank_mask:0xf bound_ctrl:1
	v_add_f32_dpp v27, v27, v27 row_mirror row_mask:0xf bank_mask:0xf bound_ctrl:1
	v_readlane_b32 s10, v12, 16
	v_readlane_b32 s11, v12, 48
	v_readlane_b32 s12, v26, 16
	v_readlane_b32 s13, v26, 48
	v_readlane_b32 s2, v12, 0
	v_readlane_b32 s3, v12, 32
	v_readlane_b32 s4, v26, 0
	v_readlane_b32 s5, v26, 32
	v_readlane_b32 s8, v27, 0
	v_readlane_b32 s14, v27, 16
	v_readlane_b32 s9, v27, 32
	v_readlane_b32 s15, v27, 48
	v_mov_b32_e32 v26, s10
	v_mov_b32_e32 v27, s11
	v_mov_b32_e32 v34, s12
	v_mov_b32_e32 v35, s13
	v_mov_b32_e32 v36, s14
	v_mov_b32_e32 v37, s15
	v_pk_add_f32 v[26:27], s[2:3], v[26:27]
	v_pk_add_f32 v[34:35], s[4:5], v[34:35]
	v_pk_add_f32 v[36:37], s[8:9], v[36:37]
	v_add_f32_e32 v12, v26, v27
	v_add_f32_e32 v26, v34, v35
	v_add_f32_e32 v27, v36, v37
	v_mul_f32_e32 v12, 0x3b800000, v12
	v_mul_f32_e32 v26, 0x3b800000, v26
	v_pk_add_f32 v[14:15], v[14:15], v[12:13] op_sel_hi:[1,0] neg_lo:[0,1] neg_hi:[0,1]
	v_pk_add_f32 v[18:19], v[18:19], v[26:27] op_sel_hi:[1,0] neg_lo:[0,1] neg_hi:[0,1]
	v_mul_f32_e32 v34, 0x3b800000, v27
	v_pk_add_f32 v[16:17], v[16:17], v[12:13] op_sel_hi:[1,0] neg_lo:[0,1] neg_hi:[0,1]
	v_pk_add_f32 v[20:21], v[20:21], v[26:27] op_sel_hi:[1,0] neg_lo:[0,1] neg_hi:[0,1]
	v_pk_mul_f32 v[26:27], v[14:15], v[14:15]
	v_pk_mul_f32 v[36:37], v[18:19], v[18:19]
	v_pk_add_f32 v[22:23], v[22:23], v[34:35] op_sel_hi:[1,0] neg_lo:[0,1] neg_hi:[0,1]
	v_pk_add_f32 v[24:25], v[24:25], v[34:35] op_sel_hi:[1,0] neg_lo:[0,1] neg_hi:[0,1]
	v_pk_mul_f32 v[34:35], v[16:17], v[16:17]
	v_pk_mul_f32 v[38:39], v[20:21], v[20:21]
	v_add_f32_e32 v12, v26, v27
	v_add_f32_e32 v26, v36, v37
	v_add_f32_e32 v12, v34, v12
	v_add_f32_e32 v26, v38, v26
	v_add_f32_e32 v12, v35, v12
	v_add_f32_e32 v26, v39, v26
	v_pk_mul_f32 v[40:41], v[22:23], v[22:23]
	v_add_f32_dpp v12, v12, v12 quad_perm:[1,0,3,2] row_mask:0xf bank_mask:0xf bound_ctrl:1
	v_add_f32_dpp v26, v26, v26 quad_perm:[1,0,3,2] row_mask:0xf bank_mask:0xf bound_ctrl:1
	s_nop 0
	v_add_f32_dpp v12, v12, v12 quad_perm:[2,3,0,1] row_mask:0xf bank_mask:0xf bound_ctrl:1
	v_add_f32_dpp v26, v26, v26 quad_perm:[2,3,0,1] row_mask:0xf bank_mask:0xf bound_ctrl:1
	s_nop 0
	v_add_f32_dpp v12, v12, v12 row_half_mirror row_mask:0xf bank_mask:0xf bound_ctrl:1
	v_add_f32_dpp v26, v26, v26 row_half_mirror row_mask:0xf bank_mask:0xf bound_ctrl:1
	s_nop 0
	v_add_f32_dpp v12, v12, v12 row_mirror row_mask:0xf bank_mask:0xf bound_ctrl:1
	v_add_f32_dpp v26, v26, v26 row_mirror row_mask:0xf bank_mask:0xf bound_ctrl:1
	v_readlane_b32 s8, v12, 16
	v_readlane_b32 s9, v12, 48
	v_readlane_b32 s10, v26, 16
	v_readlane_b32 s11, v26, 48
	v_readlane_b32 s2, v12, 0
	v_readlane_b32 s3, v12, 32
	v_readlane_b32 s4, v26, 0
	v_readlane_b32 s5, v26, 32
	v_mov_b32_e32 v26, s8
	v_mov_b32_e32 v27, s9
	v_mov_b32_e32 v34, s10
	v_mov_b32_e32 v35, s11
	v_pk_add_f32 v[26:27], s[2:3], v[26:27]
	v_pk_add_f32 v[34:35], s[4:5], v[34:35]
	v_mov_b32_e32 v37, v26
	v_mov_b32_e32 v36, v34
	v_mov_b32_e32 v26, v35
	v_pk_add_f32 v[26:27], v[36:37], v[26:27]
	v_add_f32_e32 v36, v40, v41
	v_pk_fma_f32 v[26:27], v[26:27], s[6:7], v[10:11] op_sel_hi:[1,0,0]
	s_nop 0
	v_mul_f32_e32 v12, 0x4b800000, v27
	v_cmp_gt_f32_e64 s[2:3], s7, v27
	v_mul_f32_e32 v34, 0x4b800000, v26
	v_cmp_gt_f32_e64 s[4:5], s7, v26
	v_cndmask_b32_e64 v12, v27, v12, s[2:3]
	v_rsq_f32_e32 v12, v12
	v_cndmask_b32_e64 v26, v26, v34, s[4:5]
	v_rsq_f32_e32 v34, v26
	v_pk_mul_f32 v[26:27], v[24:25], v[24:25]
	v_mul_f32_e32 v35, 0x45800000, v12
	v_cndmask_b32_e64 v12, v12, v35, s[2:3]
	v_mul_f32_e32 v37, 0x45800000, v34
	v_cndmask_b32_e64 v34, v34, v37, s[4:5]
	v_pk_mul_f32 v[14:15], v[14:15], v[12:13] op_sel_hi:[1,0]
	v_pk_mul_f32 v[16:17], v[16:17], v[12:13] op_sel_hi:[1,0]
	s_waitcnt vmcnt(1)
	v_cmp_eq_u32_e64 s[2:3], 0, v30
	v_pk_mul_f32 v[18:19], v[18:19], v[34:35] op_sel_hi:[1,0]
	v_pk_mul_f32 v[20:21], v[20:21], v[34:35] op_sel_hi:[1,0]
	v_pk_fma_f32 v[34:35], v[2:3], v[14:15], v[6:7]
	v_pk_fma_f32 v[16:17], v[4:5], v[16:17], v[8:9]
	v_cndmask_b32_e64 v12, 1.0, 0, s[2:3]
	v_cmp_eq_u32_e64 s[2:3], 0, v31
	v_pk_fma_f32 v[18:19], v[2:3], v[18:19], v[6:7]
	v_pk_fma_f32 v[20:21], v[4:5], v[20:21], v[8:9]
	v_cndmask_b32_e64 v14, 1.0, 0, s[2:3]
	v_pk_fma_f32 v[30:31], v[12:13], v[34:35], 0 op_sel_hi:[0,1,0]
	v_pk_fma_f32 v[16:17], v[12:13], v[16:17], 0 op_sel_hi:[0,1,0]
	v_pk_fma_f32 v[30:31], v[14:15], v[18:19], v[30:31] op_sel_hi:[0,1,1]
	v_pk_fma_f32 v[20:21], v[14:15], v[20:21], v[16:17] op_sel_hi:[0,1,1]
	v_add_f32_e32 v15, v26, v36
	v_add_f32_e32 v15, v27, v15
	ds_read_b128 v[16:19], v29 offset:40496
	s_waitcnt lgkmcnt(0)
	v_add_f32_dpp v15, v15, v15 quad_perm:[1,0,3,2] row_mask:0xf bank_mask:0xf bound_ctrl:1
	s_barrier
	s_nop 0
	v_add_f32_dpp v15, v15, v15 quad_perm:[2,3,0,1] row_mask:0xf bank_mask:0xf bound_ctrl:1
	s_nop 1
	v_add_f32_dpp v15, v15, v15 row_half_mirror row_mask:0xf bank_mask:0xf bound_ctrl:1
	s_nop 1
	v_add_f32_dpp v15, v15, v15 row_mirror row_mask:0xf bank_mask:0xf bound_ctrl:1
	s_nop 0
	v_readlane_b32 s2, v15, 0
	v_readlane_b32 s4, v15, 16
	v_readlane_b32 s3, v15, 32
	v_readlane_b32 s5, v15, 48
	v_add_f32_e32 v15, v16, v17
	v_add_f32_e32 v15, v15, v18
	v_add_f32_e32 v15, v15, v19
	v_mov_b32_e32 v26, s4
	v_mov_b32_e32 v27, s5
	v_add_f32_dpp v15, v15, v15 quad_perm:[1,0,3,2] row_mask:0xf bank_mask:0xf bound_ctrl:1
	v_pk_add_f32 v[26:27], s[2:3], v[26:27]
	s_nop 0
	v_add_f32_dpp v15, v15, v15 quad_perm:[2,3,0,1] row_mask:0xf bank_mask:0xf bound_ctrl:1
	s_nop 1
	v_add_f32_dpp v15, v15, v15 row_half_mirror row_mask:0xf bank_mask:0xf bound_ctrl:1
	s_nop 1
	v_add_f32_dpp v15, v15, v15 row_mirror row_mask:0xf bank_mask:0xf bound_ctrl:1
	s_nop 0
	v_readlane_b32 s4, v15, 16
	v_readlane_b32 s5, v15, 48
	v_readlane_b32 s2, v15, 0
	v_readlane_b32 s3, v15, 32
	v_mov_b32_e32 v34, s4
	v_mov_b32_e32 v35, s5
	v_pk_add_f32 v[34:35], s[2:3], v[34:35]
	s_nop 0
	v_add_f32_e32 v15, v34, v35
	v_mul_f32_e32 v34, 0x3b800000, v15
	v_pk_add_f32 v[36:37], v[16:17], v[34:35] op_sel_hi:[1,0] neg_lo:[0,1] neg_hi:[0,1]
	v_pk_add_f32 v[18:19], v[18:19], v[34:35] op_sel_hi:[1,0] neg_lo:[0,1] neg_hi:[0,1]
	v_pk_mul_f32 v[16:17], v[36:37], v[36:37]
	v_pk_mul_f32 v[34:35], v[18:19], v[18:19]
	v_add_f32_e32 v15, v16, v17
	v_add_f32_e32 v15, v34, v15
	v_add_f32_e32 v15, v35, v15
	v_mov_b32_e32 v35, v26
	s_nop 0
	v_add_f32_dpp v15, v15, v15 quad_perm:[1,0,3,2] row_mask:0xf bank_mask:0xf bound_ctrl:1
	s_nop 1
	v_add_f32_dpp v15, v15, v15 quad_perm:[2,3,0,1] row_mask:0xf bank_mask:0xf bound_ctrl:1
	s_nop 1
	v_add_f32_dpp v15, v15, v15 row_half_mirror row_mask:0xf bank_mask:0xf bound_ctrl:1
	s_nop 1
	v_add_f32_dpp v15, v15, v15 row_mirror row_mask:0xf bank_mask:0xf bound_ctrl:1
	s_nop 0
	v_readlane_b32 s4, v15, 16
	v_readlane_b32 s5, v15, 48
	v_readlane_b32 s2, v15, 0
	v_readlane_b32 s3, v15, 32
	v_mov_b32_e32 v16, s4
	v_mov_b32_e32 v17, s5
	v_pk_add_f32 v[16:17], s[2:3], v[16:17]
	s_waitcnt vmcnt(0)
	v_cmp_eq_u32_e64 s[4:5], 0, v32
	v_mov_b32_e32 v34, v16
	v_mov_b32_e32 v26, v17
	v_pk_add_f32 v[16:17], v[34:35], v[26:27]
	s_nop 0
	v_pk_fma_f32 v[26:27], v[16:17], s[6:7], v[10:11] op_sel_hi:[1,0,0]
	s_nop 0
	v_mul_f32_e32 v10, 0x4b800000, v27
	v_cmp_gt_f32_e64 s[2:3], s7, v27
	s_nop 1
	v_cndmask_b32_e64 v10, v27, v10, s[2:3]
	v_rsq_f32_e32 v11, v10
	v_cndmask_b32_e64 v10, 1.0, 0, s[4:5]
	v_cmp_eq_u32_e64 s[4:5], 0, v33
	v_mul_f32_e32 v15, 0x45800000, v11
	v_cndmask_b32_e64 v32, v11, v15, s[2:3]
	v_pk_mul_f32 v[22:23], v[22:23], v[32:33] op_sel_hi:[1,0]
	v_cmp_gt_f32_e64 s[2:3], s7, v26
	v_pk_fma_f32 v[22:23], v[2:3], v[22:23], v[6:7]
	v_pk_mul_f32 v[24:25], v[24:25], v[32:33] op_sel_hi:[1,0]
	v_pk_fma_f32 v[22:23], v[10:11], v[22:23], v[30:31] op_sel_hi:[0,1,1]
	v_mul_f32_e32 v11, 0x4b800000, v26
	v_cndmask_b32_e64 v11, v26, v11, s[2:3]
	v_rsq_f32_e32 v11, v11
	v_pk_fma_f32 v[24:25], v[4:5], v[24:25], v[8:9]
	v_cndmask_b32_e64 v16, 1.0, 0, s[4:5]
	v_mul_f32_e32 v15, 0x45800000, v11
	v_pk_fma_f32 v[20:21], v[10:11], v[24:25], v[20:21] op_sel_hi:[0,1,1]
	v_cndmask_b32_e64 v24, v11, v15, s[2:3]
	v_pk_mul_f32 v[26:27], v[36:37], v[24:25] op_sel_hi:[1,0]
	v_cmp_eq_u32_e64 s[2:3], 0, v28
	v_pk_fma_f32 v[2:3], v[2:3], v[26:27], v[6:7]
	v_pk_mul_f32 v[6:7], v[18:19], v[24:25] op_sel_hi:[1,0]
	v_pk_fma_f32 v[2:3], v[16:17], v[2:3], v[22:23] op_sel_hi:[0,1,1]
	v_pk_fma_f32 v[4:5], v[4:5], v[6:7], v[8:9]
	s_nop 0
	v_pk_fma_f32 v[4:5], v[16:17], v[4:5], v[20:21] op_sel_hi:[0,1,1]
	ds_write_b128 v66, v[2:5] offset:4096
	s_and_saveexec_b64 s[4:5], s[2:3]
	v_add_f32_e32 v2, v12, v14
	v_add_f32_e32 v2, v2, v10
	v_add_f32_e32 v2, v2, v16
	ds_write_b32 v13, v2 offset:12288
	s_or_b64 exec, exec, s[4:5]
	s_and_b32 s2, s30, 0x7ffffff
	s_waitcnt lgkmcnt(0)
	s_barrier
	s_and_saveexec_b64 s[4:5], vcc
	s_cbranch_execnz .LBB6_9
	s_or_b64 exec, exec, s[4:5]
	v_cmp_eq_u32_e32 vcc, 0, v0
	s_and_saveexec_b64 s[4:5], vcc
	s_cbranch_execnz .LBB6_10

	.amdhsa_kernel _Z4k_k2ILb1EEvPKDF16_S1_PKfS3_S3_S1_S1_PfS3_S3_S1_PDF16_PKiS4_S4_
		.amdhsa_group_segment_fixed_size 98816
		.amdhsa_private_segment_fixed_size 0
		.amdhsa_kernarg_size 120
		.amdhsa_user_sgpr_count 2
		.amdhsa_user_sgpr_dispatch_ptr 0
		.amdhsa_user_sgpr_queue_ptr 0
		.amdhsa_user_sgpr_kernarg_segment_ptr 1
		.amdhsa_user_sgpr_dispatch_id 0
		.amdhsa_user_sgpr_kernarg_preload_length 0
		.amdhsa_user_sgpr_kernarg_preload_offset 0
		.amdhsa_user_sgpr_private_segment_size 0
		.amdhsa_uses_dynamic_stack 0
		.amdhsa_enable_private_segment 0
		.amdhsa_system_sgpr_workgroup_id_x 1
		.amdhsa_system_sgpr_workgroup_id_y 0
		.amdhsa_system_sgpr_workgroup_id_z 0
		.amdhsa_system_sgpr_workgroup_info 0
		.amdhsa_system_vgpr_workitem_id 0
		.amdhsa_next_free_vgpr 196
		.amdhsa_next_free_sgpr 96
		.amdhsa_accum_offset 196
		.amdhsa_reserve_vcc 1
		.amdhsa_float_round_mode_32 0
		.amdhsa_float_round_mode_16_64 0
		.amdhsa_float_denorm_mode_32 3
		.amdhsa_float_denorm_mode_16_64 3
		.amdhsa_dx10_clamp 1
		.amdhsa_ieee_mode 1
		.amdhsa_fp16_overflow 0
		.amdhsa_tg_split 0
		.amdhsa_exception_fp_ieee_invalid_op 0
		.amdhsa_exception_fp_denorm_src 0
		.amdhsa_exception_fp_ieee_div_zero 0
		.amdhsa_exception_fp_ieee_overflow 0
		.amdhsa_exception_fp_ieee_underflow 0
		.amdhsa_exception_fp_ieee_inexact 0
		.amdhsa_exception_int_div_zero 0
	.end_amdhsa_kernel

amdhsa.kernels:
  - .agpr_count:     0
    .args:
      - .actual_access:  read_only
        .address_space:  global
        .offset:         0
        .size:           8
        .value_kind:     global_buffer
      - .actual_access:  write_only
        .address_space:  global
        .offset:         8
        .size:           8
        .value_kind:     global_buffer
      - .offset:         16
        .size:           4
        .value_kind:     by_value
      - .offset:         20
        .size:           4
        .value_kind:     by_value
      - .actual_access:  read_only
        .address_space:  global
        .offset:         24
        .size:           8
        .value_kind:     global_buffer
      - .actual_access:  write_only
        .address_space:  global
        .offset:         32
        .size:           8
        .value_kind:     global_buffer
      - .offset:         40
        .size:           4
        .value_kind:     by_value
      - .offset:         44
        .size:           4
        .value_kind:     by_value
      - .actual_access:  read_only
        .address_space:  global
        .offset:         48
        .size:           8
        .value_kind:     global_buffer
      - .actual_access:  write_only
        .address_space:  global
        .offset:         56
        .size:           8
        .value_kind:     global_buffer
      - .offset:         64
        .size:           4
        .value_kind:     by_value
      - .offset:         68
        .size:           4
        .value_kind:     by_value
      - .actual_access:  read_only
        .address_space:  global
        .offset:         72
        .size:           8
        .value_kind:     global_buffer
      - .actual_access:  write_only
        .address_space:  global
        .offset:         80
        .size:           8
        .value_kind:     global_buffer
      - .offset:         88
        .size:           4
        .value_kind:     by_value
      - .actual_access:  read_only
        .address_space:  global
        .offset:         96
        .size:           8
        .value_kind:     global_buffer
      - .actual_access:  write_only
        .address_space:  global
        .offset:         104
        .size:           8
        .value_kind:     global_buffer
      - .offset:         112
        .size:           4
        .value_kind:     by_value
      - .offset:         120
        .size:           4
        .value_kind:     hidden_block_count_x
      - .offset:         124
        .size:           4
        .value_kind:     hidden_block_count_y
      - .offset:         128
        .size:           4
        .value_kind:     hidden_block_count_z
      - .offset:         132
        .size:           2
        .value_kind:     hidden_group_size_x
      - .offset:         134
        .size:           2
        .value_kind:     hidden_group_size_y
      - .offset:         136
        .size:           2
        .value_kind:     hidden_group_size_z
      - .offset:         138
        .size:           2
        .value_kind:     hidden_remainder_x
      - .offset:         140
        .size:           2
        .value_kind:     hidden_remainder_y
      - .offset:         142
        .size:           2
        .value_kind:     hidden_remainder_z
      - .offset:         160
        .size:           8
        .value_kind:     hidden_global_offset_x
      - .offset:         168
        .size:           8
        .value_kind:     hidden_global_offset_y
      - .offset:         176
        .size:           8
        .value_kind:     hidden_global_offset_z
      - .offset:         184
        .size:           2
        .value_kind:     hidden_grid_dims
    .group_segment_fixed_size: 0
    .kernarg_segment_align: 8
    .kernarg_segment_size: 376
    .language:       OpenCL C
    .language_version:
      - 2
      - 0
    .max_flat_workgroup_size: 1024
    .name:           _Z5k_swzPKfPDF16_iiS0_S1_iiS0_S1_iiS0_PfiS0_S1_i
    .private_segment_fixed_size: 0
    .sgpr_count:     32
    .sgpr_spill_count: 0
    .symbol:         _Z5k_swzPKfPDF16_iiS0_S1_iiS0_S1_iiS0_PfiS0_S1_i.kd
    .uniform_work_group_size: 1
    .uses_dynamic_stack: false
    .vgpr_count:     14
    .vgpr_spill_count: 0
    .wavefront_size: 64
  - .agpr_count:     0
    .args:
      - .actual_access:  read_only
        .address_space:  global
        .offset:         0
        .size:           8
        .value_kind:     global_buffer
      - .actual_access:  read_only
        .address_space:  global
        .offset:         8
        .size:           8
        .value_kind:     global_buffer
      - .actual_access:  write_only
        .address_space:  global
        .offset:         16
        .size:           8
        .value_kind:     global_buffer
      - .actual_access:  read_only
        .address_space:  global
        .offset:         24
        .size:           8
        .value_kind:     global_buffer
      - .actual_access:  read_only
        .address_space:  global
        .offset:         32
        .size:           8
        .value_kind:     global_buffer
      - .actual_access:  read_only
        .address_space:  global
        .offset:         40
        .size:           8
        .value_kind:     global_buffer
      - .actual_access:  write_only
        .address_space:  global
        .offset:         48
        .size:           8
        .value_kind:     global_buffer
    .group_segment_fixed_size: 98816
    .kernarg_segment_align: 8
    .kernarg_segment_size: 56
    .language:       OpenCL C
    .language_version:
      - 2
      - 0
    .max_flat_workgroup_size: 512
    .name:           _Z10k_ka_firstPKfPKiPfS0_S0_PKDF16_PDF16_
    .private_segment_fixed_size: 0
    .sgpr_count:     59
    .sgpr_spill_count: 0
    .symbol:         _Z10k_ka_firstPKfPKiPfS0_S0_PKDF16_PDF16_.kd
    .uniform_work_group_size: 1
    .uses_dynamic_stack: false
    .vgpr_count:     174
    .vgpr_spill_count: 0
    .wavefront_size: 64
  - .agpr_count:     0
    .args:
      - .actual_access:  read_only
        .address_space:  global
        .offset:         0
        .size:           8
        .value_kind:     global_buffer
      - .actual_access:  read_only
        .address_space:  global
        .offset:         8
        .size:           8
        .value_kind:     global_buffer
      - .actual_access:  read_only
        .address_space:  global
        .offset:         16
        .size:           8
        .value_kind:     global_buffer
      - .actual_access:  read_only
        .address_space:  global
        .offset:         24
        .size:           8
        .value_kind:     global_buffer
      - .actual_access:  read_only
        .address_space:  global
        .offset:         32
        .size:           8
        .value_kind:     global_buffer
      - .actual_access:  read_only
        .address_space:  global
        .offset:         40
        .size:           8
        .value_kind:     global_buffer
      - .actual_access:  write_only
        .address_space:  global
        .offset:         48
        .size:           8
        .value_kind:     global_buffer
      - .actual_access:  write_only
        .address_space:  global
        .offset:         56
        .size:           8
        .value_kind:     global_buffer
      - .actual_access:  write_only
        .address_space:  global
        .offset:         64
        .size:           8
        .value_kind:     global_buffer
      - .actual_access:  read_only
        .address_space:  global
        .offset:         72
        .size:           8
        .value_kind:     global_buffer
      - .actual_access:  write_only
        .address_space:  global
        .offset:         80
        .size:           8
        .value_kind:     global_buffer
      - .actual_access:  write_only
        .address_space:  global
        .offset:         88
        .size:           8
        .value_kind:     global_buffer
    .group_segment_fixed_size: 47616
    .kernarg_segment_align: 8
    .kernarg_segment_size: 96
    .language:       OpenCL C
    .language_version:
      - 2
      - 0
    .max_flat_workgroup_size: 512
    .name:           _Z12k_conv_xprojPKDF16_PKfS2_S0_S0_S2_PDF16_S3_PfS2_S3_S4_
    .private_segment_fixed_size: 0
    .sgpr_count:     32
    .sgpr_spill_count: 0
    .symbol:         _Z12k_conv_xprojPKDF16_PKfS2_S0_S0_S2_PDF16_S3_PfS2_S3_S4_.kd
    .uniform_work_group_size: 1
    .uses_dynamic_stack: false
    .vgpr_count:     160
    .vgpr_spill_count: 0
    .wavefront_size: 64
  - .agpr_count:     0
    .args:
      - .actual_access:  read_only
        .address_space:  global
        .offset:         0
        .size:           8
        .value_kind:     global_buffer
      - .actual_access:  read_only
        .address_space:  global
        .offset:         8
        .size:           8
        .value_kind:     global_buffer
      - .actual_access:  read_only
        .address_space:  global
        .offset:         16
        .size:           8
        .value_kind:     global_buffer
      - .actual_access:  write_only
        .address_space:  global
        .offset:         24
        .size:           8
        .value_kind:     global_buffer
    .group_segment_fixed_size: 16384
    .kernarg_segment_align: 8
    .kernarg_segment_size: 32
    .language:       OpenCL C
    .language_version:
      - 2
      - 0
    .max_flat_workgroup_size: 512
    .name:           _Z11k_scan_combPKDF16_PKfS2_PDF16_
    .private_segment_fixed_size: 0
    .sgpr_count:     18
    .sgpr_spill_count: 0
    .symbol:         _Z11k_scan_combPKDF16_PKfS2_PDF16_.kd
    .uniform_work_group_size: 1
    .uses_dynamic_stack: false
    .vgpr_count:     120
    .vgpr_spill_count: 0
    .wavefront_size: 64
  - .agpr_count:     0
    .args:
      - .actual_access:  read_only
        .address_space:  global
        .offset:         0
        .size:           8
        .value_kind:     global_buffer
      - .actual_access:  read_only
        .address_space:  global
        .offset:         8
        .size:           8
        .value_kind:     global_buffer
      - .actual_access:  read_only
        .address_space:  global
        .offset:         16
        .size:           8
        .value_kind:     global_buffer
      - .actual_access:  read_only
        .address_space:  global
        .offset:         24
        .size:           8
        .value_kind:     global_buffer
      - .actual_access:  write_only
        .address_space:  global
        .offset:         32
        .size:           8
        .value_kind:     global_buffer
    .group_segment_fixed_size: 32
    .kernarg_segment_align: 8
    .kernarg_segment_size: 40
    .language:       OpenCL C
    .language_version:
      - 2
      - 0
    .max_flat_workgroup_size: 256
    .name:           _Z6k_headPKfS0_S0_S0_Pf
    .private_segment_fixed_size: 0
    .sgpr_count:     86
    .sgpr_spill_count: 0
    .symbol:         _Z6k_headPKfS0_S0_S0_Pf.kd
    .uniform_work_group_size: 1
    .uses_dynamic_stack: false
    .vgpr_count:     92
    .vgpr_spill_count: 0
    .wavefront_size: 64
  - .agpr_count:     0
    .args:
      - .actual_access:  read_only
        .address_space:  global
        .offset:         0
        .size:           8
        .value_kind:     global_buffer
      - .actual_access:  read_only
        .address_space:  global
        .offset:         8
        .size:           8
        .value_kind:     global_buffer
      - .actual_access:  read_only
        .address_space:  global
        .offset:         16
        .size:           8
        .value_kind:     global_buffer
      - .actual_access:  read_only
        .address_space:  global
        .offset:         24
        .size:           8
        .value_kind:     global_buffer
      - .actual_access:  read_only
        .address_space:  global
        .offset:         32
        .size:           8
        .value_kind:     global_buffer
      - .actual_access:  read_only
        .address_space:  global
        .offset:         40
        .size:           8
        .value_kind:     global_buffer
      - .actual_access:  read_only
        .address_space:  global
        .offset:         48
        .size:           8
        .value_kind:     global_buffer
      - .address_space:  global
        .offset:         56
        .size:           8
        .value_kind:     global_buffer
      - .actual_access:  read_only
        .address_space:  global
        .offset:         64
        .size:           8
        .value_kind:     global_buffer
      - .actual_access:  read_only
        .address_space:  global
        .offset:         72
        .size:           8
        .value_kind:     global_buffer
      - .actual_access:  read_only
        .address_space:  global
        .offset:         80
        .size:           8
        .value_kind:     global_buffer
      - .address_space:  global
        .offset:         88
        .size:           8
        .value_kind:     global_buffer
      - .actual_access:  read_only
        .address_space:  global
        .offset:         96
        .size:           8
        .value_kind:     global_buffer
      - .actual_access:  read_only
        .address_space:  global
        .offset:         104
        .size:           8
        .value_kind:     global_buffer
      - .actual_access:  read_only
        .address_space:  global
        .offset:         112
        .size:           8
        .value_kind:     global_buffer
    .group_segment_fixed_size: 98816
    .kernarg_segment_align: 8
    .kernarg_segment_size: 120
    .language:       OpenCL C
    .language_version:
      - 2
      - 0
    .max_flat_workgroup_size: 512
    .name:           _Z4k_k2ILb0EEvPKDF16_S1_PKfS3_S3_S1_S1_PfS3_S3_S1_PDF16_PKiS4_S4_
    .private_segment_fixed_size: 0
    .sgpr_count:     106
    .sgpr_spill_count: 0
    .symbol:         _Z4k_k2ILb0EEvPKDF16_S1_PKfS3_S3_S1_S1_PfS3_S3_S1_PDF16_PKiS4_S4_.kd
    .uniform_work_group_size: 1
    .uses_dynamic_stack: false
    .vgpr_count:     232
    .vgpr_spill_count: 0
    .wavefront_size: 64
  - .agpr_count:     0
    .args:
      - .actual_access:  read_only
        .address_space:  global
        .offset:         0
        .size:           8
        .value_kind:     global_buffer
      - .actual_access:  read_only
        .address_space:  global
        .offset:         8
        .size:           8
        .value_kind:     global_buffer
      - .actual_access:  read_only
        .address_space:  global
        .offset:         16
        .size:           8
        .value_kind:     global_buffer
      - .actual_access:  read_only
        .address_space:  global
        .offset:         24
        .size:           8
        .value_kind:     global_buffer
      - .actual_access:  read_only
        .address_space:  global
        .offset:         32
        .size:           8
        .value_kind:     global_buffer
      - .actual_access:  read_only
        .address_space:  global
        .offset:         40
        .size:           8
        .value_kind:     global_buffer
      - .actual_access:  read_only
        .address_space:  global
        .offset:         48
        .size:           8
        .value_kind:     global_buffer
      - .actual_access:  read_only
        .address_space:  global
        .offset:         56
        .size:           8
        .value_kind:     global_buffer
      - .actual_access:  read_only
        .address_space:  global
        .offset:         64
        .size:           8
        .value_kind:     global_buffer
      - .actual_access:  read_only
        .address_space:  global
        .offset:         72
        .size:           8
        .value_kind:     global_buffer
      - .actual_access:  read_only
        .address_space:  global
        .offset:         80
        .size:           8
        .value_kind:     global_buffer
      - .actual_access:  read_only
        .address_space:  global
        .offset:         88
        .size:           8
        .value_kind:     global_buffer
      - .actual_access:  read_only
        .address_space:  global
        .offset:         96
        .size:           8
        .value_kind:     global_buffer
      - .actual_access:  write_only
        .address_space:  global
        .offset:         104
        .size:           8
        .value_kind:     global_buffer
      - .actual_access:  write_only
        .address_space:  global
        .offset:         112
        .size:           8
        .value_kind:     global_buffer
    .group_segment_fixed_size: 98816
    .kernarg_segment_align: 8
    .kernarg_segment_size: 120
    .language:       OpenCL C
    .language_version:
      - 2
      - 0
    .max_flat_workgroup_size: 512
    .name:           _Z4k_k2ILb1EEvPKDF16_S1_PKfS3_S3_S1_S1_PfS3_S3_S1_PDF16_PKiS4_S4_
    .private_segment_fixed_size: 0
    .sgpr_count:     44
    .sgpr_spill_count: 0
    .symbol:         _Z4k_k2ILb1EEvPKDF16_S1_PKfS3_S3_S1_S1_PfS3_S3_S1_PDF16_PKiS4_S4_.kd
    .uniform_work_group_size: 1
    .uses_dynamic_stack: false
    .vgpr_count:     196
    .vgpr_spill_count: 0
    .wavefront_size: 64
